# instruction selection: bf16 pair packing in S1/S3 image writes as v_perm_b32 (276 sites), selectors in s100/s101
# baseline (speedup 1.0000x reference)
.LBB0_410:
	s_or_b64 exec, exec, s[0:1]
	s_mov_b32 s0, s86
	s_waitcnt lgkmcnt(0)
	s_waitcnt vmcnt(0)
	s_barrier
	s_mov_b32 s100, 0x05040100
	s_mov_b32 s101, 0x07060302
	v_readlane_b32 s4, v242, 55
	v_mbcnt_lo_u32_b32 v0, -1, 0
	v_mbcnt_hi_u32_b32 v0, -1, v0
	s_mov_b32 s65, s79
	v_lshl_add_u32 v122, s0, 6, v0
	s_mov_b32 s0, s79
	s_cmp_eq_u32 s4, 3
	s_cselect_b64 s[6:7], -1, 0
	s_add_i32 s0, s0, 0x25f98
	v_mov_b32_e32 v0, s0
	ds_read_b64 v[0:1], v0
	v_readfirstlane_b32 s70, v122
	s_ashr_i32 s93, s70, 6
	v_readlane_b32 s5, v242, 56
	v_and_b32_e32 v160, 63, v122
	s_waitcnt lgkmcnt(0)
	v_readfirstlane_b32 s0, v0
	v_readfirstlane_b32 s1, v1
	s_add_u32 s8, s0, 0x43800000
	s_addc_u32 s9, s1, 0
	s_add_u32 s2, s0, 0x65800000
	v_writelane_b32 v242, s2, 58
	s_addc_u32 s2, s1, 0
	v_writelane_b32 v242, s2, 60
	s_add_u32 s2, s0, 0x6da00000
	s_addc_u32 s3, s1, 0
	v_writelane_b32 v242, s2, 62
	s_nop 1
	v_writelane_b32 v242, s3, 63
	s_add_u32 s2, s0, 0x3f700000
	v_writelane_b32 v241, s2, 0
	s_addc_u32 s2, s1, 0
	v_writelane_b32 v241, s2, 2
	v_readlane_b32 s2, v243, 47
	v_readlane_b32 s3, v243, 48
	s_add_u32 s0, s0, s2
	s_addc_u32 s1, s1, s3
	s_add_u32 s30, s0, 0x6dc00000
	s_mov_b32 s0, s79
	s_addc_u32 s31, s1, 0
	s_add_i32 s0, s0, 0x25f60
	v_mov_b32_e32 v0, s0
	ds_read_b64 v[0:1], v0
	s_lshl_b32 s78, s4, 3
	s_lshl_b64 s[2:3], s[78:79], 2
	s_waitcnt lgkmcnt(0)
	v_readfirstlane_b32 s0, v0
	v_readfirstlane_b32 s1, v1
	s_add_u32 s0, s0, s2
	v_writelane_b32 v241, s2, 4
	s_addc_u32 s1, s1, s3
	s_lshl_b32 s78, s4, 7
	v_writelane_b32 v241, s3, 5
	v_writelane_b32 v241, s0, 6
	s_lshl_b64 s[2:3], s[78:79], 2
	s_mov_b64 s[4:5], -1
	v_writelane_b32 v241, s1, 7
	s_mov_b32 s0, s79
	s_add_i32 s0, s0, 0x25f58
	v_mov_b32_e32 v0, s0
	ds_read_b64 v[0:1], v0
	s_waitcnt lgkmcnt(0)
	v_readfirstlane_b32 s0, v0
	s_add_u32 s55, s0, s2
	v_writelane_b32 v241, s2, 8
	v_readfirstlane_b32 s1, v1
	s_addc_u32 s56, s1, s3
	v_writelane_b32 v241, s3, 9
	v_writelane_b32 v241, s6, 10
	v_readlane_b32 s0, v243, 49
	v_readlane_b32 s1, v243, 50
	v_writelane_b32 v241, s7, 11
	v_writelane_b32 v241, s88, 12
	s_or_b64 s[0:1], s[0:1], s[6:7]
	s_andn2_b64 vcc, exec, s[0:1]
	v_writelane_b32 v241, s89, 13
	v_writelane_b32 v241, s8, 14
	s_nop 1
	v_writelane_b32 v241, s9, 15
	v_writelane_b32 v241, s75, 16
	s_cbranch_vccz .LBB0_497
	v_readlane_b32 s0, v243, 53
	v_readlane_b32 s1, v243, 54
	s_and_b64 vcc, exec, s[0:1]
	v_lshlrev_b32_e32 v64, 1, v160
	s_cbranch_vccz .LBB0_435
	s_lshl_b32 s88, s93, 3
	v_readlane_b32 s0, v243, 55
	s_bfe_u32 s48, s70, 0x20006
	v_lshlrev_b32_e32 v66, 2, v160
	v_mov_b32_e32 v67, v65
	v_readlane_b32 s1, v243, 56
	v_writelane_b32 v241, s88, 25
	s_ashr_i32 s33, s70, 8
	v_lshl_add_u64 v[68:69], s[8:9], 0, v[66:67]
	s_lshl_b32 s64, s48, 4
	s_andn2_b64 vcc, exec, s[0:1]
	v_lshlrev_b32_e32 v56, 2, v64
	v_writelane_b32 v241, s55, 55
	v_writelane_b32 v241, s56, 59
	s_cbranch_vccnz .LBB0_437
	s_lshl_b32 s0, s93, 1
	s_and_b32 s0, s0, 0x3ffffc
	v_lshrrev_b32_e32 v0, 4, v160
	v_lshlrev_b32_e32 v148, 2, v160
	v_or_b32_e32 v0, s0, v0
	s_lshl_b32 s0, s93, 5
	v_lshlrev_b32_e32 v0, 10, v0
	v_and_b32_e32 v1, 60, v148
	s_and_b32 s1, s0, 32
	v_bitop3_b32 v0, v0, s1, v1 bitop3:0xf6
	s_lshl_b32 s1, s93, 9
	v_writelane_b32 v241, s1, 41
	s_and_b32 s1, s1, 0x200
	s_or_b32 s61, s88, 1
	v_or_b32_e32 v1, s1, v0
	s_lshl_b32 s1, s61, 6
	s_and_b32 s1, s1, 0x240
	s_or_b32 s57, s88, 2
	v_or_b32_e32 v2, s1, v0
	s_lshl_b32 s1, s57, 6
	s_and_b32 s1, s1, 0x280
	s_or_b32 s60, s88, 3
	v_or_b32_e32 v3, s1, v0
	s_lshl_b32 s1, s60, 6
	s_and_b32 s1, s1, 0x2c0
	v_or_b32_e32 v4, s1, v0
	s_or_b32 s1, s88, 4
	s_sub_i32 s2, 63, s1
	s_mov_b32 s96, s1
	s_lshl_b32 s1, s1, 6
	s_and_b32 s1, s1, 0x300
	v_or_b32_e32 v5, s1, v0
	s_or_b32 s1, s88, 5
	s_mov_b32 s62, s2
	v_cvt_f32_i32_e32 v153, s2
	s_sub_i32 s2, 63, s1
	s_mov_b32 s72, s1
	s_lshl_b32 s1, s1, 6
	s_and_b32 s1, s1, 0x340
	v_or_b32_e32 v6, s1, v0
	s_or_b32 s1, s88, 6
	v_writelane_b32 v241, s2, 45
	v_cvt_f32_i32_e32 v154, s2
	s_sub_i32 s2, 63, s1
	v_writelane_b32 v241, s2, 23
	v_writelane_b32 v241, s1, 19
	s_lshl_b32 s1, s1, 6
	s_and_b32 s1, s1, 0x380
	v_or_b32_e32 v7, s1, v0
	s_or_b32 s1, s88, 7
	v_cvt_f32_i32_e32 v155, s2
	s_sub_i32 s2, 63, s1
	v_writelane_b32 v241, s2, 27
	v_writelane_b32 v241, s1, 21
	s_lshl_b32 s1, s1, 6
	s_and_b32 s1, s1, 0x3c0
	s_sub_i32 s58, 63, s88
	s_sub_i32 s63, 63, s61
	s_sub_i32 s59, 63, s57
	s_sub_i32 s66, 63, s60
	v_or_b32_e32 v0, s1, v0
	s_lshl_b32 s4, s93, 4
	v_readlane_b32 s1, v242, 28
	v_ashrrev_i32_e32 v123, 31, v122
	s_add_u32 s6, s8, s1
	v_lshlrev_b64 v[124:125], 3, v[122:123]
	s_mov_b64 s[10:11], 0x1000
	s_addc_u32 s7, s9, 0
	s_and_b32 s5, s93, -4
	v_lshl_add_u64 v[126:127], v[124:125], 0, s[10:11]
	s_mov_b64 s[10:11], 0x2000
	s_add_i32 s1, s65, 0x12000
	s_lshl_b32 s8, s5, 12
	v_lshl_add_u64 v[128:129], v[124:125], 0, s[10:11]
	s_mov_b64 s[10:11], 0x3000
	v_lshrrev_b32_e32 v8, 2, v122
	s_lshl_b32 s3, s48, 11
	s_add_i32 s22, s1, s8
	s_lshl_b32 s8, s5, 11
	v_lshl_add_u64 v[130:131], v[124:125], 0, s[10:11]
	s_mov_b64 s[10:11], 0x4000
	v_cvt_f32_i32_e32 v156, s2
	v_and_b32_e32 v8, 14, v8
	s_lshl_b32 s2, s48, 12
	s_add_i32 s3, s65, s3
	s_add_i32 s23, s65, s8
	s_lshl_b32 s8, s93, 11
	s_lshl_b32 s26, s33, 6
	v_lshl_add_u64 v[132:133], v[124:125], 0, s[10:11]
	s_mov_b64 s[10:11], 0x5000
	v_lshlrev_b32_e32 v161, 3, v160
	v_add_lshl_u32 v158, v8, s33, 10
	v_lshlrev_b32_e32 v8, 7, v160
	s_lshl_b32 s16, s33, 1
	s_add_i32 s2, s65, s2
	s_add_i32 s3, s3, 0x10000
	s_add_i32 s24, s65, s8
	s_add_i32 s25, s65, 0x1b600
	s_xor_b32 s27, s26, 64
	s_lshl_b32 s20, s48, 1
	v_lshl_add_u64 v[134:135], v[124:125], 0, s[10:11]
	s_mov_b64 s[10:11], 0x6000
	v_and_b32_e32 v159, 0x380, v8
	v_and_b32_e32 v8, 32, v161
	s_cmp_lt_u32 s70, 64
	v_lshl_add_u64 v[136:137], v[124:125], 0, s[10:11]
	s_mov_b64 s[10:11], 0x7000
	v_bitop3_b32 v67, s4, v8, 48 bitop3:0x6c
	v_writelane_b32 v241, s8, 49
	s_cselect_b64 s[8:9], -1, 0
	v_lshl_add_u64 v[138:139], v[124:125], 0, s[10:11]
	s_lshl_b32 s10, s5, 4
	s_or_b32 s12, s4, 48
	s_lshl_b32 s28, s48, 8
	s_lshl_b32 s4, s33, 7
	s_ashr_i32 s11, s10, 31
	s_ashr_i32 s13, s12, 31
	s_add_i32 s28, s28, s4
	s_cmp_le_i32 s16, s48
	s_cselect_b64 s[14:15], -1, 0
	s_lshl_b32 s42, s33, 13
	s_lshl_b32 s43, s33, 5
	s_lshl_b32 s44, s33, 10
	s_or_b32 s4, s16, 1
	s_cmp_lt_i32 s16, s48
	s_cselect_b64 s[16:17], -1, 0
	s_lshl_b32 s45, s4, 12
	s_lshl_b32 s46, s4, 4
	s_lshl_b32 s47, s4, 5
	v_readlane_b32 s4, v242, 29
	v_readlane_b32 s5, v241, 0
	v_cvt_f32_i32_e32 v149, s58
	v_cvt_f32_i32_e32 v150, s63
	v_cvt_f32_i32_e32 v151, s59
	v_cvt_f32_i32_e32 v152, s66
	s_add_u32 s18, s5, s4
	v_readlane_b32 s4, v241, 2
	s_addc_u32 s19, s4, 0
	v_readlane_b32 s4, v242, 62
	v_add3_u32 v8, s65, v158, v159
	v_mov_b32_e32 v57, v65
	v_readlane_b32 s5, v242, 63
	s_mov_b32 s29, 1
	s_or_b32 s49, s20, 24
	v_lshl_add_u64 v[58:59], s[4:5], 0, v[56:57]
	v_add_u32_e32 v57, s65, v1
	v_add_u32_e32 v123, s65, v2
	v_add_u32_e32 v157, s65, v3
	v_add_u32_e32 v162, s65, v4
	v_add_u32_e32 v163, s65, v5
	v_add_u32_e32 v164, s65, v6
	v_add_u32_e32 v165, s65, v7
	v_add_u32_e32 v166, s65, v0
	v_add_u32_e32 v167, v8, v67
	s_branch .LBB0_415

.LBB0_417:
	s_waitcnt vmcnt(23)
	v_lshlrev_b32_e32 v8, 16, v168
	v_mov_b32_e32 v81, v160
	v_mul_f32_e32 v8, v178, v8
	v_and_b32_e32 v9, 0xffff0000, v168
	v_mul_f32_e32 v9, v178, v9
	v_cvt_pk_bf16_f32 v12, v8, v9
	s_waitcnt vmcnt(20)
	v_lshlrev_b32_e32 v8, 16, v171
	v_mul_f32_e32 v8, v179, v8
	v_and_b32_e32 v9, 0xffff0000, v171
	ds_write2st64_b32 v57, v170, v168 offset1:64
	v_mul_f32_e32 v9, v179, v9
	v_cvt_pk_bf16_f32 v13, v8, v9
	s_waitcnt vmcnt(17)
	v_lshlrev_b32_e32 v8, 16, v175
	v_mul_f32_e32 v8, v180, v8
	v_and_b32_e32 v9, 0xffff0000, v175
	ds_write2st64_b32 v123, v173, v171 offset1:64
	v_mul_f32_e32 v9, v180, v9
	v_cvt_pk_bf16_f32 v14, v8, v9
	s_waitcnt vmcnt(14)
	v_lshlrev_b32_e32 v8, 16, v183
	v_mul_f32_e32 v8, v181, v8
	v_and_b32_e32 v9, 0xffff0000, v183
	ds_write2st64_b32 v157, v177, v175 offset1:64
	v_mul_f32_e32 v9, v181, v9
	v_cvt_pk_bf16_f32 v15, v8, v9
	s_waitcnt vmcnt(11)
	v_lshlrev_b32_e32 v8, 16, v189
	v_mul_f32_e32 v8, v182, v8
	v_and_b32_e32 v9, 0xffff0000, v189
	ds_write2st64_b32 v162, v188, v183 offset1:64
	v_mul_f32_e32 v9, v182, v9
	v_cvt_pk_bf16_f32 v16, v8, v9
	s_waitcnt vmcnt(8)
	v_lshlrev_b32_e32 v8, 16, v192
	v_mul_f32_e32 v8, v184, v8
	v_and_b32_e32 v9, 0xffff0000, v192
	ds_write2st64_b32 v163, v191, v189 offset1:64
	v_mul_f32_e32 v9, v184, v9
	v_cvt_pk_bf16_f32 v17, v8, v9
	s_waitcnt vmcnt(5)
	v_lshlrev_b32_e32 v8, 16, v195
	v_mul_f32_e32 v8, v185, v8
	v_and_b32_e32 v9, 0xffff0000, v195
	ds_write2st64_b32 v164, v194, v192 offset1:64
	v_mul_f32_e32 v9, v185, v9
	v_cvt_pk_bf16_f32 v18, v8, v9
	s_waitcnt vmcnt(2)
	v_lshlrev_b32_e32 v8, 16, v213
	v_mul_f32_e32 v8, v187, v8
	v_and_b32_e32 v9, 0xffff0000, v213
	ds_write2st64_b32 v165, v212, v195 offset1:64
	v_mul_f32_e32 v9, v187, v9
	v_cvt_pk_bf16_f32 v19, v8, v9
	v_and_b32_e32 v8, 0xffff, v12
	v_lshl_or_b32 v8, v13, 16, v8
	v_perm_b32 v12, v13, v12, s101
	v_perm_b32 v9, v15, v14, s100
	v_perm_b32 v13, v15, v14, s101
	v_perm_b32 v10, v17, v16, s100
	v_perm_b32 v11, v19, v18, s100
	v_perm_b32 v14, v17, v16, s101
	v_perm_b32 v15, v19, v18, s101
	s_add_i32 s40, s66, -1
	s_waitcnt vmcnt(0)
	ds_write2st64_b32 v166, v215, v213 offset1:64
	ds_write_b128 v167, v[8:11] offset:32768
	ds_write_b128 v167, v[12:15] offset:32832
	v_perm_b32 v8, v172, v169, s100
	v_perm_b32 v9, v186, v176, s100
	v_perm_b32 v10, v193, v190, s100
	v_perm_b32 v11, v214, v211, s100
	v_perm_b32 v12, v172, v169, s101
	v_perm_b32 v13, v186, v176, s101
	v_perm_b32 v14, v193, v190, s101
	v_perm_b32 v15, v214, v211, s101
	s_cmp_gt_u32 s40, 2
	ds_write_b128 v167, v[8:11] offset:49152
	ds_write_b128 v167, v[12:15] offset:49216
	s_cbranch_scc1 .LBB0_419
	s_and_b64 s[68:69], s[4:5], exec
	s_cselect_b32 s21, s66, s59
	s_lshl_b32 s21, s21, 6
	v_readlane_b32 s35, v242, 24
	s_add_i32 s41, s21, s35
	s_add_i32 s21, s41, s50
	v_mad_i64_i32 v[8:9], s[68:69], s21, v205, v[68:69]
	v_lshl_add_u64 v[10:11], v[8:9], 0, s[78:79]
	s_mov_b32 s21, s79
	s_mov_b32 s35, s79
	global_load_dword v168, v[10:11], off
	v_lshl_add_u64 v[10:11], v[8:9], 0, s[20:21]
	v_lshl_add_u64 v[8:9], v[8:9], 0, s[34:35]
	s_add_i32 s67, s41, s51
	global_load_dword v169, v[10:11], off
	global_load_dword v170, v[8:9], off
	v_mad_i64_i32 v[8:9], s[68:69], s67, v205, v[68:69]
	v_lshl_add_u64 v[10:11], v[8:9], 0, s[78:79]
	global_load_dword v171, v[10:11], off
	v_lshl_add_u64 v[10:11], v[8:9], 0, s[20:21]
	v_lshl_add_u64 v[8:9], v[8:9], 0, s[34:35]
	s_add_i32 s67, s41, s52
	global_load_dword v172, v[10:11], off
	global_load_dword v173, v[8:9], off
	v_mad_i64_i32 v[8:9], s[68:69], s67, v205, v[68:69]
	v_lshl_add_u64 v[10:11], v[8:9], 0, s[78:79]
	global_load_dword v175, v[10:11], off
	v_lshl_add_u64 v[10:11], v[8:9], 0, s[20:21]
	v_lshl_add_u64 v[8:9], v[8:9], 0, s[34:35]
	s_add_i32 s67, s41, s53
	global_load_dword v176, v[10:11], off
	global_load_dword v177, v[8:9], off
	v_mad_i64_i32 v[8:9], s[68:69], s67, v205, v[68:69]
	v_lshl_add_u64 v[10:11], v[8:9], 0, s[78:79]
	global_load_dword v183, v[10:11], off
	v_lshl_add_u64 v[10:11], v[8:9], 0, s[20:21]
	v_lshl_add_u64 v[8:9], v[8:9], 0, s[34:35]
	s_add_i32 s67, s41, s54
	global_load_dword v186, v[10:11], off
	global_load_dword v188, v[8:9], off
	v_mad_i64_i32 v[8:9], s[68:69], s67, v205, v[68:69]
	v_lshl_add_u64 v[10:11], v[8:9], 0, s[78:79]
	global_load_dword v189, v[10:11], off
	v_lshl_add_u64 v[10:11], v[8:9], 0, s[20:21]
	v_lshl_add_u64 v[8:9], v[8:9], 0, s[34:35]
	s_add_i32 s67, s41, s55
	global_load_dword v190, v[10:11], off
	global_load_dword v191, v[8:9], off
	v_mad_i64_i32 v[8:9], s[68:69], s67, v205, v[68:69]
	v_lshl_add_u64 v[10:11], v[8:9], 0, s[78:79]
	global_load_dword v192, v[10:11], off
	v_lshl_add_u64 v[10:11], v[8:9], 0, s[20:21]
	v_lshl_add_u64 v[8:9], v[8:9], 0, s[34:35]
	s_add_i32 s67, s41, s57
	global_load_dword v193, v[10:11], off
	global_load_dword v194, v[8:9], off
	v_mad_i64_i32 v[8:9], s[68:69], s67, v205, v[68:69]
	v_lshl_add_u64 v[10:11], v[8:9], 0, s[78:79]
	global_load_dword v195, v[10:11], off
	v_lshl_add_u64 v[10:11], v[8:9], 0, s[20:21]
	v_lshl_add_u64 v[8:9], v[8:9], 0, s[34:35]
	s_add_i32 s41, s41, s58
	global_load_dword v211, v[10:11], off
	global_load_dword v212, v[8:9], off
	v_mad_i64_i32 v[8:9], s[68:69], s41, v205, v[68:69]
	v_lshl_add_u64 v[10:11], v[8:9], 0, s[78:79]
	global_load_dword v213, v[10:11], off
	v_lshl_add_u64 v[10:11], v[8:9], 0, s[20:21]
	v_lshl_add_u64 v[8:9], v[8:9], 0, s[34:35]
	global_load_dword v214, v[10:11], off
	global_load_dword v215, v[8:9], off

.LBB0_443:
	s_waitcnt vmcnt(23)
	v_lshlrev_b32_e32 v32, 16, v162
	v_and_b32_e32 v33, 0xffff0000, v162
	v_pk_add_f32 v[34:35], v[32:33], 0 op_sel_hi:[1,0]
	s_waitcnt vmcnt(20)
	v_lshlrev_b32_e32 v36, 16, v165
	v_and_b32_e32 v37, 0xffff0000, v165
	v_pk_add_f32 v[38:39], v[34:35], v[36:37]
	s_waitcnt vmcnt(17)
	v_lshlrev_b32_e32 v40, 16, v168
	v_and_b32_e32 v41, 0xffff0000, v168
	v_pk_add_f32 v[42:43], v[38:39], v[40:41]
	s_waitcnt vmcnt(14)
	v_lshlrev_b32_e32 v44, 16, v171
	v_and_b32_e32 v45, 0xffff0000, v171
	v_pk_add_f32 v[46:47], v[42:43], v[44:45]
	s_waitcnt vmcnt(11)
	v_lshlrev_b32_e32 v48, 16, v174
	v_and_b32_e32 v49, 0xffff0000, v174
	v_pk_add_f32 v[50:51], v[46:47], v[48:49]
	s_waitcnt vmcnt(8)
	v_lshlrev_b32_e32 v26, 16, v177
	v_and_b32_e32 v27, 0xffff0000, v177
	v_pk_add_f32 v[28:29], v[50:51], v[26:27]
	s_waitcnt vmcnt(5)
	v_lshlrev_b32_e32 v22, 16, v180
	v_and_b32_e32 v23, 0xffff0000, v180
	v_pk_add_f32 v[24:25], v[28:29], v[22:23]
	s_waitcnt vmcnt(2)
	v_lshlrev_b32_e32 v18, 16, v183
	v_and_b32_e32 v19, 0xffff0000, v183
	v_mov_b32_e32 v186, v160
	v_pk_add_f32 v[20:21], v[24:25], v[18:19]
	v_add_u32_e32 v8, s1, v161
	ds_write_b64 v8, v[20:21]
	s_waitcnt lgkmcnt(0)
	s_barrier
	v_add_u32_e32 v52, s0, v161
	ds_read2st64_b64 v[8:11], v52 offset1:1
	ds_read2st64_b64 v[12:15], v52 offset0:2 offset1:3
	v_pk_mul_f32 v[32:33], v[32:33], s[94:95] op_sel_hi:[1,0]
	v_pk_mul_f32 v[26:27], v[26:27], s[94:95] op_sel_hi:[1,0]
	v_exp_f32_e32 v32, v32
	s_waitcnt lgkmcnt(1)
	v_pk_add_f32 v[8:9], v[8:9], 0 op_sel_hi:[1,0]
	v_exp_f32_e32 v33, v33
	v_cndmask_b32_e64 v17, 0, v9, s[4:5]
	v_cndmask_b32_e64 v16, 0, v8, s[4:5]
	v_pk_add_f32 v[30:31], v[10:11], v[16:17]
	v_pk_add_f32 v[8:9], v[8:9], v[10:11]
	v_cndmask_b32_e64 v17, v17, v31, s[6:7]
	v_cndmask_b32_e64 v16, v16, v30, s[6:7]
	s_waitcnt lgkmcnt(0)
	v_pk_add_f32 v[10:11], v[12:13], v[16:17]
	v_pk_add_f32 v[12:13], v[8:9], v[12:13]
	v_cndmask_b32_e64 v17, v17, v11, s[8:9]
	v_cndmask_b32_e64 v16, v16, v10, s[8:9]
	ds_read2st64_b64 v[8:11], v52 offset0:4 offset1:5
	v_pk_add_f32 v[30:31], v[14:15], v[16:17]
	v_pk_add_f32 v[32:33], v[32:33], 1.0 op_sel_hi:[1,0] neg_lo:[1,0] neg_hi:[1,0]
	v_cndmask_b32_e64 v31, v17, v31, s[10:11]
	v_cndmask_b32_e64 v30, v16, v30, s[10:11]
	v_pk_add_f32 v[16:17], v[12:13], v[14:15]
	ds_read2st64_b64 v[12:15], v52 offset0:6 offset1:7
	s_waitcnt lgkmcnt(1)
	v_pk_add_f32 v[52:53], v[8:9], v[30:31]
	v_exp_f32_e32 v26, v26
	v_cndmask_b32_e64 v31, v31, v53, s[12:13]
	v_cndmask_b32_e64 v30, v30, v52, s[12:13]
	v_pk_add_f32 v[52:53], v[10:11], v[30:31]
	v_exp_f32_e32 v27, v27
	v_cndmask_b32_e64 v31, v31, v53, s[14:15]
	v_cndmask_b32_e64 v30, v30, v52, s[14:15]
	s_waitcnt lgkmcnt(0)
	v_pk_add_f32 v[52:53], v[12:13], v[30:31]
	v_pk_add_f32 v[26:27], v[26:27], 1.0 op_sel_hi:[1,0] neg_lo:[1,0] neg_hi:[1,0]
	v_cndmask_b32_e64 v31, v31, v53, s[16:17]
	v_cndmask_b32_e64 v30, v30, v52, s[16:17]
	v_pk_add_f32 v[52:53], v[14:15], v[30:31]
	v_pk_mul_f32 v[22:23], v[22:23], s[94:95] op_sel_hi:[1,0]
	v_cndmask_b32_e64 v31, v31, v53, s[18:19]
	v_cndmask_b32_e64 v30, v30, v52, s[18:19]
	v_pk_add_f32 v[30:31], v[30:31], v[16:17] neg_lo:[0,1] neg_hi:[0,1]
	v_exp_f32_e32 v22, v22
	v_pk_mul_f32 v[30:31], v[30:31], s[94:95] op_sel_hi:[1,0]
	v_exp_f32_e32 v23, v23
	v_pk_fma_f32 v[34:35], v[34:35], s[94:95], v[30:31] op_sel_hi:[1,0,1]
	v_pk_fma_f32 v[28:29], v[28:29], s[94:95], v[30:31] op_sel_hi:[1,0,1]
	v_med3_f32 v52, v35, s81, v206
	v_med3_f32 v53, v34, s81, v206
	v_exp_f32_e64 v34, -v53
	v_exp_f32_e64 v35, -v52
	v_pk_fma_f32 v[24:25], v[24:25], s[94:95], v[30:31] op_sel_hi:[1,0,1]
	v_pk_add_f32 v[22:23], v[22:23], 1.0 op_sel_hi:[1,0] neg_lo:[1,0] neg_hi:[1,0]
	v_pk_fma_f32 v[20:21], v[20:21], s[94:95], v[30:31] op_sel_hi:[1,0,1]
	v_pk_mul_f32 v[32:33], v[32:33], v[34:35]
	v_exp_f32_e32 v34, v53
	v_exp_f32_e32 v35, v52
	v_cvt_pk_bf16_f32 v52, v32, v33
	v_lshlrev_b32_e32 v32, 16, v164
	v_and_b32_e32 v33, 0xffff0000, v164
	v_pk_mul_f32 v[32:33], v[34:35], v[32:33]
	v_pk_fma_f32 v[34:35], v[38:39], s[94:95], v[30:31] op_sel_hi:[1,0,1]
	v_cvt_pk_bf16_f32 v32, v32, v33
	ds_write2st64_b32 v123, v32, v52 offset1:64
	v_med3_f32 v38, v35, s81, v206
	v_med3_f32 v39, v34, s81, v206
	v_pk_mul_f32 v[34:35], v[36:37], s[94:95] op_sel_hi:[1,0]
	v_exp_f32_e64 v36, -v39
	v_exp_f32_e32 v34, v34
	v_exp_f32_e32 v35, v35
	v_exp_f32_e64 v37, -v38
	v_pk_mul_f32 v[18:19], v[18:19], s[94:95] op_sel_hi:[1,0]
	v_pk_add_f32 v[8:9], v[16:17], v[8:9]
	v_pk_add_f32 v[32:33], v[34:35], 1.0 op_sel_hi:[1,0] neg_lo:[1,0] neg_hi:[1,0]
	v_exp_f32_e32 v34, v39
	v_exp_f32_e32 v35, v38
	v_pk_mul_f32 v[32:33], v[32:33], v[36:37]
	v_exp_f32_e32 v18, v18
	v_cvt_pk_bf16_f32 v36, v32, v33
	v_lshlrev_b32_e32 v32, 16, v167
	v_and_b32_e32 v33, 0xffff0000, v167
	v_pk_mul_f32 v[32:33], v[34:35], v[32:33]
	v_exp_f32_e32 v19, v19
	v_cvt_pk_bf16_f32 v37, v32, v33
	v_pk_fma_f32 v[32:33], v[42:43], s[94:95], v[30:31] op_sel_hi:[1,0,1]
	v_add_u32_e32 v42, 0x80, v123
	v_med3_f32 v38, v33, s81, v206
	v_med3_f32 v39, v32, s81, v206
	v_pk_mul_f32 v[32:33], v[40:41], s[94:95] op_sel_hi:[1,0]
	v_exp_f32_e64 v34, -v39
	v_exp_f32_e32 v32, v32
	v_exp_f32_e32 v33, v33
	v_exp_f32_e64 v35, -v38
	v_add_u32_e32 v40, 64, v123
	ds_write2st64_b32 v40, v37, v36 offset1:64
	v_pk_add_f32 v[32:33], v[32:33], 1.0 op_sel_hi:[1,0] neg_lo:[1,0] neg_hi:[1,0]
	v_pk_add_f32 v[18:19], v[18:19], 1.0 op_sel_hi:[1,0] neg_lo:[1,0] neg_hi:[1,0]
	v_pk_mul_f32 v[32:33], v[32:33], v[34:35]
	v_exp_f32_e32 v34, v39
	v_exp_f32_e32 v35, v38
	v_cvt_pk_bf16_f32 v37, v32, v33
	v_lshlrev_b32_e32 v32, 16, v169
	v_and_b32_e32 v33, 0xffff0000, v169
	v_pk_mul_f32 v[32:33], v[34:35], v[32:33]
	v_pk_add_f32 v[8:9], v[8:9], v[10:11]
	v_cvt_pk_bf16_f32 v38, v32, v33
	v_pk_fma_f32 v[32:33], v[46:47], s[94:95], v[30:31] op_sel_hi:[1,0,1]
	ds_write2st64_b32 v42, v38, v37 offset1:64
	v_med3_f32 v39, v33, s81, v206
	v_med3_f32 v41, v32, s81, v206
	v_pk_mul_f32 v[32:33], v[44:45], s[94:95] op_sel_hi:[1,0]
	v_exp_f32_e64 v34, -v41
	v_exp_f32_e32 v32, v32
	v_exp_f32_e32 v33, v33
	v_exp_f32_e64 v35, -v39
	v_add_u32_e32 v44, 0xc0, v123
	v_pk_add_f32 v[8:9], v[8:9], v[12:13]
	v_pk_add_f32 v[32:33], v[32:33], 1.0 op_sel_hi:[1,0] neg_lo:[1,0] neg_hi:[1,0]
	v_pk_add_f32 v[114:115], v[8:9], v[14:15]
	v_pk_mul_f32 v[32:33], v[32:33], v[34:35]
	v_exp_f32_e32 v34, v41
	v_exp_f32_e32 v35, v39
	v_cvt_pk_bf16_f32 v38, v32, v33
	v_lshlrev_b32_e32 v32, 16, v173
	v_and_b32_e32 v33, 0xffff0000, v173
	v_pk_mul_f32 v[32:33], v[34:35], v[32:33]
	v_cvt_pk_bf16_f32 v39, v32, v33
	v_pk_fma_f32 v[32:33], v[50:51], s[94:95], v[30:31] op_sel_hi:[1,0,1]
	ds_write2st64_b32 v44, v39, v38 offset1:64
	v_med3_f32 v41, v33, s81, v206
	v_med3_f32 v43, v32, s81, v206
	v_pk_mul_f32 v[32:33], v[48:49], s[94:95] op_sel_hi:[1,0]
	v_exp_f32_e64 v34, -v43
	v_exp_f32_e32 v32, v32
	v_exp_f32_e32 v33, v33
	v_exp_f32_e64 v35, -v41
	v_perm_b32 v8, v36, v52, s100
	v_pk_add_f32 v[32:33], v[32:33], 1.0 op_sel_hi:[1,0] neg_lo:[1,0] neg_hi:[1,0]
	v_perm_b32 v9, v38, v37, s100
	v_pk_mul_f32 v[32:33], v[32:33], v[34:35]
	v_exp_f32_e32 v34, v43
	v_exp_f32_e32 v35, v41
	v_cvt_pk_bf16_f32 v39, v32, v33
	v_lshlrev_b32_e32 v32, 16, v176
	v_and_b32_e32 v33, 0xffff0000, v176
	v_pk_mul_f32 v[32:33], v[34:35], v[32:33]
	v_med3_f32 v34, v29, s81, v206
	v_med3_f32 v35, v28, s81, v206
	v_exp_f32_e64 v28, -v35
	v_exp_f32_e64 v29, -v34
	v_cvt_pk_bf16_f32 v32, v32, v33
	ds_write2st64_b32 v123, v32, v39 offset0:1 offset1:65
	v_pk_mul_f32 v[26:27], v[26:27], v[28:29]
	v_exp_f32_e32 v28, v35
	v_exp_f32_e32 v29, v34
	v_cvt_pk_bf16_f32 v32, v26, v27
	s_waitcnt vmcnt(0)
	v_lshlrev_b32_e32 v26, 16, v179
	v_and_b32_e32 v27, 0xffff0000, v179
	v_pk_mul_f32 v[26:27], v[28:29], v[26:27]
	v_med3_f32 v28, v25, s81, v206
	v_med3_f32 v29, v24, s81, v206
	v_exp_f32_e64 v24, -v29
	v_exp_f32_e64 v25, -v28
	v_cvt_pk_bf16_f32 v26, v26, v27
	ds_write2st64_b32 v40, v26, v32 offset0:1 offset1:65
	v_perm_b32 v10, v32, v39, s100
	v_pk_mul_f32 v[22:23], v[22:23], v[24:25]
	v_exp_f32_e32 v24, v29
	v_exp_f32_e32 v25, v28
	v_cvt_pk_bf16_f32 v26, v22, v23
	v_lshlrev_b32_e32 v22, 16, v182
	v_and_b32_e32 v23, 0xffff0000, v182
	v_pk_mul_f32 v[22:23], v[24:25], v[22:23]
	v_med3_f32 v24, v21, s81, v206
	v_med3_f32 v25, v20, s81, v206
	v_exp_f32_e64 v20, -v25
	v_exp_f32_e64 v21, -v24
	v_cvt_pk_bf16_f32 v22, v22, v23
	ds_write2st64_b32 v42, v22, v26 offset0:1 offset1:65
	v_pk_mul_f32 v[18:19], v[18:19], v[20:21]
	v_exp_f32_e32 v20, v25
	v_exp_f32_e32 v21, v24
	v_cvt_pk_bf16_f32 v22, v18, v19
	v_lshlrev_b32_e32 v18, 16, v185
	v_and_b32_e32 v19, 0xffff0000, v185
	v_pk_mul_f32 v[18:19], v[20:21], v[18:19]
	v_perm_b32 v11, v22, v26, s100
	v_cvt_pk_bf16_f32 v18, v18, v19
	ds_write2st64_b32 v44, v18, v22 offset0:1 offset1:65
	v_perm_b32 v12, v36, v52, s101
	v_perm_b32 v13, v38, v37, s101
	v_perm_b32 v14, v32, v39, s101
	v_perm_b32 v15, v22, v26, s101
	ds_write_b128 v143, v[8:11] offset:32768
	ds_write_b128 v143, v[12:15] offset:32832
	v_perm_b32 v8, v166, v163, s100
	v_perm_b32 v9, v172, v170, s100
	v_perm_b32 v10, v178, v175, s100
	v_perm_b32 v11, v184, v181, s100
	s_andn2_b64 vcc, exec, s[36:37]
	s_mov_b64 s[60:61], -1
	v_perm_b32 v12, v166, v163, s101
	v_perm_b32 v13, v172, v170, s101
	v_perm_b32 v14, v178, v175, s101
	v_perm_b32 v15, v184, v181, s101
	ds_write_b128 v143, v[8:11] offset:49152
	ds_write_b128 v143, v[12:15] offset:49216
	s_cbranch_vccnz .LBB0_461
	s_cbranch_execz .LBB0_462

.LBB0_471:
	s_mul_hi_i32 s21, s20, 0x82082083
	s_add_i32 s21, s21, s20
	s_lshr_b32 s27, s21, 31
	s_ashr_i32 s44, s21, 5
	s_add_i32 s44, s44, s27
	s_mul_i32 s21, s44, 63
	s_sub_i32 s20, s20, s21
	s_add_i32 s27, s20, 1
	s_and_b32 s29, s44, 1
	s_sub_i32 s28, 64, s20
	s_cmp_eq_u32 s29, 0
	s_cselect_b64 s[38:39], -1, 0
	s_and_b64 s[20:21], s[38:39], exec
	s_cselect_b32 s27, s27, s28
	s_bitcmp0_b32 s44, 3
	v_add_u32_e32 v172, s1, v169
	s_mul_i32 s28, s44, 0x41
	s_cbranch_scc1 .LBB0_474
	s_bfe_u32 s20, s44, 0x20001
	s_lshl_b32 s21, s29, 4
	s_lshl_b32 s40, s20, 2
	s_or_b32 s21, s21, s40
	v_readlane_b32 s40, v241, 6
	v_mov_b32_e32 v0, s21
	v_readlane_b32 s41, v241, 7
	s_mov_b32 s21, 0xc2ce8ed0
	s_lshl_b32 s42, s20, 8
	v_readlane_b32 s51, v241, 27
	s_nop 1
	global_load_dword v0, v0, s[40:41]
	s_lshl_b32 s40, s27, 8
	s_waitcnt vmcnt(0)
	v_mul_f32_e32 v1, 0x3fb8aa3b, v0
	v_fma_f32 v2, v0, s94, -v1
	v_rndne_f32_e32 v3, v1
	v_fmac_f32_e32 v2, 0x32a5705f, v0
	v_sub_f32_e32 v1, v1, v3
	v_add_f32_e32 v1, v1, v2
	v_exp_f32_e32 v1, v1
	v_cvt_i32_f32_e32 v2, v3
	v_cmp_ngt_f32_e32 vcc, s21, v0
	s_mov_b32 s21, 0x42b17218
	v_ldexp_f32 v1, v1, v2
	v_cndmask_b32_e32 v1, 0, v1, vcc
	v_cmp_nlt_f32_e32 vcc, s21, v0
	s_lshr_b32 s21, s44, 4
	s_mulk_i32 s21, 0x4100
	s_add_i32 s40, s40, s21
	s_and_b64 s[20:21], s[38:39], exec
	s_cselect_b32 s20, 0, 0xc0
	s_or_b32 s50, s40, s20
	v_cndmask_b32_e32 v9, v204, v1, vcc
	s_and_b64 s[20:21], s[38:39], exec
	v_mul_f32_e32 v0, 0xc2800000, v9
	s_cselect_b32 s41, s88, s58
	v_mul_f32_e32 v0, 0x3fb8aa3b, v0
	s_add_i32 s20, s50, s41
	v_exp_f32_e32 v8, v0
	v_mad_i64_i32 v[0:1], s[20:21], s20, v205, v[140:141]
	s_or_b32 s78, s42, 0x1800
	v_lshl_add_u64 v[2:3], v[0:1], 0, s[78:79]
	global_load_dword v25, v[2:3], off
	s_or_b32 s20, s42, 0x1c00
	s_and_b64 s[42:43], s[38:39], exec
	s_mov_b32 s21, s79
	s_cselect_b32 s42, s61, s63
	v_lshl_add_u64 v[0:1], v[0:1], 0, s[20:21]
	s_add_i32 s43, s50, s42
	global_load_dword v0, v[0:1], off
	v_mad_i64_i32 v[2:3], s[46:47], s43, v205, v[140:141]
	v_lshl_add_u64 v[4:5], v[2:3], 0, s[78:79]
	global_load_dword v29, v[4:5], off
	s_and_b64 s[46:47], s[38:39], exec
	s_cselect_b32 s43, s57, s59
	v_lshl_add_u64 v[2:3], v[2:3], 0, s[20:21]
	s_add_i32 s45, s50, s43
	global_load_dword v1, v[2:3], off
	v_mad_i64_i32 v[2:3], s[46:47], s45, v205, v[140:141]
	v_lshl_add_u64 v[4:5], v[2:3], 0, s[78:79]
	global_load_dword v31, v[4:5], off
	s_and_b64 s[46:47], s[38:39], exec
	s_cselect_b32 s45, s60, s66
	v_lshl_add_u64 v[2:3], v[2:3], 0, s[20:21]
	s_add_i32 s46, s50, s45
	global_load_dword v2, v[2:3], off
	v_mad_i64_i32 v[4:5], s[46:47], s46, v205, v[140:141]
	v_lshl_add_u64 v[6:7], v[4:5], 0, s[78:79]
	global_load_dword v32, v[6:7], off
	s_and_b64 s[46:47], s[38:39], exec
	s_cselect_b32 s46, s85, s89
	v_lshl_add_u64 v[4:5], v[4:5], 0, s[20:21]
	s_add_i32 s47, s50, s46
	global_load_dword v3, v[4:5], off
	v_mad_i64_i32 v[4:5], s[48:49], s47, v205, v[140:141]
	v_lshl_add_u64 v[6:7], v[4:5], 0, s[78:79]
	s_and_b64 s[48:49], s[38:39], exec
	v_readlane_b32 s47, v241, 45
	global_load_dword v33, v[6:7], off
	s_cselect_b32 s47, s97, s47
	v_lshl_add_u64 v[4:5], v[4:5], 0, s[20:21]
	s_add_i32 s48, s50, s47
	global_load_dword v27, v[4:5], off
	v_mad_i64_i32 v[4:5], s[48:49], s48, v205, v[140:141]
	s_and_b64 s[48:49], s[38:39], exec
	v_readlane_b32 s48, v241, 19
	v_readlane_b32 s49, v241, 23
	s_cselect_b32 s48, s48, s49
	v_lshl_add_u64 v[6:7], v[4:5], 0, s[78:79]
	v_lshl_add_u64 v[4:5], v[4:5], 0, s[20:21]
	s_add_i32 s49, s50, s48
	global_load_dword v34, v[6:7], off
	global_load_dword v28, v[4:5], off
	v_mad_i64_i32 v[4:5], s[52:53], s49, v205, v[140:141]
	s_and_b64 s[52:53], s[38:39], exec
	v_readlane_b32 s49, v241, 21
	s_cselect_b32 s49, s49, s51
	v_lshl_add_u64 v[6:7], v[4:5], 0, s[78:79]
	v_lshl_add_u64 v[4:5], v[4:5], 0, s[20:21]
	s_add_i32 s50, s50, s49
	global_load_dword v35, v[6:7], off
	global_load_dword v30, v[4:5], off
	v_mad_i64_i32 v[4:5], s[50:51], s50, v205, v[140:141]
	s_lshl_b32 s52, s29, 6
	s_or_b32 s50, s52, s40
	s_add_i32 s53, s50, 64
	v_lshl_add_u64 v[6:7], v[4:5], 0, s[78:79]
	v_lshl_add_u64 v[4:5], v[4:5], 0, s[20:21]
	s_add_i32 s50, s53, s41
	global_load_dword v37, v[6:7], off
	global_load_dword v36, v[4:5], off
	v_mad_i64_i32 v[4:5], s[50:51], s50, v205, v[140:141]
	v_lshl_add_u64 v[6:7], v[4:5], 0, s[78:79]
	v_lshl_add_u64 v[4:5], v[4:5], 0, s[20:21]
	s_add_i32 s50, s53, s42
	global_load_dword v15, v[6:7], off
	global_load_dword v10, v[4:5], off
	v_mad_i64_i32 v[4:5], s[50:51], s50, v205, v[140:141]
	v_lshl_add_u64 v[6:7], v[4:5], 0, s[78:79]
	v_lshl_add_u64 v[4:5], v[4:5], 0, s[20:21]
	s_add_i32 s50, s53, s43
	global_load_dword v17, v[6:7], off
	global_load_dword v11, v[4:5], off
	v_mad_i64_i32 v[4:5], s[50:51], s50, v205, v[140:141]
	v_lshl_add_u64 v[6:7], v[4:5], 0, s[78:79]
	v_lshl_add_u64 v[4:5], v[4:5], 0, s[20:21]
	s_add_i32 s50, s53, s45
	global_load_dword v19, v[6:7], off
	global_load_dword v12, v[4:5], off
	v_mad_i64_i32 v[4:5], s[50:51], s50, v205, v[140:141]
	v_lshl_add_u64 v[6:7], v[4:5], 0, s[78:79]
	v_lshl_add_u64 v[4:5], v[4:5], 0, s[20:21]
	s_add_i32 s50, s53, s46
	global_load_dword v20, v[6:7], off
	global_load_dword v13, v[4:5], off
	v_mad_i64_i32 v[4:5], s[50:51], s50, v205, v[140:141]
	v_lshl_add_u64 v[6:7], v[4:5], 0, s[78:79]
	v_lshl_add_u64 v[4:5], v[4:5], 0, s[20:21]
	s_add_i32 s50, s53, s47
	global_load_dword v22, v[6:7], off
	global_load_dword v14, v[4:5], off
	v_mad_i64_i32 v[4:5], s[50:51], s50, v205, v[140:141]
	v_lshl_add_u64 v[6:7], v[4:5], 0, s[78:79]
	v_lshl_add_u64 v[4:5], v[4:5], 0, s[20:21]
	s_add_i32 s50, s53, s48
	global_load_dword v23, v[6:7], off
	global_load_dword v16, v[4:5], off
	v_mad_i64_i32 v[4:5], s[50:51], s50, v205, v[140:141]
	v_lshl_add_u64 v[6:7], v[4:5], 0, s[78:79]
	v_lshl_add_u64 v[4:5], v[4:5], 0, s[20:21]
	s_add_i32 s53, s53, s49
	global_load_dword v24, v[6:7], off
	global_load_dword v18, v[4:5], off
	v_mad_i64_i32 v[4:5], s[50:51], s53, v205, v[140:141]
	s_sub_i32 s50, s40, s52
	s_add_i32 s52, s50, 0x80
	v_lshl_add_u64 v[6:7], v[4:5], 0, s[78:79]
	v_lshl_add_u64 v[4:5], v[4:5], 0, s[20:21]
	s_add_i32 s50, s52, s41
	global_load_dword v26, v[6:7], off
	global_load_dword v21, v[4:5], off
	v_mad_i64_i32 v[4:5], s[50:51], s50, v205, v[140:141]
	v_lshl_add_u64 v[6:7], v[4:5], 0, s[78:79]
	v_lshl_add_u64 v[4:5], v[4:5], 0, s[20:21]
	s_add_i32 s50, s52, s42
	global_load_dword v41, v[6:7], off
	s_nop 0
	global_load_dword v4, v[4:5], off
	v_mad_i64_i32 v[6:7], s[50:51], s50, v205, v[140:141]
	v_lshl_add_u64 v[38:39], v[6:7], 0, s[78:79]
	v_lshl_add_u64 v[6:7], v[6:7], 0, s[20:21]
	s_add_i32 s50, s52, s43
	global_load_dword v45, v[38:39], off
	global_load_dword v5, v[6:7], off
	v_mad_i64_i32 v[6:7], s[50:51], s50, v205, v[140:141]
	v_lshl_add_u64 v[38:39], v[6:7], 0, s[78:79]
	v_lshl_add_u64 v[6:7], v[6:7], 0, s[20:21]
	s_add_i32 s50, s52, s45
	global_load_dword v68, v[38:39], off
	s_nop 0
	global_load_dword v6, v[6:7], off
	v_mad_i64_i32 v[38:39], s[50:51], s50, v205, v[140:141]
	v_lshl_add_u64 v[42:43], v[38:39], 0, s[78:79]
	v_lshl_add_u64 v[38:39], v[38:39], 0, s[20:21]
	s_add_i32 s50, s52, s46
	global_load_dword v69, v[42:43], off
	global_load_dword v7, v[38:39], off
	v_mad_i64_i32 v[38:39], s[50:51], s50, v205, v[140:141]
	v_lshl_add_u64 v[42:43], v[38:39], 0, s[78:79]
	v_lshl_add_u64 v[38:39], v[38:39], 0, s[20:21]
	s_add_i32 s50, s52, s47
	global_load_dword v75, v[42:43], off
	global_load_dword v40, v[38:39], off
	v_mad_i64_i32 v[38:39], s[50:51], s50, v205, v[140:141]
	v_lshl_add_u64 v[42:43], v[38:39], 0, s[78:79]
	v_lshl_add_u64 v[38:39], v[38:39], 0, s[20:21]
	s_add_i32 s50, s52, s48
	global_load_dword v77, v[42:43], off
	global_load_dword v44, v[38:39], off
	v_mad_i64_i32 v[38:39], s[50:51], s50, v205, v[140:141]
	v_lshl_add_u64 v[42:43], v[38:39], 0, s[78:79]
	v_lshl_add_u64 v[38:39], v[38:39], 0, s[20:21]
	s_add_i32 s52, s52, s49
	global_load_dword v78, v[42:43], off
	global_load_dword v67, v[38:39], off
	v_mad_i64_i32 v[38:39], s[50:51], s52, v205, v[140:141]
	v_lshl_add_u64 v[42:43], v[38:39], 0, s[78:79]
	v_lshl_add_u64 v[38:39], v[38:39], 0, s[20:21]
	global_load_dword v79, v[42:43], off
	global_load_dword v74, v[38:39], off
	v_mul_f32_e64 v38, v123, -v9
	v_mul_f32_e32 v38, 0x3fb8aa3b, v38
	v_exp_f32_e32 v46, v38
	s_waitcnt vmcnt(47)
	v_lshlrev_b32_e32 v38, 16, v25
	v_and_b32_e32 v25, 0xffff0000, v25
	s_waitcnt lgkmcnt(0)
	v_mul_f32_e32 v38, v46, v38
	v_mul_f32_e32 v25, v46, v25
	s_barrier
	v_cvt_pk_bf16_f32 v25, v38, v25
	v_mul_f32_e64 v38, v162, -v9
	v_mul_f32_e32 v38, 0x3fb8aa3b, v38
	v_exp_f32_e32 v47, v38
	s_waitcnt vmcnt(45)
	v_lshlrev_b32_e32 v38, 16, v29
	v_and_b32_e32 v29, 0xffff0000, v29
	s_and_b64 s[50:51], s[38:39], exec
	v_mul_f32_e32 v38, v47, v38
	v_mul_f32_e32 v29, v47, v29
	v_cvt_pk_bf16_f32 v29, v38, v29
	v_mul_f32_e64 v38, v163, -v9
	v_mul_f32_e32 v38, 0x3fb8aa3b, v38
	v_exp_f32_e32 v48, v38
	s_waitcnt vmcnt(43)
	v_lshlrev_b32_e32 v38, 16, v31
	v_and_b32_e32 v31, 0xffff0000, v31
	s_cselect_b32 s50, 0xc0, 0
	v_mul_f32_e32 v38, v48, v38
	v_mul_f32_e32 v31, v48, v31
	v_cvt_pk_bf16_f32 v31, v38, v31
	v_mul_f32_e64 v38, v164, -v9
	v_mul_f32_e32 v38, 0x3fb8aa3b, v38
	v_exp_f32_e32 v49, v38
	s_waitcnt vmcnt(41)
	v_lshlrev_b32_e32 v38, 16, v32
	v_and_b32_e32 v32, 0xffff0000, v32
	s_or_b32 s50, s40, s50
	v_mul_f32_e32 v38, v49, v38
	v_mul_f32_e32 v32, v49, v32
	v_cvt_pk_bf16_f32 v38, v38, v32
	v_mul_f32_e64 v32, v165, -v9
	v_mul_f32_e32 v32, 0x3fb8aa3b, v32
	v_exp_f32_e32 v50, v32
	s_waitcnt vmcnt(39)
	v_lshlrev_b32_e32 v32, 16, v33
	v_and_b32_e32 v33, 0xffff0000, v33
	s_add_i32 s40, s50, s41
	v_mul_f32_e32 v32, v50, v32
	v_mul_f32_e32 v33, v50, v33
	v_cvt_pk_bf16_f32 v39, v32, v33
	v_mul_f32_e64 v32, v166, -v9
	v_mul_f32_e32 v32, 0x3fb8aa3b, v32
	v_exp_f32_e32 v51, v32
	s_waitcnt vmcnt(37)
	v_lshlrev_b32_e32 v32, 16, v34
	v_and_b32_e32 v33, 0xffff0000, v34
	v_mul_f32_e32 v32, v51, v32
	v_mul_f32_e32 v33, v51, v33
	v_cvt_pk_bf16_f32 v42, v32, v33
	v_mul_f32_e64 v32, v167, -v9
	v_mul_f32_e32 v32, 0x3fb8aa3b, v32
	v_exp_f32_e32 v52, v32
	s_waitcnt vmcnt(35)
	v_lshlrev_b32_e32 v32, 16, v35
	v_and_b32_e32 v33, 0xffff0000, v35
	v_perm_b32 v34, v42, v39, s100
	v_mul_f32_e32 v32, v52, v32
	v_mul_f32_e32 v33, v52, v33
	v_cvt_pk_bf16_f32 v43, v32, v33
	v_mul_f32_e64 v32, v168, -v9
	v_mul_f32_e32 v32, 0x3fb8aa3b, v32
	v_exp_f32_e32 v53, v32
	s_waitcnt vmcnt(33)
	v_lshlrev_b32_e32 v32, 16, v37
	v_and_b32_e32 v33, 0xffff0000, v37
	v_mul_f32_e32 v32, v53, v32
	v_mul_f32_e32 v33, v53, v33
	v_cvt_pk_bf16_f32 v37, v32, v33
	v_and_b32_e32 v32, 0xffff, v25
	v_lshrrev_b32_e32 v25, 16, v25
	v_and_or_b32 v54, v29, s95, v25
	v_lshrrev_b32_e32 v25, 16, v31
	v_and_or_b32 v55, v38, s95, v25
	v_lshrrev_b32_e32 v25, 16, v39
	v_and_or_b32 v56, v42, s95, v25
	v_lshrrev_b32_e32 v25, 16, v43
	v_lshl_or_b32 v32, v29, 16, v32
	v_perm_b32 v33, v38, v31, s100
	v_perm_b32 v35, v37, v43, s100
	v_and_or_b32 v57, v37, s95, v25
	v_and_b32_e32 v25, 0xffff, v0
	ds_write_b128 v171, v[32:35] offset:32768
	ds_write_b128 v171, v[54:57] offset:32832
	v_lshl_or_b32 v32, v1, 16, v25
	v_and_b32_e32 v25, 0xffff, v2
	v_lshl_or_b32 v33, v3, 16, v25
	v_and_b32_e32 v25, 0xffff, v27
	v_lshl_or_b32 v34, v28, 16, v25
	v_and_b32_e32 v25, 0xffff, v30
	v_perm_b32 v0, v1, v0, s101
	s_waitcnt vmcnt(32)
	v_lshl_or_b32 v35, v36, 16, v25
	v_perm_b32 v1, v3, v2, s101
	v_perm_b32 v2, v28, v27, s101
	v_perm_b32 v3, v36, v30, s101
	ds_write_b128 v171, v[32:35] offset:49152
	ds_write_b128 v171, v[0:3] offset:49216
	v_mad_i64_i32 v[0:1], s[40:41], s40, v205, v[140:141]
	v_lshl_add_u64 v[2:3], v[0:1], 0, s[78:79]
	v_lshl_add_u64 v[0:1], v[0:1], 0, s[20:21]
	s_add_i32 s40, s50, s42
	global_load_dword v59, v[2:3], off
	global_load_dword v54, v[0:1], off
	v_mad_i64_i32 v[0:1], s[40:41], s40, v205, v[140:141]
	v_lshl_add_u64 v[2:3], v[0:1], 0, s[78:79]
	v_lshl_add_u64 v[0:1], v[0:1], 0, s[20:21]
	s_add_i32 s40, s50, s43
	global_load_dword v61, v[2:3], off
	global_load_dword v55, v[0:1], off
	v_mad_i64_i32 v[0:1], s[40:41], s40, v205, v[140:141]
	v_lshl_add_u64 v[2:3], v[0:1], 0, s[78:79]
	v_lshl_add_u64 v[0:1], v[0:1], 0, s[20:21]
	s_add_i32 s40, s50, s45
	global_load_dword v63, v[2:3], off
	global_load_dword v56, v[0:1], off
	v_mad_i64_i32 v[0:1], s[40:41], s40, v205, v[140:141]
	v_lshl_add_u64 v[2:3], v[0:1], 0, s[78:79]
	v_lshl_add_u64 v[0:1], v[0:1], 0, s[20:21]
	s_add_i32 s40, s50, s46
	global_load_dword v66, v[2:3], off
	global_load_dword v57, v[0:1], off
	v_mad_i64_i32 v[0:1], s[40:41], s40, v205, v[140:141]
	v_lshl_add_u64 v[2:3], v[0:1], 0, s[78:79]
	v_lshl_add_u64 v[0:1], v[0:1], 0, s[20:21]
	s_add_i32 s40, s50, s47
	global_load_dword v71, v[2:3], off
	global_load_dword v58, v[0:1], off
	v_mad_i64_i32 v[0:1], s[40:41], s40, v205, v[140:141]
	v_lshl_add_u64 v[2:3], v[0:1], 0, s[78:79]
	v_lshl_add_u64 v[0:1], v[0:1], 0, s[20:21]
	s_add_i32 s40, s50, s48
	global_load_dword v72, v[2:3], off
	global_load_dword v60, v[0:1], off
	v_mad_i64_i32 v[0:1], s[40:41], s40, v205, v[140:141]
	v_lshl_add_u64 v[2:3], v[0:1], 0, s[78:79]
	v_lshl_add_u64 v[0:1], v[0:1], 0, s[20:21]
	s_add_i32 s50, s50, s49
	global_load_dword v73, v[2:3], off
	global_load_dword v62, v[0:1], off
	v_mad_i64_i32 v[0:1], s[40:41], s50, v205, v[140:141]
	v_lshl_add_u64 v[2:3], v[0:1], 0, s[78:79]
	v_lshl_add_u64 v[0:1], v[0:1], 0, s[20:21]
	global_load_dword v76, v[2:3], off
	global_load_dword v70, v[0:1], off
	s_waitcnt lgkmcnt(0)
	s_barrier
	ds_read_b128 v[0:3], v172 offset:32768
	ds_read_b128 v[28:31], v172 offset:33792
	ds_read_b128 v[244:247], v170 offset:49152
	ds_read_b128 v[248:251], v170 offset:50176
	ds_read_b128 v[252:255], v170 offset:51200
	ds_read_b128 v[196:199], v170 offset:52224
	s_waitcnt lgkmcnt(3)
	v_mfma_f32_16x16x32_bf16 v[32:35], v[0:3], v[244:247], 0
	s_waitcnt vmcnt(47)
	v_lshlrev_b32_e32 v25, 16, v15
	v_and_b32_e32 v15, 0xffff0000, v15
	v_mul_f32_e32 v25, v46, v25
	s_waitcnt lgkmcnt(2)
	v_mfma_f32_16x16x32_bf16 v[32:35], v[28:31], v[248:251], v[32:35]
	ds_read_b128 v[244:247], v170 offset:53248
	ds_read_b128 v[248:251], v170 offset:54272
	v_mul_f32_e32 v15, v46, v15
	s_add_i32 s20, s27, s28
	s_ashr_i32 s21, s20, 31
	s_lshl_b64 s[40:41], s[20:21], 15
	v_readlane_b32 s42, v242, 58
	s_nop 2
	v_pk_fma_f32 v[42:43], v[8:9], 0, v[32:33] op_sel_hi:[0,0,1]
	v_pk_fma_f32 v[88:89], v[8:9], 0, v[34:35] op_sel_hi:[0,0,1]
	s_waitcnt lgkmcnt(3)
	v_mfma_f32_16x16x32_bf16 v[32:35], v[0:3], v[252:255], 0
	s_add_u32 s40, s42, s40
	v_readlane_b32 s42, v242, 60
	s_addc_u32 s41, s42, s41
	s_waitcnt lgkmcnt(2)
	v_mfma_f32_16x16x32_bf16 v[32:35], v[28:31], v[196:199], v[32:35]
	ds_read_b128 v[252:255], v170 offset:55296
	ds_read_b128 v[196:199], v170 offset:56320
	s_mov_b64 s[42:43], 0
	s_and_b64 vcc, exec, s[34:35]
	s_nop 5
	v_pk_fma_f32 v[90:91], v[8:9], 0, v[32:33] op_sel_hi:[0,0,1]
	v_pk_fma_f32 v[92:93], v[8:9], 0, v[34:35] op_sel_hi:[0,0,1]
	s_waitcnt lgkmcnt(3)
	v_mfma_f32_16x16x32_bf16 v[32:35], v[0:3], v[244:247], 0
	s_waitcnt lgkmcnt(2)
	v_mfma_f32_16x16x32_bf16 v[32:35], v[28:31], v[248:251], v[32:35]
	ds_read_b128 v[244:247], v170 offset:57344
	ds_read_b128 v[248:251], v170 offset:58368
	s_nop 7
	v_pk_fma_f32 v[94:95], v[8:9], 0, v[32:33] op_sel_hi:[0,0,1]
	v_pk_fma_f32 v[96:97], v[8:9], 0, v[34:35] op_sel_hi:[0,0,1]
	s_waitcnt lgkmcnt(3)
	v_mfma_f32_16x16x32_bf16 v[32:35], v[0:3], v[252:255], 0
	s_waitcnt lgkmcnt(2)
	v_mfma_f32_16x16x32_bf16 v[32:35], v[28:31], v[196:199], v[32:35]
	ds_read_b128 v[252:255], v170 offset:59392
	ds_read_b128 v[196:199], v170 offset:60416
	s_nop 7
	v_pk_fma_f32 v[98:99], v[8:9], 0, v[32:33] op_sel_hi:[0,0,1]
	v_pk_fma_f32 v[100:101], v[8:9], 0, v[34:35] op_sel_hi:[0,0,1]
	s_waitcnt lgkmcnt(3)
	v_mfma_f32_16x16x32_bf16 v[32:35], v[0:3], v[244:247], 0
	s_waitcnt lgkmcnt(2)
	v_mfma_f32_16x16x32_bf16 v[32:35], v[28:31], v[248:251], v[32:35]
	ds_read_b128 v[244:247], v170 offset:61440
	ds_read_b128 v[248:251], v170 offset:62464
	s_nop 7
	v_pk_fma_f32 v[102:103], v[8:9], 0, v[32:33] op_sel_hi:[0,0,1]
	v_pk_fma_f32 v[104:105], v[8:9], 0, v[34:35] op_sel_hi:[0,0,1]
	s_waitcnt lgkmcnt(3)
	v_mfma_f32_16x16x32_bf16 v[32:35], v[0:3], v[252:255], 0
	s_waitcnt lgkmcnt(2)
	v_mfma_f32_16x16x32_bf16 v[32:35], v[28:31], v[196:199], v[32:35]
	ds_read_b128 v[252:255], v170 offset:63488
	ds_read_b128 v[196:199], v170 offset:64512
	s_nop 7
	v_pk_fma_f32 v[106:107], v[8:9], 0, v[32:33] op_sel_hi:[0,0,1]
	v_pk_fma_f32 v[108:109], v[8:9], 0, v[34:35] op_sel_hi:[0,0,1]
	s_waitcnt lgkmcnt(3)
	v_mfma_f32_16x16x32_bf16 v[32:35], v[0:3], v[244:247], 0
	s_waitcnt lgkmcnt(2)
	v_mfma_f32_16x16x32_bf16 v[32:35], v[28:31], v[248:251], v[32:35]
	s_nop 7
	v_pk_fma_f32 v[110:111], v[8:9], 0, v[32:33] op_sel_hi:[0,0,1]
	v_pk_fma_f32 v[112:113], v[8:9], 0, v[34:35] op_sel_hi:[0,0,1]
	v_cvt_pk_bf16_f32 v15, v25, v15
	s_waitcnt vmcnt(45)
	v_lshlrev_b32_e32 v25, 16, v17
	v_and_b32_e32 v17, 0xffff0000, v17
	v_mul_f32_e32 v25, v47, v25
	v_mul_f32_e32 v17, v47, v17
	v_cvt_pk_bf16_f32 v17, v25, v17
	s_waitcnt vmcnt(43)
	v_lshlrev_b32_e32 v25, 16, v19
	v_and_b32_e32 v19, 0xffff0000, v19
	v_mul_f32_e32 v25, v48, v25
	v_mul_f32_e32 v19, v48, v19
	s_waitcnt lgkmcnt(1)
	v_mfma_f32_16x16x32_bf16 v[0:3], v[0:3], v[252:255], 0
	v_cvt_pk_bf16_f32 v19, v25, v19
	s_waitcnt vmcnt(41)
	v_lshlrev_b32_e32 v25, 16, v20
	v_and_b32_e32 v20, 0xffff0000, v20
	v_mul_f32_e32 v25, v49, v25
	v_mul_f32_e32 v20, v49, v20
	v_cvt_pk_bf16_f32 v20, v25, v20
	s_waitcnt vmcnt(39)
	v_lshlrev_b32_e32 v25, 16, v22
	v_and_b32_e32 v22, 0xffff0000, v22
	v_mul_f32_e32 v22, v50, v22
	s_waitcnt lgkmcnt(0)
	v_mfma_f32_16x16x32_bf16 v[0:3], v[28:31], v[196:199], v[0:3]
	v_mul_f32_e32 v25, v50, v25
	v_cvt_pk_bf16_f32 v28, v25, v22
	s_waitcnt vmcnt(37)
	v_lshlrev_b32_e32 v22, 16, v23
	v_mul_f32_e32 v22, v51, v22
	v_and_b32_e32 v23, 0xffff0000, v23
	v_mul_f32_e32 v23, v51, v23
	v_cvt_pk_bf16_f32 v29, v22, v23
	s_waitcnt vmcnt(35)
	v_lshlrev_b32_e32 v22, 16, v24
	v_mul_f32_e32 v22, v52, v22
	v_and_b32_e32 v23, 0xffff0000, v24
	v_mul_f32_e32 v23, v52, v23
	v_cvt_pk_bf16_f32 v30, v22, v23
	s_waitcnt vmcnt(33)
	v_lshlrev_b32_e32 v22, 16, v26
	v_mul_f32_e32 v22, v53, v22
	v_and_b32_e32 v23, 0xffff0000, v26
	v_mul_f32_e32 v23, v53, v23
	v_cvt_pk_bf16_f32 v31, v22, v23
	v_and_b32_e32 v22, 0xffff, v15
	v_lshrrev_b32_e32 v15, 16, v15
	v_and_or_b32 v26, v17, s95, v15
	v_lshrrev_b32_e32 v15, 16, v19
	v_and_or_b32 v27, v20, s95, v15
	v_lshrrev_b32_e32 v15, 16, v28
	v_and_b32_e32 v24, 0xffff, v28
	v_and_or_b32 v28, v29, s95, v15
	v_lshrrev_b32_e32 v15, 16, v30
	v_lshl_or_b32 v22, v17, 16, v22
	v_perm_b32 v23, v20, v19, s100
	v_lshl_or_b32 v24, v29, 16, v24
	v_perm_b32 v25, v31, v30, s100
	v_and_or_b32 v29, v31, s95, v15
	v_and_b32_e32 v15, 0xffff, v10
	ds_write_b128 v171, v[22:25]
	ds_write_b128 v171, v[26:29] offset:64
	v_lshl_or_b32 v22, v11, 16, v15
	v_and_b32_e32 v15, 0xffff, v12
	v_lshl_or_b32 v23, v13, 16, v15
	v_and_b32_e32 v15, 0xffff, v14
	v_lshl_or_b32 v24, v16, 16, v15
	v_and_b32_e32 v15, 0xffff, v18
	v_perm_b32 v10, v11, v10, s101
	s_waitcnt vmcnt(32)
	v_lshl_or_b32 v25, v21, 16, v15
	v_perm_b32 v11, v13, v12, s101
	v_perm_b32 v12, v16, v14, s101
	v_perm_b32 v13, v21, v18, s101
	ds_write_b128 v171, v[22:25] offset:16384
	ds_write_b128 v171, v[10:13] offset:16448
	s_waitcnt lgkmcnt(0)
	s_barrier
	ds_read_b128 v[80:83], v172
	ds_read_b128 v[84:87], v172 offset:1024
	ds_read_b128 v[244:247], v170 offset:16384
	ds_read_b128 v[248:251], v170 offset:17408
	ds_read_b128 v[252:255], v170 offset:18432
	ds_read_b128 v[196:199], v170 offset:19456
	s_waitcnt lgkmcnt(3)
	v_mfma_f32_16x16x32_bf16 v[10:13], v[80:83], v[244:247], 0
	v_fma_f32 v0, v8, 0, v0
	v_fma_f32 v1, v8, 0, v1
	v_pk_fma_f32 v[2:3], v[8:9], 0, v[2:3] op_sel_hi:[0,0,1]
	s_waitcnt lgkmcnt(2)
	v_mfma_f32_16x16x32_bf16 v[10:13], v[84:87], v[248:251], v[10:13]
	ds_read_b128 v[244:247], v170 offset:20480
	ds_read_b128 v[248:251], v170 offset:21504
	s_nop 7
	v_pk_fma_f32 v[26:27], v[8:9], v[88:89], v[12:13] op_sel_hi:[0,1,1]
	v_pk_fma_f32 v[14:15], v[8:9], v[42:43], v[10:11] op_sel_hi:[0,1,1]
	s_waitcnt lgkmcnt(3)
	v_mfma_f32_16x16x32_bf16 v[10:13], v[80:83], v[252:255], 0
	s_waitcnt lgkmcnt(2)
	v_mfma_f32_16x16x32_bf16 v[10:13], v[84:87], v[196:199], v[10:13]
	ds_read_b128 v[252:255], v170 offset:22528
	ds_read_b128 v[196:199], v170 offset:23552
	s_nop 7
	v_pk_fma_f32 v[28:29], v[8:9], v[92:93], v[12:13] op_sel_hi:[0,1,1]
	v_pk_fma_f32 v[16:17], v[8:9], v[90:91], v[10:11] op_sel_hi:[0,1,1]
	s_waitcnt lgkmcnt(3)
	v_mfma_f32_16x16x32_bf16 v[10:13], v[80:83], v[244:247], 0
	s_waitcnt lgkmcnt(2)
	v_mfma_f32_16x16x32_bf16 v[10:13], v[84:87], v[248:251], v[10:13]
	ds_read_b128 v[244:247], v170 offset:24576
	ds_read_b128 v[248:251], v170 offset:25600
	s_nop 7
	v_pk_fma_f32 v[30:31], v[8:9], v[96:97], v[12:13] op_sel_hi:[0,1,1]
	v_pk_fma_f32 v[18:19], v[8:9], v[94:95], v[10:11] op_sel_hi:[0,1,1]
	s_waitcnt lgkmcnt(3)
	v_mfma_f32_16x16x32_bf16 v[10:13], v[80:83], v[252:255], 0
	s_waitcnt lgkmcnt(2)
	v_mfma_f32_16x16x32_bf16 v[10:13], v[84:87], v[196:199], v[10:13]
	ds_read_b128 v[252:255], v170 offset:26624
	ds_read_b128 v[196:199], v170 offset:27648
	s_nop 7
	v_pk_fma_f32 v[32:33], v[8:9], v[100:101], v[12:13] op_sel_hi:[0,1,1]
	v_pk_fma_f32 v[20:21], v[8:9], v[98:99], v[10:11] op_sel_hi:[0,1,1]
	s_waitcnt lgkmcnt(3)
	v_mfma_f32_16x16x32_bf16 v[10:13], v[80:83], v[244:247], 0
	s_waitcnt lgkmcnt(2)
	v_mfma_f32_16x16x32_bf16 v[10:13], v[84:87], v[248:251], v[10:13]
	ds_read_b128 v[244:247], v170 offset:28672
	ds_read_b128 v[248:251], v170 offset:29696
	s_nop 7
	v_pk_fma_f32 v[34:35], v[8:9], v[104:105], v[12:13] op_sel_hi:[0,1,1]
	v_pk_fma_f32 v[22:23], v[8:9], v[102:103], v[10:11] op_sel_hi:[0,1,1]
	s_waitcnt lgkmcnt(3)
	v_mfma_f32_16x16x32_bf16 v[10:13], v[80:83], v[252:255], 0
	s_waitcnt lgkmcnt(2)
	v_mfma_f32_16x16x32_bf16 v[10:13], v[84:87], v[196:199], v[10:13]
	ds_read_b128 v[252:255], v170 offset:30720
	ds_read_b128 v[196:199], v170 offset:31744
	s_nop 7
	v_pk_fma_f32 v[36:37], v[8:9], v[108:109], v[12:13] op_sel_hi:[0,1,1]
	v_pk_fma_f32 v[24:25], v[8:9], v[106:107], v[10:11] op_sel_hi:[0,1,1]
	s_waitcnt lgkmcnt(3)
	v_mfma_f32_16x16x32_bf16 v[10:13], v[80:83], v[244:247], 0
	s_waitcnt lgkmcnt(2)
	v_mfma_f32_16x16x32_bf16 v[88:91], v[84:87], v[248:251], v[10:13]
	s_nop 7
	v_pk_fma_f32 v[10:11], v[8:9], v[112:113], v[90:91] op_sel_hi:[0,1,1]
	v_pk_fma_f32 v[12:13], v[8:9], v[110:111], v[88:89] op_sel_hi:[0,1,1]
	s_waitcnt lgkmcnt(1)
	v_mfma_f32_16x16x32_bf16 v[80:83], v[80:83], v[252:255], 0
	s_waitcnt lgkmcnt(0)
	v_mfma_f32_16x16x32_bf16 v[80:83], v[84:87], v[196:199], v[80:83]
	s_nop 7
	v_pk_fma_f32 v[42:43], v[8:9], v[0:1], v[80:81] op_sel_hi:[0,1,1]
	s_waitcnt vmcnt(31)
	v_lshlrev_b32_e32 v0, 16, v41
	v_mul_f32_e32 v0, v46, v0
	v_and_b32_e32 v1, 0xffff0000, v41
	v_mul_f32_e32 v1, v46, v1
	v_cvt_pk_bf16_f32 v41, v0, v1
	s_waitcnt vmcnt(29)
	v_lshlrev_b32_e32 v0, 16, v45
	v_mul_f32_e32 v0, v47, v0
	v_and_b32_e32 v1, 0xffff0000, v45
	v_mul_f32_e32 v1, v47, v1
	v_cvt_pk_bf16_f32 v45, v0, v1
	s_waitcnt vmcnt(27)
	v_lshlrev_b32_e32 v0, 16, v68
	v_mul_f32_e32 v0, v48, v0
	v_and_b32_e32 v1, 0xffff0000, v68
	v_mul_f32_e32 v1, v48, v1
	v_cvt_pk_bf16_f32 v68, v0, v1
	s_waitcnt vmcnt(25)
	v_lshlrev_b32_e32 v0, 16, v69
	v_mul_f32_e32 v0, v49, v0
	v_and_b32_e32 v1, 0xffff0000, v69
	v_mul_f32_e32 v1, v49, v1
	v_cvt_pk_bf16_f32 v69, v0, v1
	s_waitcnt vmcnt(23)
	v_lshlrev_b32_e32 v0, 16, v75
	v_mul_f32_e32 v0, v50, v0
	v_and_b32_e32 v1, 0xffff0000, v75
	v_mul_f32_e32 v1, v50, v1
	v_cvt_pk_bf16_f32 v75, v0, v1
	s_waitcnt vmcnt(21)
	v_lshlrev_b32_e32 v0, 16, v77
	v_mul_f32_e32 v0, v51, v0
	v_and_b32_e32 v1, 0xffff0000, v77
	v_mul_f32_e32 v1, v51, v1
	v_cvt_pk_bf16_f32 v77, v0, v1
	s_waitcnt vmcnt(19)
	v_lshlrev_b32_e32 v0, 16, v78
	v_mul_f32_e32 v0, v52, v0
	v_and_b32_e32 v1, 0xffff0000, v78
	v_mul_f32_e32 v1, v52, v1
	v_cvt_pk_bf16_f32 v81, v0, v1
	s_waitcnt vmcnt(17)
	v_lshlrev_b32_e32 v0, 16, v79
	v_mul_f32_e32 v0, v53, v0
	v_and_b32_e32 v1, 0xffff0000, v79
	v_pk_fma_f32 v[38:39], v[8:9], v[2:3], v[82:83] op_sel_hi:[0,1,1]
	v_mul_f32_e32 v1, v53, v1
	v_cvt_pk_bf16_f32 v82, v0, v1
	v_and_b32_e32 v0, 0xffff, v41
	v_lshrrev_b32_e32 v41, 16, v41
	v_and_or_b32 v78, v45, s95, v41
	v_lshrrev_b32_e32 v41, 16, v68
	v_and_or_b32 v79, v69, s95, v41
	v_lshrrev_b32_e32 v41, 16, v75
	v_lshl_or_b32 v0, v45, 16, v0
	v_perm_b32 v1, v69, v68, s100
	v_perm_b32 v2, v77, v75, s100
	v_perm_b32 v3, v82, v81, s100
	v_and_or_b32 v80, v77, s95, v41
	v_lshrrev_b32_e32 v41, 16, v81
	v_and_or_b32 v81, v82, s95, v41
	ds_write_b128 v171, v[0:3] offset:32768
	ds_write_b128 v171, v[78:81] offset:32832
	v_and_b32_e32 v0, 0xffff, v4
	v_lshl_or_b32 v0, v5, 16, v0
	v_perm_b32 v4, v5, v4, s101
	v_perm_b32 v1, v7, v6, s100
	v_perm_b32 v2, v44, v40, s100
	s_waitcnt vmcnt(16)
	v_perm_b32 v3, v74, v67, s100
	v_perm_b32 v5, v7, v6, s101
	v_perm_b32 v6, v44, v40, s101
	v_perm_b32 v7, v74, v67, s101
	ds_write_b128 v171, v[0:3] offset:49152
	ds_write_b128 v171, v[4:7] offset:49216
	s_waitcnt lgkmcnt(0)
	s_barrier
	ds_read_b128 v[0:3], v172 offset:32768
	ds_read_b128 v[4:7], v172 offset:33792
	ds_read_b128 v[244:247], v170 offset:49152
	ds_read_b128 v[248:251], v170 offset:50176
	ds_read_b128 v[252:255], v170 offset:51200
	ds_read_b128 v[196:199], v170 offset:52224
	s_waitcnt lgkmcnt(3)
	v_mfma_f32_16x16x32_bf16 v[78:81], v[0:3], v[244:247], 0
	s_waitcnt lgkmcnt(2)
	v_mfma_f32_16x16x32_bf16 v[78:81], v[4:7], v[248:251], v[78:81]
	ds_read_b128 v[244:247], v170 offset:53248
	ds_read_b128 v[248:251], v170 offset:54272
	s_nop 7
	v_pk_fma_f32 v[14:15], v[8:9], v[14:15], v[78:79] op_sel_hi:[0,1,1]
	v_pk_fma_f32 v[26:27], v[8:9], v[26:27], v[80:81] op_sel_hi:[0,1,1]
	s_waitcnt lgkmcnt(3)
	v_mfma_f32_16x16x32_bf16 v[78:81], v[0:3], v[252:255], 0
	s_waitcnt lgkmcnt(2)
	v_mfma_f32_16x16x32_bf16 v[78:81], v[4:7], v[196:199], v[78:81]
	ds_read_b128 v[252:255], v170 offset:55296
	ds_read_b128 v[196:199], v170 offset:56320
	s_nop 7
	v_pk_fma_f32 v[16:17], v[8:9], v[16:17], v[78:79] op_sel_hi:[0,1,1]
	v_pk_fma_f32 v[28:29], v[8:9], v[28:29], v[80:81] op_sel_hi:[0,1,1]
	s_waitcnt lgkmcnt(3)
	v_mfma_f32_16x16x32_bf16 v[78:81], v[0:3], v[244:247], 0
	s_waitcnt lgkmcnt(2)
	v_mfma_f32_16x16x32_bf16 v[78:81], v[4:7], v[248:251], v[78:81]
	ds_read_b128 v[244:247], v170 offset:57344
	ds_read_b128 v[248:251], v170 offset:58368
	s_nop 7
	v_pk_fma_f32 v[18:19], v[8:9], v[18:19], v[78:79] op_sel_hi:[0,1,1]
	v_pk_fma_f32 v[30:31], v[8:9], v[30:31], v[80:81] op_sel_hi:[0,1,1]
	s_waitcnt lgkmcnt(3)
	v_mfma_f32_16x16x32_bf16 v[78:81], v[0:3], v[252:255], 0
	s_waitcnt lgkmcnt(2)
	v_mfma_f32_16x16x32_bf16 v[78:81], v[4:7], v[196:199], v[78:81]
	ds_read_b128 v[252:255], v170 offset:59392
	ds_read_b128 v[196:199], v170 offset:60416
	s_nop 7
	v_pk_fma_f32 v[20:21], v[8:9], v[20:21], v[78:79] op_sel_hi:[0,1,1]
	v_pk_fma_f32 v[32:33], v[8:9], v[32:33], v[80:81] op_sel_hi:[0,1,1]
	s_waitcnt lgkmcnt(3)
	v_mfma_f32_16x16x32_bf16 v[78:81], v[0:3], v[244:247], 0
	s_waitcnt lgkmcnt(2)
	v_mfma_f32_16x16x32_bf16 v[78:81], v[4:7], v[248:251], v[78:81]
	ds_read_b128 v[244:247], v170 offset:61440
	ds_read_b128 v[248:251], v170 offset:62464
	s_nop 7
	v_pk_fma_f32 v[22:23], v[8:9], v[22:23], v[78:79] op_sel_hi:[0,1,1]
	v_pk_fma_f32 v[34:35], v[8:9], v[34:35], v[80:81] op_sel_hi:[0,1,1]
	s_waitcnt lgkmcnt(3)
	v_mfma_f32_16x16x32_bf16 v[78:81], v[0:3], v[252:255], 0
	s_waitcnt lgkmcnt(2)
	v_mfma_f32_16x16x32_bf16 v[78:81], v[4:7], v[196:199], v[78:81]
	ds_read_b128 v[252:255], v170 offset:63488
	ds_read_b128 v[196:199], v170 offset:64512
	s_nop 7
	v_pk_fma_f32 v[24:25], v[8:9], v[24:25], v[78:79] op_sel_hi:[0,1,1]
	v_pk_fma_f32 v[36:37], v[8:9], v[36:37], v[80:81] op_sel_hi:[0,1,1]
	s_waitcnt lgkmcnt(3)
	v_mfma_f32_16x16x32_bf16 v[78:81], v[0:3], v[244:247], 0
	s_waitcnt lgkmcnt(2)
	v_mfma_f32_16x16x32_bf16 v[78:81], v[4:7], v[248:251], v[78:81]
	s_nop 7
	v_pk_fma_f32 v[40:41], v[8:9], v[12:13], v[78:79] op_sel_hi:[0,1,1]
	v_pk_fma_f32 v[44:45], v[8:9], v[10:11], v[80:81] op_sel_hi:[0,1,1]
	s_waitcnt lgkmcnt(1)
	v_mfma_f32_16x16x32_bf16 v[0:3], v[0:3], v[252:255], 0
	s_waitcnt lgkmcnt(0)
	v_mfma_f32_16x16x32_bf16 v[0:3], v[4:7], v[196:199], v[0:3]
	s_nop 7
	v_pk_fma_f32 v[10:11], v[8:9], v[42:43], v[0:1] op_sel_hi:[0,1,1]
	s_waitcnt vmcnt(15)
	v_lshlrev_b32_e32 v0, 16, v59
	v_mul_f32_e32 v0, v46, v0
	v_and_b32_e32 v1, 0xffff0000, v59
	v_mul_f32_e32 v1, v46, v1
	v_cvt_pk_bf16_f32 v4, v0, v1
	s_waitcnt vmcnt(13)
	v_lshlrev_b32_e32 v0, 16, v61
	v_mul_f32_e32 v0, v47, v0
	v_and_b32_e32 v1, 0xffff0000, v61
	v_mul_f32_e32 v1, v47, v1
	v_cvt_pk_bf16_f32 v5, v0, v1
	s_waitcnt vmcnt(11)
	v_lshlrev_b32_e32 v0, 16, v63
	v_mul_f32_e32 v0, v48, v0
	v_and_b32_e32 v1, 0xffff0000, v63
	v_mul_f32_e32 v1, v48, v1
	v_cvt_pk_bf16_f32 v6, v0, v1
	s_waitcnt vmcnt(9)
	v_lshlrev_b32_e32 v0, 16, v66
	v_mul_f32_e32 v0, v49, v0
	v_and_b32_e32 v1, 0xffff0000, v66
	v_mul_f32_e32 v1, v49, v1
	v_cvt_pk_bf16_f32 v7, v0, v1
	s_waitcnt vmcnt(7)
	v_lshlrev_b32_e32 v0, 16, v71
	v_mul_f32_e32 v0, v50, v0
	v_and_b32_e32 v1, 0xffff0000, v71
	v_pk_fma_f32 v[12:13], v[8:9], v[38:39], v[2:3] op_sel_hi:[0,1,1]
	v_mul_f32_e32 v1, v50, v1
	v_cvt_pk_bf16_f32 v38, v0, v1
	s_waitcnt vmcnt(5)
	v_lshlrev_b32_e32 v0, 16, v72
	v_mul_f32_e32 v0, v51, v0
	v_and_b32_e32 v1, 0xffff0000, v72
	v_mul_f32_e32 v1, v51, v1
	v_cvt_pk_bf16_f32 v39, v0, v1
	s_waitcnt vmcnt(3)
	v_lshlrev_b32_e32 v0, 16, v73
	v_mul_f32_e32 v0, v52, v0
	v_and_b32_e32 v1, 0xffff0000, v73
	v_mul_f32_e32 v1, v52, v1
	v_cvt_pk_bf16_f32 v42, v0, v1
	s_waitcnt vmcnt(1)
	v_lshlrev_b32_e32 v0, 16, v76
	v_mul_f32_e32 v0, v53, v0
	v_and_b32_e32 v1, 0xffff0000, v76
	v_mul_f32_e32 v1, v53, v1
	v_cvt_pk_bf16_f32 v43, v0, v1
	v_and_b32_e32 v0, 0xffff, v4
	v_lshl_or_b32 v0, v5, 16, v0
	v_perm_b32 v4, v5, v4, s101
	v_perm_b32 v1, v7, v6, s100
	v_perm_b32 v2, v39, v38, s100
	v_perm_b32 v3, v43, v42, s100
	v_perm_b32 v5, v7, v6, s101
	v_perm_b32 v6, v39, v38, s101
	v_perm_b32 v7, v43, v42, s101
	ds_write_b128 v171, v[0:3]
	ds_write_b128 v171, v[4:7] offset:64
	v_perm_b32 v0, v55, v54, s100
	v_perm_b32 v1, v57, v56, s100
	v_perm_b32 v2, v60, v58, s100
	s_waitcnt vmcnt(0)
	v_perm_b32 v3, v70, v62, s100
	v_perm_b32 v4, v55, v54, s101
	v_perm_b32 v5, v57, v56, s101
	v_perm_b32 v6, v60, v58, s101
	v_perm_b32 v7, v70, v62, s101
	ds_write_b128 v171, v[0:3] offset:16384
	ds_write_b128 v171, v[4:7] offset:16448
	s_waitcnt lgkmcnt(0)
	s_barrier
	ds_read_b128 v[4:7], v172
	ds_read_b128 v[0:3], v172 offset:1024
	ds_read_b128 v[244:247], v170 offset:16384
	ds_read_b128 v[248:251], v170 offset:17408
	ds_read_b128 v[252:255], v170 offset:18432
	ds_read_b128 v[196:199], v170 offset:19456
	s_waitcnt lgkmcnt(3)
	v_mfma_f32_16x16x32_bf16 v[46:49], v[4:7], v[244:247], 0
	s_waitcnt lgkmcnt(2)
	v_mfma_f32_16x16x32_bf16 v[46:49], v[0:3], v[248:251], v[46:49]
	ds_read_b128 v[244:247], v170 offset:20480
	ds_read_b128 v[248:251], v170 offset:21504
	s_nop 7
	v_pk_fma_f32 v[26:27], v[8:9], v[26:27], v[48:49] op_sel_hi:[0,1,1]
	v_pk_fma_f32 v[14:15], v[8:9], v[14:15], v[46:47] op_sel_hi:[0,1,1]
	s_waitcnt lgkmcnt(3)
	v_mfma_f32_16x16x32_bf16 v[46:49], v[4:7], v[252:255], 0
	s_waitcnt lgkmcnt(2)
	v_mfma_f32_16x16x32_bf16 v[46:49], v[0:3], v[196:199], v[46:49]
	ds_read_b128 v[252:255], v170 offset:22528
	ds_read_b128 v[196:199], v170 offset:23552
	s_nop 7
	v_pk_fma_f32 v[28:29], v[8:9], v[28:29], v[48:49] op_sel_hi:[0,1,1]
	v_pk_fma_f32 v[16:17], v[8:9], v[16:17], v[46:47] op_sel_hi:[0,1,1]
	s_waitcnt lgkmcnt(3)
	v_mfma_f32_16x16x32_bf16 v[46:49], v[4:7], v[244:247], 0
	s_waitcnt lgkmcnt(2)
	v_mfma_f32_16x16x32_bf16 v[46:49], v[0:3], v[248:251], v[46:49]
	ds_read_b128 v[244:247], v170 offset:24576
	ds_read_b128 v[248:251], v170 offset:25600
	s_nop 7
	v_pk_fma_f32 v[38:39], v[8:9], v[30:31], v[48:49] op_sel_hi:[0,1,1]
	v_pk_fma_f32 v[42:43], v[8:9], v[18:19], v[46:47] op_sel_hi:[0,1,1]
	s_waitcnt lgkmcnt(3)
	v_mfma_f32_16x16x32_bf16 v[46:49], v[4:7], v[252:255], 0
	s_waitcnt lgkmcnt(2)
	v_mfma_f32_16x16x32_bf16 v[46:49], v[0:3], v[196:199], v[46:49]
	ds_read_b128 v[252:255], v170 offset:26624
	ds_read_b128 v[196:199], v170 offset:27648
	s_nop 7
	v_pk_fma_f32 v[48:49], v[8:9], v[32:33], v[48:49] op_sel_hi:[0,1,1]
	v_pk_fma_f32 v[46:47], v[8:9], v[20:21], v[46:47] op_sel_hi:[0,1,1]
	s_waitcnt lgkmcnt(3)
	v_mfma_f32_16x16x32_bf16 v[18:21], v[4:7], v[244:247], 0
	s_waitcnt lgkmcnt(2)
	v_mfma_f32_16x16x32_bf16 v[18:21], v[0:3], v[248:251], v[18:21]
	ds_read_b128 v[244:247], v170 offset:28672
	ds_read_b128 v[248:251], v170 offset:29696
	s_nop 7
	v_pk_fma_f32 v[34:35], v[8:9], v[34:35], v[20:21] op_sel_hi:[0,1,1]
	v_pk_fma_f32 v[50:51], v[8:9], v[22:23], v[18:19] op_sel_hi:[0,1,1]
	s_waitcnt lgkmcnt(3)
	v_mfma_f32_16x16x32_bf16 v[18:21], v[4:7], v[252:255], 0
	s_waitcnt lgkmcnt(2)
	v_mfma_f32_16x16x32_bf16 v[18:21], v[0:3], v[196:199], v[18:21]
	ds_read_b128 v[252:255], v170 offset:30720
	ds_read_b128 v[196:199], v170 offset:31744
	s_nop 7
	v_pk_fma_f32 v[30:31], v[8:9], v[36:37], v[20:21] op_sel_hi:[0,1,1]
	v_pk_fma_f32 v[32:33], v[8:9], v[24:25], v[18:19] op_sel_hi:[0,1,1]
	s_waitcnt lgkmcnt(3)
	v_mfma_f32_16x16x32_bf16 v[18:21], v[4:7], v[244:247], 0
	s_waitcnt lgkmcnt(2)
	v_mfma_f32_16x16x32_bf16 v[18:21], v[0:3], v[248:251], v[18:21]
	s_nop 7
	v_pk_fma_f32 v[36:37], v[8:9], v[44:45], v[20:21] op_sel_hi:[0,1,1]
	v_pk_fma_f32 v[40:41], v[8:9], v[40:41], v[18:19] op_sel_hi:[0,1,1]
	s_waitcnt lgkmcnt(1)
	v_mfma_f32_16x16x32_bf16 v[4:7], v[4:7], v[252:255], 0
	s_waitcnt lgkmcnt(0)
	v_mfma_f32_16x16x32_bf16 v[0:3], v[0:3], v[196:199], v[4:7]
	v_cvt_pk_bf16_f32 v4, v14, v15
	v_cvt_pk_bf16_f32 v5, v26, v27
	s_nop 5
	v_lshl_add_u64 v[6:7], s[40:41], 0, v[124:125]
	global_store_dwordx2 v[6:7], v[4:5], off
	v_lshl_add_u64 v[6:7], s[40:41], 0, v[126:127]
	v_cvt_pk_bf16_f32 v4, v16, v17
	v_cvt_pk_bf16_f32 v5, v28, v29
	global_store_dwordx2 v[6:7], v[4:5], off
	v_lshl_add_u64 v[6:7], s[40:41], 0, v[128:129]
	v_cvt_pk_bf16_f32 v4, v42, v43
	v_cvt_pk_bf16_f32 v5, v38, v39
	global_store_dwordx2 v[6:7], v[4:5], off
	v_lshl_add_u64 v[6:7], s[40:41], 0, v[130:131]
	v_cvt_pk_bf16_f32 v4, v46, v47
	v_cvt_pk_bf16_f32 v5, v48, v49
	global_store_dwordx2 v[6:7], v[4:5], off
	v_lshl_add_u64 v[6:7], s[40:41], 0, v[132:133]
	v_cvt_pk_bf16_f32 v4, v50, v51
	v_cvt_pk_bf16_f32 v5, v34, v35
	global_store_dwordx2 v[6:7], v[4:5], off
	v_lshl_add_u64 v[6:7], s[40:41], 0, v[134:135]
	v_pk_fma_f32 v[2:3], v[8:9], v[12:13], v[2:3] op_sel_hi:[0,1,1]
	v_pk_fma_f32 v[0:1], v[8:9], v[10:11], v[0:1] op_sel_hi:[0,1,1]
	v_cvt_pk_bf16_f32 v4, v32, v33
	v_cvt_pk_bf16_f32 v5, v30, v31
	global_store_dwordx2 v[6:7], v[4:5], off
	v_lshl_add_u64 v[6:7], s[40:41], 0, v[136:137]
	v_cvt_pk_bf16_f32 v4, v40, v41
	v_cvt_pk_bf16_f32 v5, v36, v37
	global_store_dwordx2 v[6:7], v[4:5], off
	v_cvt_pk_bf16_f32 v0, v0, v1
	v_cvt_pk_bf16_f32 v1, v2, v3
	v_lshl_add_u64 v[2:3], s[40:41], 0, v[138:139]
	s_mov_b64 s[40:41], 0
	global_store_dwordx2 v[2:3], v[0:1], off
	s_cbranch_vccz .LBB0_475
	v_mul_f32_e32 v0, 0xc3800000, v9
	v_mul_f32_e32 v0, 0x3fb8aa3b, v0
	v_exp_f32_e32 v0, v0
	s_mov_b64 s[40:41], -1
	v_mov_b32_e32 v1, v0
	s_branch .LBB0_475

.LBB0_475:
	s_and_b64 vcc, exec, s[42:43]
	s_cbranch_vccz .LBB0_494
	s_lshl_b32 s20, s44, 6
	s_and_b32 s42, s20, 0x180
	s_lshl_b32 s52, s27, 8
	s_lshr_b32 s43, s44, 4
	s_and_b64 s[20:21], s[38:39], exec
	s_movk_i32 s20, 0x400
	s_cselect_b32 s20, 0x200, s20
	s_mulk_i32 s43, 0x4100
	s_or_b32 s44, s20, s42
	s_add_i32 s52, s52, s43
	s_and_b64 s[20:21], s[38:39], exec
	s_cselect_b32 s20, 0, 0xc0
	s_or_b32 s45, s52, s20
	s_and_b64 s[20:21], s[38:39], exec
	s_cselect_b32 s54, s88, s58
	s_add_i32 s20, s45, s54
	s_lshl_b32 s78, s44, 1
	s_lshl_b32 s42, s42, 1
	v_mad_i64_i32 v[0:1], s[20:21], s20, v205, v[140:141]
	s_and_b64 s[20:21], s[38:39], exec
	s_cselect_b32 s53, s61, s63
	s_add_i32 s20, s45, s53
	s_waitcnt vmcnt(8)
	v_mad_i64_i32 v[4:5], s[20:21], s20, v205, v[140:141]
	s_and_b64 s[20:21], s[38:39], exec
	s_cselect_b32 s51, s57, s59
	s_add_i32 s20, s45, s51
	v_mad_i64_i32 v[8:9], s[20:21], s20, v205, v[140:141]
	s_and_b64 s[20:21], s[38:39], exec
	s_cselect_b32 s50, s60, s66
	s_add_i32 s20, s45, s50
	v_mad_i64_i32 v[12:13], s[20:21], s20, v205, v[140:141]
	s_and_b64 s[20:21], s[38:39], exec
	s_mov_b32 s43, s79
	s_cselect_b32 s49, s85, s89
	v_lshl_add_u64 v[2:3], v[0:1], 0, s[78:79]
	v_lshl_add_u64 v[0:1], v[0:1], 0, s[42:43]
	s_add_i32 s20, s45, s49
	v_lshl_add_u64 v[6:7], v[4:5], 0, s[78:79]
	v_lshl_add_u64 v[4:5], v[4:5], 0, s[42:43]
	v_lshl_add_u64 v[10:11], v[8:9], 0, s[78:79]
	v_lshl_add_u64 v[8:9], v[8:9], 0, s[42:43]
	v_lshl_add_u64 v[14:15], v[12:13], 0, s[78:79]
	v_lshl_add_u64 v[12:13], v[12:13], 0, s[42:43]
	global_load_dword v24, v[2:3], off
	global_load_dword v54, v[0:1], off offset:3072
	global_load_dword v25, v[6:7], off
	global_load_dword v55, v[4:5], off offset:3072
	global_load_dword v27, v[10:11], off
	global_load_dword v56, v[8:9], off offset:3072
	global_load_dword v31, v[14:15], off
	global_load_dword v57, v[12:13], off offset:3072
	v_mad_i64_i32 v[0:1], s[20:21], s20, v205, v[140:141]
	s_and_b64 s[20:21], s[38:39], exec
	v_readlane_b32 s20, v241, 45
	s_cselect_b32 s48, s97, s20
	s_add_i32 s20, s45, s48
	v_mad_i64_i32 v[4:5], s[20:21], s20, v205, v[140:141]
	s_and_b64 s[20:21], s[38:39], exec
	v_readlane_b32 s20, v241, 19
	v_readlane_b32 s21, v241, 23
	s_cselect_b32 s47, s20, s21
	s_add_i32 s20, s45, s47
	v_mad_i64_i32 v[8:9], s[20:21], s20, v205, v[140:141]
	s_and_b64 s[20:21], s[38:39], exec
	v_readlane_b32 s20, v241, 21
	v_readlane_b32 s21, v241, 27
	s_cselect_b32 s46, s20, s21
	s_add_i32 s45, s45, s46
	v_lshl_add_u64 v[2:3], v[0:1], 0, s[78:79]
	v_mad_i64_i32 v[12:13], s[20:21], s45, v205, v[140:141]
	v_lshl_add_u64 v[0:1], v[0:1], 0, s[42:43]
	v_lshl_add_u64 v[6:7], v[4:5], 0, s[78:79]
	v_lshl_add_u64 v[4:5], v[4:5], 0, s[42:43]
	v_lshl_add_u64 v[10:11], v[8:9], 0, s[78:79]
	v_lshl_add_u64 v[8:9], v[8:9], 0, s[42:43]
	v_lshl_add_u64 v[14:15], v[12:13], 0, s[78:79]
	v_lshl_add_u64 v[12:13], v[12:13], 0, s[42:43]
	global_load_dword v35, v[2:3], off
	global_load_dword v58, v[0:1], off offset:3072
	global_load_dword v39, v[6:7], off
	global_load_dword v59, v[4:5], off offset:3072
	global_load_dword v43, v[10:11], off
	global_load_dword v60, v[8:9], off offset:3072
	global_load_dword v47, v[14:15], off
	global_load_dword v61, v[12:13], off offset:3072
	s_lshl_b32 s29, s29, 6
	s_or_b32 s20, s29, s52
	s_add_i32 s44, s20, 64
	s_add_i32 s20, s44, s54
	v_mad_i64_i32 v[0:1], s[20:21], s20, v205, v[140:141]
	s_add_i32 s20, s44, s53
	s_nop 0
	v_mad_i64_i32 v[4:5], s[20:21], s20, v205, v[140:141]
	s_add_i32 s20, s44, s51
	v_lshl_add_u64 v[6:7], v[4:5], 0, s[78:79]
	v_lshl_add_u64 v[8:9], v[4:5], 0, s[42:43]
	v_mad_i64_i32 v[4:5], s[20:21], s20, v205, v[140:141]
	s_add_i32 s20, s44, s50
	v_lshl_add_u64 v[10:11], v[4:5], 0, s[78:79]
	v_lshl_add_u64 v[12:13], v[4:5], 0, s[42:43]
	v_mad_i64_i32 v[4:5], s[20:21], s20, v205, v[140:141]
	v_lshl_add_u64 v[2:3], v[0:1], 0, s[78:79]
	v_lshl_add_u64 v[0:1], v[0:1], 0, s[42:43]
	s_add_i32 s20, s44, s49
	v_lshl_add_u64 v[14:15], v[4:5], 0, s[78:79]
	v_lshl_add_u64 v[16:17], v[4:5], 0, s[42:43]
	global_load_dword v5, v[2:3], off
	global_load_dword v90, v[0:1], off offset:3072
	global_load_dword v4, v[6:7], off
	global_load_dword v106, v[8:9], off offset:3072
	s_nop 0
	global_load_dword v3, v[10:11], off
	global_load_dword v108, v[12:13], off offset:3072
	global_load_dword v2, v[14:15], off
	global_load_dword v109, v[16:17], off offset:3072
	v_mad_i64_i32 v[0:1], s[20:21], s20, v205, v[140:141]
	s_add_i32 s20, s44, s48
	s_nop 0
	v_mad_i64_i32 v[8:9], s[20:21], s20, v205, v[140:141]
	s_add_i32 s20, s44, s47
	v_lshl_add_u64 v[10:11], v[8:9], 0, s[78:79]
	v_lshl_add_u64 v[12:13], v[8:9], 0, s[42:43]
	v_mad_i64_i32 v[8:9], s[20:21], s20, v205, v[140:141]
	s_add_i32 s44, s44, s46
	v_lshl_add_u64 v[14:15], v[8:9], 0, s[78:79]
	v_lshl_add_u64 v[16:17], v[8:9], 0, s[42:43]
	v_mad_i64_i32 v[8:9], s[20:21], s44, v205, v[140:141]
	s_sub_i32 s20, s52, s29
	s_add_i32 s29, s20, 0x80
	v_lshl_add_u64 v[6:7], v[0:1], 0, s[78:79]
	v_lshl_add_u64 v[0:1], v[0:1], 0, s[42:43]
	s_add_i32 s20, s29, s54
	v_lshl_add_u64 v[18:19], v[8:9], 0, s[78:79]
	v_lshl_add_u64 v[20:21], v[8:9], 0, s[42:43]
	global_load_dword v9, v[6:7], off
	global_load_dword v113, v[0:1], off offset:3072
	global_load_dword v8, v[10:11], off
	global_load_dword v114, v[12:13], off offset:3072
	s_nop 0
	global_load_dword v7, v[14:15], off
	global_load_dword v115, v[16:17], off offset:3072
	global_load_dword v6, v[18:19], off
	global_load_dword v116, v[20:21], off offset:3072
	v_mad_i64_i32 v[0:1], s[20:21], s20, v205, v[140:141]
	s_add_i32 s20, s29, s53
	s_nop 0
	v_mad_i64_i32 v[12:13], s[20:21], s20, v205, v[140:141]
	s_add_i32 s20, s29, s51
	s_nop 0
	v_mad_i64_i32 v[16:17], s[20:21], s20, v205, v[140:141]
	s_add_i32 s20, s29, s50
	s_nop 0
	v_mad_i64_i32 v[20:21], s[20:21], s20, v205, v[140:141]
	v_lshl_add_u64 v[10:11], v[0:1], 0, s[78:79]
	v_lshl_add_u64 v[0:1], v[0:1], 0, s[42:43]
	s_add_i32 s20, s29, s49
	v_lshl_add_u64 v[14:15], v[12:13], 0, s[78:79]
	v_lshl_add_u64 v[12:13], v[12:13], 0, s[42:43]
	v_lshl_add_u64 v[18:19], v[16:17], 0, s[78:79]
	v_lshl_add_u64 v[16:17], v[16:17], 0, s[42:43]
	v_lshl_add_u64 v[22:23], v[20:21], 0, s[78:79]
	v_lshl_add_u64 v[20:21], v[20:21], 0, s[42:43]
	global_load_dword v89, v[10:11], off
	global_load_dword v92, v[0:1], off offset:3072
	global_load_dword v88, v[14:15], off
	global_load_dword v93, v[12:13], off offset:3072
	global_load_dword v87, v[18:19], off
	global_load_dword v94, v[16:17], off offset:3072
	global_load_dword v86, v[22:23], off
	global_load_dword v95, v[20:21], off offset:3072
	v_mad_i64_i32 v[0:1], s[20:21], s20, v205, v[140:141]
	s_add_i32 s20, s29, s48
	s_nop 0
	v_mad_i64_i32 v[12:13], s[20:21], s20, v205, v[140:141]
	s_add_i32 s20, s29, s47
	s_nop 0
	v_mad_i64_i32 v[16:17], s[20:21], s20, v205, v[140:141]
	s_add_i32 s29, s29, s46
	v_lshl_add_u64 v[10:11], v[0:1], 0, s[78:79]
	v_lshl_add_u64 v[18:19], v[16:17], 0, s[78:79]
	v_mad_i64_i32 v[20:21], s[20:21], s29, v205, v[140:141]
	v_lshl_add_u64 v[0:1], v[0:1], 0, s[42:43]
	v_lshl_add_u64 v[14:15], v[12:13], 0, s[78:79]
	v_lshl_add_u64 v[12:13], v[12:13], 0, s[42:43]
	v_lshl_add_u64 v[16:17], v[16:17], 0, s[42:43]
	v_lshl_add_u64 v[22:23], v[20:21], 0, s[78:79]
	v_lshl_add_u64 v[20:21], v[20:21], 0, s[42:43]
	global_load_dword v111, v[10:11], off
	global_load_dword v96, v[0:1], off offset:3072
	global_load_dword v107, v[14:15], off
	global_load_dword v97, v[12:13], off offset:3072
	global_load_dword v91, v[18:19], off
	global_load_dword v98, v[16:17], off offset:3072
	global_load_dword v104, v[22:23], off
	global_load_dword v99, v[20:21], off offset:3072
	s_waitcnt vmcnt(47)
	v_lshlrev_b32_e32 v18, 16, v24
	v_and_b32_e32 v19, 0xffff0000, v24
	v_pk_add_f32 v[20:21], v[18:19], 0 op_sel_hi:[1,0]
	s_waitcnt vmcnt(45)
	v_lshlrev_b32_e32 v22, 16, v25
	v_and_b32_e32 v23, 0xffff0000, v25
	v_pk_add_f32 v[24:25], v[20:21], v[22:23]
	s_waitcnt vmcnt(43)
	v_lshlrev_b32_e32 v26, 16, v27
	v_and_b32_e32 v27, 0xffff0000, v27
	v_pk_add_f32 v[28:29], v[24:25], v[26:27]
	s_waitcnt vmcnt(41)
	v_lshlrev_b32_e32 v30, 16, v31
	v_and_b32_e32 v31, 0xffff0000, v31
	v_pk_add_f32 v[32:33], v[28:29], v[30:31]
	s_waitcnt vmcnt(39)
	v_lshlrev_b32_e32 v34, 16, v35
	v_and_b32_e32 v35, 0xffff0000, v35
	v_pk_add_f32 v[36:37], v[32:33], v[34:35]
	s_waitcnt vmcnt(37)
	v_lshlrev_b32_e32 v38, 16, v39
	v_and_b32_e32 v39, 0xffff0000, v39
	v_pk_add_f32 v[40:41], v[36:37], v[38:39]
	s_waitcnt vmcnt(35)
	v_lshlrev_b32_e32 v42, 16, v43
	v_and_b32_e32 v43, 0xffff0000, v43
	v_pk_add_f32 v[44:45], v[40:41], v[42:43]
	s_waitcnt vmcnt(33)
	v_lshlrev_b32_e32 v46, 16, v47
	v_and_b32_e32 v47, 0xffff0000, v47
	v_pk_add_f32 v[48:49], v[44:45], v[46:47]
	v_add_u32_e32 v117, s22, v161
	ds_write_b64 v117, v[48:49]
	s_waitcnt lgkmcnt(0)
	s_barrier
	v_add_u32_e32 v100, s3, v161
	ds_read2st64_b64 v[10:13], v100 offset1:1
	ds_read2st64_b64 v[14:17], v100 offset0:2 offset1:3
	v_pk_mul_f32 v[18:19], v[18:19], s[94:95] op_sel_hi:[1,0]
	s_mov_b32 s20, 0x42f00000
	v_exp_f32_e32 v18, v18
	s_waitcnt lgkmcnt(1)
	v_pk_add_f32 v[0:1], v[10:11], 0 op_sel_hi:[1,0]
	v_exp_f32_e32 v19, v19
	v_cndmask_b32_e64 v11, 0, v1, s[4:5]
	v_cndmask_b32_e64 v10, 0, v0, s[4:5]
	v_pk_add_f32 v[50:51], v[12:13], v[10:11]
	v_pk_add_f32 v[0:1], v[0:1], v[12:13]
	v_cndmask_b32_e64 v11, v11, v51, s[6:7]
	v_cndmask_b32_e64 v10, v10, v50, s[6:7]
	s_waitcnt lgkmcnt(0)
	v_pk_add_f32 v[12:13], v[14:15], v[10:11]
	v_pk_add_f32 v[0:1], v[0:1], v[14:15]
	v_cndmask_b32_e64 v51, v11, v13, s[8:9]
	v_cndmask_b32_e64 v50, v10, v12, s[8:9]
	ds_read2st64_b64 v[10:13], v100 offset0:4 offset1:5
	v_pk_add_f32 v[14:15], v[16:17], v[50:51]
	v_pk_add_f32 v[0:1], v[0:1], v[16:17]
	v_cndmask_b32_e64 v51, v51, v15, s[10:11]
	v_cndmask_b32_e64 v50, v50, v14, s[10:11]
	ds_read2st64_b64 v[14:17], v100 offset0:6 offset1:7
	s_waitcnt lgkmcnt(1)
	v_pk_add_f32 v[52:53], v[10:11], v[50:51]
	v_pk_add_f32 v[18:19], v[18:19], 1.0 op_sel_hi:[1,0] neg_lo:[1,0] neg_hi:[1,0]
	v_cndmask_b32_e64 v51, v51, v53, s[12:13]
	v_cndmask_b32_e64 v50, v50, v52, s[12:13]
	v_pk_add_f32 v[52:53], v[12:13], v[50:51]
	v_pk_mul_f32 v[22:23], v[22:23], s[94:95] op_sel_hi:[1,0]
	v_cndmask_b32_e64 v51, v51, v53, s[14:15]
	v_cndmask_b32_e64 v50, v50, v52, s[14:15]
	s_waitcnt lgkmcnt(0)
	v_pk_add_f32 v[52:53], v[14:15], v[50:51]
	v_exp_f32_e32 v22, v22
	v_cndmask_b32_e64 v51, v51, v53, s[16:17]
	v_cndmask_b32_e64 v50, v50, v52, s[16:17]
	v_pk_add_f32 v[52:53], v[16:17], v[50:51]
	v_exp_f32_e32 v23, v23
	v_cndmask_b32_e64 v51, v51, v53, s[18:19]
	v_cndmask_b32_e64 v50, v50, v52, s[18:19]
	v_pk_add_f32 v[50:51], v[50:51], v[0:1] neg_lo:[0,1] neg_hi:[0,1]
	v_pk_add_f32 v[10:11], v[0:1], v[10:11]
	v_pk_mul_f32 v[50:51], v[50:51], s[94:95] op_sel_hi:[1,0]
	v_pk_add_f32 v[10:11], v[10:11], v[12:13]
	v_pk_fma_f32 v[20:21], v[20:21], s[94:95], v[50:51] op_sel_hi:[1,0,1]
	v_pk_add_f32 v[10:11], v[10:11], v[14:15]
	v_med3_f32 v20, -v20, s20, v207
	v_med3_f32 v21, -v21, s20, v207
	v_exp_f32_e32 v20, v20
	v_exp_f32_e32 v21, v21
	v_pk_add_f32 v[144:145], v[10:11], v[16:17]
	s_andn2_b64 vcc, exec, s[36:37]
	s_mov_b64 s[44:45], -1
	v_pk_mul_f32 v[18:19], v[18:19], v[20:21]
	v_pk_add_f32 v[20:21], v[22:23], 1.0 op_sel_hi:[1,0] neg_lo:[1,0] neg_hi:[1,0]
	v_cvt_pk_bf16_f32 v52, v18, v19
	v_pk_fma_f32 v[18:19], v[24:25], s[94:95], v[50:51] op_sel_hi:[1,0,1]
	v_pk_mul_f32 v[22:23], v[26:27], s[94:95] op_sel_hi:[1,0]
	v_med3_f32 v18, -v18, s20, v207
	v_med3_f32 v19, -v19, s20, v207
	v_exp_f32_e32 v18, v18
	v_exp_f32_e32 v19, v19
	v_exp_f32_e32 v22, v22
	v_exp_f32_e32 v23, v23
	v_pk_mul_f32 v[24:25], v[46:47], s[94:95] op_sel_hi:[1,0]
	v_pk_mul_f32 v[18:19], v[20:21], v[18:19]
	v_exp_f32_e32 v24, v24
	v_cvt_pk_bf16_f32 v26, v18, v19
	v_pk_fma_f32 v[18:19], v[28:29], s[94:95], v[50:51] op_sel_hi:[1,0,1]
	v_pk_add_f32 v[20:21], v[22:23], 1.0 op_sel_hi:[1,0] neg_lo:[1,0] neg_hi:[1,0]
	v_med3_f32 v18, -v18, s20, v207
	v_med3_f32 v19, -v19, s20, v207
	v_exp_f32_e32 v18, v18
	v_exp_f32_e32 v19, v19
	v_pk_mul_f32 v[22:23], v[30:31], s[94:95] op_sel_hi:[1,0]
	v_exp_f32_e32 v25, v25
	v_exp_f32_e32 v22, v22
	v_pk_mul_f32 v[18:19], v[20:21], v[18:19]
	v_exp_f32_e32 v23, v23
	v_cvt_pk_bf16_f32 v27, v18, v19
	v_pk_fma_f32 v[18:19], v[32:33], s[94:95], v[50:51] op_sel_hi:[1,0,1]
	v_med3_f32 v18, -v18, s20, v207
	v_med3_f32 v19, -v19, s20, v207
	v_exp_f32_e32 v18, v18
	v_exp_f32_e32 v19, v19
	v_pk_add_f32 v[20:21], v[22:23], 1.0 op_sel_hi:[1,0] neg_lo:[1,0] neg_hi:[1,0]
	v_pk_mul_f32 v[22:23], v[34:35], s[94:95] op_sel_hi:[1,0]
	v_pk_mul_f32 v[18:19], v[20:21], v[18:19]
	v_exp_f32_e32 v22, v22
	v_cvt_pk_bf16_f32 v28, v18, v19
	v_pk_fma_f32 v[18:19], v[36:37], s[94:95], v[50:51] op_sel_hi:[1,0,1]
	v_exp_f32_e32 v23, v23
	v_med3_f32 v18, -v18, s20, v207
	v_med3_f32 v19, -v19, s20, v207
	v_exp_f32_e32 v18, v18
	v_exp_f32_e32 v19, v19
	v_pk_add_f32 v[20:21], v[22:23], 1.0 op_sel_hi:[1,0] neg_lo:[1,0] neg_hi:[1,0]
	v_pk_mul_f32 v[22:23], v[38:39], s[94:95] op_sel_hi:[1,0]
	v_perm_b32 v10, v26, v52, s100
	v_pk_mul_f32 v[18:19], v[20:21], v[18:19]
	v_exp_f32_e32 v22, v22
	v_exp_f32_e32 v23, v23
	v_cvt_pk_bf16_f32 v29, v18, v19
	v_pk_fma_f32 v[18:19], v[40:41], s[94:95], v[50:51] op_sel_hi:[1,0,1]
	v_med3_f32 v18, -v18, s20, v207
	v_med3_f32 v19, -v19, s20, v207
	v_exp_f32_e32 v18, v18
	v_exp_f32_e32 v19, v19
	v_pk_add_f32 v[20:21], v[22:23], 1.0 op_sel_hi:[1,0] neg_lo:[1,0] neg_hi:[1,0]
	v_pk_mul_f32 v[22:23], v[42:43], s[94:95] op_sel_hi:[1,0]
	v_perm_b32 v11, v28, v27, s100
	v_exp_f32_e32 v22, v22
	v_exp_f32_e32 v23, v23
	v_pk_mul_f32 v[18:19], v[20:21], v[18:19]
	v_cvt_pk_bf16_f32 v30, v18, v19
	v_pk_fma_f32 v[18:19], v[44:45], s[94:95], v[50:51] op_sel_hi:[1,0,1]
	v_pk_add_f32 v[20:21], v[22:23], 1.0 op_sel_hi:[1,0] neg_lo:[1,0] neg_hi:[1,0]
	v_med3_f32 v18, -v18, s20, v207
	v_med3_f32 v19, -v19, s20, v207
	v_exp_f32_e32 v18, v18
	v_exp_f32_e32 v19, v19
	v_pk_fma_f32 v[22:23], v[48:49], s[94:95], v[50:51] op_sel_hi:[1,0,1]
	v_perm_b32 v12, v30, v29, s100
	v_med3_f32 v22, -v22, s20, v207
	v_med3_f32 v23, -v23, s20, v207
	v_exp_f32_e32 v22, v22
	v_exp_f32_e32 v23, v23
	v_pk_mul_f32 v[18:19], v[20:21], v[18:19]
	v_cvt_pk_bf16_f32 v20, v18, v19
	v_pk_add_f32 v[18:19], v[24:25], 1.0 op_sel_hi:[1,0] neg_lo:[1,0] neg_hi:[1,0]
	v_pk_mul_f32 v[18:19], v[18:19], v[22:23]
	v_cvt_pk_bf16_f32 v18, v18, v19
	v_perm_b32 v13, v18, v20, s100
	v_perm_b32 v14, v26, v52, s101
	v_perm_b32 v15, v28, v27, s101
	v_perm_b32 v16, v30, v29, s101
	v_perm_b32 v17, v18, v20, s101
	ds_write_b128 v171, v[10:13] offset:32768
	ds_write_b128 v171, v[14:17] offset:32832
	v_perm_b32 v10, v55, v54, s100
	v_perm_b32 v11, v57, v56, s100
	v_perm_b32 v12, v59, v58, s100
	s_waitcnt vmcnt(32)
	v_perm_b32 v13, v61, v60, s100
	v_perm_b32 v14, v55, v54, s101
	v_perm_b32 v15, v57, v56, s101
	v_perm_b32 v16, v59, v58, s101
	v_perm_b32 v17, v61, v60, s101
	ds_write_b128 v171, v[10:13] offset:49152
	ds_write_b128 v171, v[14:17] offset:49216
	v_cndmask_b32_e64 v10, 0, 1, s[36:37]
	v_cmp_ne_u32_e64 s[20:21], 1, v10
	s_cbranch_vccnz .LBB0_478
	s_mov_b64 s[44:45], 0

.LBB0_480:
	s_and_b64 s[38:39], s[38:39], exec
	s_cselect_b32 s29, 0xc0, 0
	s_or_b32 s29, s52, s29
	s_add_i32 s38, s29, s54
	v_mad_i64_i32 v[0:1], s[38:39], s38, v205, v[140:141]
	s_mov_b32 s43, s79
	v_lshl_add_u64 v[10:11], v[0:1], 0, s[78:79]
	v_lshl_add_u64 v[0:1], v[0:1], 0, s[42:43]
	s_add_i32 s38, s29, s53
	global_load_dword v103, v[10:11], off
	global_load_dword v173, v[0:1], off offset:3072
	v_mad_i64_i32 v[0:1], s[38:39], s38, v205, v[140:141]
	v_lshl_add_u64 v[10:11], v[0:1], 0, s[78:79]
	v_lshl_add_u64 v[0:1], v[0:1], 0, s[42:43]
	s_add_i32 s38, s29, s51
	global_load_dword v105, v[10:11], off
	global_load_dword v174, v[0:1], off offset:3072
	v_mad_i64_i32 v[0:1], s[38:39], s38, v205, v[140:141]
	v_lshl_add_u64 v[10:11], v[0:1], 0, s[78:79]
	v_lshl_add_u64 v[0:1], v[0:1], 0, s[42:43]
	s_add_i32 s38, s29, s50
	global_load_dword v110, v[10:11], off
	global_load_dword v175, v[0:1], off offset:3072
	v_mad_i64_i32 v[0:1], s[38:39], s38, v205, v[140:141]
	s_waitcnt vmcnt(37)
	v_lshlrev_b32_e32 v80, 16, v5
	v_and_b32_e32 v81, 0xffff0000, v5
	v_lshl_add_u64 v[10:11], v[0:1], 0, s[78:79]
	v_lshl_add_u64 v[0:1], v[0:1], 0, s[42:43]
	s_add_i32 s38, s29, s49
	v_pk_add_f32 v[82:83], v[80:81], 0 op_sel_hi:[1,0]
	s_waitcnt vmcnt(35)
	v_lshlrev_b32_e32 v76, 16, v4
	v_and_b32_e32 v77, 0xffff0000, v4
	global_load_dword v112, v[10:11], off
	global_load_dword v176, v[0:1], off offset:3072
	v_mad_i64_i32 v[0:1], s[38:39], s38, v205, v[140:141]
	v_pk_add_f32 v[78:79], v[82:83], v[76:77]
	s_waitcnt vmcnt(35)
	v_lshlrev_b32_e32 v72, 16, v3
	v_and_b32_e32 v73, 0xffff0000, v3
	v_lshl_add_u64 v[10:11], v[0:1], 0, s[78:79]
	v_lshl_add_u64 v[0:1], v[0:1], 0, s[42:43]
	s_add_i32 s38, s29, s48
	v_pk_add_f32 v[74:75], v[78:79], v[72:73]
	s_waitcnt vmcnt(33)
	v_lshlrev_b32_e32 v68, 16, v2
	v_and_b32_e32 v69, 0xffff0000, v2
	global_load_dword v118, v[10:11], off
	global_load_dword v177, v[0:1], off offset:3072
	v_mad_i64_i32 v[0:1], s[38:39], s38, v205, v[140:141]
	v_pk_add_f32 v[70:71], v[74:75], v[68:69]
	s_waitcnt vmcnt(33)
	v_lshlrev_b32_e32 v62, 16, v9
	v_and_b32_e32 v63, 0xffff0000, v9
	v_lshl_add_u64 v[10:11], v[0:1], 0, s[78:79]
	v_lshl_add_u64 v[0:1], v[0:1], 0, s[42:43]
	s_add_i32 s38, s29, s47
	v_pk_add_f32 v[66:67], v[70:71], v[62:63]
	s_waitcnt vmcnt(31)
	v_lshlrev_b32_e32 v58, 16, v8
	v_and_b32_e32 v59, 0xffff0000, v8
	global_load_dword v119, v[10:11], off
	global_load_dword v178, v[0:1], off offset:3072
	v_mad_i64_i32 v[0:1], s[38:39], s38, v205, v[140:141]
	v_pk_add_f32 v[60:61], v[66:67], v[58:59]
	s_waitcnt vmcnt(31)
	v_lshlrev_b32_e32 v52, 16, v7
	v_and_b32_e32 v53, 0xffff0000, v7
	v_lshl_add_u64 v[10:11], v[0:1], 0, s[78:79]
	v_lshl_add_u64 v[0:1], v[0:1], 0, s[42:43]
	s_add_i32 s29, s29, s46
	v_pk_add_f32 v[56:57], v[60:61], v[52:53]
	s_waitcnt vmcnt(29)
	v_lshlrev_b32_e32 v48, 16, v6
	v_and_b32_e32 v49, 0xffff0000, v6
	global_load_dword v120, v[10:11], off
	global_load_dword v179, v[0:1], off offset:3072
	v_mad_i64_i32 v[0:1], s[38:39], s29, v205, v[140:141]
	v_pk_add_f32 v[50:51], v[56:57], v[48:49]
	v_add_u32_e32 v182, s2, v161
	v_lshl_add_u64 v[10:11], v[0:1], 0, s[78:79]
	v_lshl_add_u64 v[0:1], v[0:1], 0, s[42:43]
	ds_write_b64 v182, v[50:51]
	global_load_dword v121, v[10:11], off
	global_load_dword v180, v[0:1], off offset:3072
	s_waitcnt lgkmcnt(0)
	s_barrier
	v_add_u32_e32 v152, s0, v64
	v_add_u32_e32 v153, s23, v64
	ds_read_b128 v[36:39], v172 offset:32768
	ds_read_b128 v[40:43], v172 offset:33792
	ds_read_b128 v[4:7], v152
	ds_read_b128 v[0:3], v153
	ds_read_b128 v[8:11], v170 offset:49152
	ds_read_b128 v[12:15], v170 offset:50176
	s_waitcnt lgkmcnt(1)
	v_mfma_f32_16x16x32_bf16 v[8:11], v[36:39], v[8:11], 0
	v_add_u32_e32 v181, s24, v161
	v_pk_mul_f32 v[80:81], v[80:81], s[94:95] op_sel_hi:[1,0]
	s_mov_b32 s29, 0x42f00000
	s_waitcnt lgkmcnt(0)
	v_mfma_f32_16x16x32_bf16 v[8:11], v[40:43], v[12:15], v[8:11]
	ds_read_b128 v[12:15], v170 offset:51200
	ds_read_b128 v[16:19], v170 offset:52224
	v_pk_mul_f32 v[76:77], v[76:77], s[94:95] op_sel_hi:[1,0]
	v_pk_mul_f32 v[72:73], v[72:73], s[94:95] op_sel_hi:[1,0]
	s_waitcnt lgkmcnt(1)
	v_mfma_f32_16x16x32_bf16 v[12:15], v[36:39], v[12:15], 0
	v_mul_f32_e64 v68, v68, s94
	v_mul_f32_e64 v69, v69, s94
	v_pk_mul_f32 v[62:63], v[62:63], s[94:95] op_sel_hi:[1,0]
	v_pk_mul_f32 v[58:59], v[58:59], s[94:95] op_sel_hi:[1,0]
	s_waitcnt lgkmcnt(0)
	v_mfma_f32_16x16x32_bf16 v[12:15], v[40:43], v[16:19], v[12:15]
	ds_read_b128 v[16:19], v170 offset:53248
	ds_read_b128 v[20:23], v170 offset:54272
	v_pk_mul_f32 v[52:53], v[52:53], s[94:95] op_sel_hi:[1,0]
	v_exp_f32_e32 v80, v80
	s_waitcnt lgkmcnt(1)
	v_mfma_f32_16x16x32_bf16 v[16:19], v[36:39], v[16:19], 0
	v_exp_f32_e32 v81, v81
	v_exp_f32_e32 v76, v76
	v_exp_f32_e32 v77, v77
	s_waitcnt lgkmcnt(0)
	v_mfma_f32_16x16x32_bf16 v[16:19], v[40:43], v[20:23], v[16:19]
	ds_read_b128 v[20:23], v170 offset:55296
	ds_read_b128 v[24:27], v170 offset:56320
	v_exp_f32_e32 v72, v72
	v_exp_f32_e32 v73, v73
	s_waitcnt lgkmcnt(1)
	v_mfma_f32_16x16x32_bf16 v[20:23], v[36:39], v[20:23], 0
	v_exp_f32_e32 v68, v68
	v_exp_f32_e32 v69, v69
	v_exp_f32_e32 v62, v62
	s_waitcnt lgkmcnt(0)
	v_mfma_f32_16x16x32_bf16 v[20:23], v[40:43], v[24:27], v[20:23]
	ds_read_b128 v[24:27], v170 offset:57344
	ds_read_b128 v[28:31], v170 offset:58368
	v_exp_f32_e32 v63, v63
	v_exp_f32_e32 v58, v58
	s_waitcnt lgkmcnt(1)
	v_mfma_f32_16x16x32_bf16 v[24:27], v[36:39], v[24:27], 0
	v_exp_f32_e32 v59, v59
	v_exp_f32_e32 v52, v52
	v_exp_f32_e32 v53, v53
	s_waitcnt lgkmcnt(0)
	v_mfma_f32_16x16x32_bf16 v[24:27], v[40:43], v[28:31], v[24:27]
	ds_read_b128 v[28:31], v170 offset:59392
	ds_read_b128 v[32:35], v170 offset:60416
	v_pk_mul_f32 v[48:49], v[48:49], s[94:95] op_sel_hi:[1,0]
	v_pk_add_f32 v[80:81], v[80:81], 1.0 op_sel_hi:[1,0] neg_lo:[1,0] neg_hi:[1,0]
	s_waitcnt lgkmcnt(1)
	v_mfma_f32_16x16x32_bf16 v[28:31], v[36:39], v[28:31], 0
	v_exp_f32_e32 v48, v48
	v_exp_f32_e32 v49, v49
	v_pk_add_f32 v[76:77], v[76:77], 1.0 op_sel_hi:[1,0] neg_lo:[1,0] neg_hi:[1,0]
	s_waitcnt lgkmcnt(0)
	v_mfma_f32_16x16x32_bf16 v[28:31], v[40:43], v[32:35], v[28:31]
	ds_read_b128 v[32:35], v170 offset:61440
	ds_read_b128 v[44:47], v170 offset:62464
	v_pk_add_f32 v[72:73], v[72:73], 1.0 op_sel_hi:[1,0] neg_lo:[1,0] neg_hi:[1,0]
	v_pk_add_f32 v[68:69], v[68:69], 1.0 op_sel_hi:[1,0] neg_lo:[1,0] neg_hi:[1,0]
	s_waitcnt lgkmcnt(1)
	v_mfma_f32_16x16x32_bf16 v[32:35], v[36:39], v[32:35], 0
	v_add_f32_e64 v62, -v62, 1.0
	v_add_f32_e64 v63, -v63, 1.0
	v_pk_add_f32 v[58:59], v[58:59], 1.0 op_sel_hi:[1,0] neg_lo:[1,0] neg_hi:[1,0]
	v_pk_add_f32 v[52:53], v[52:53], 1.0 op_sel_hi:[1,0] neg_lo:[1,0] neg_hi:[1,0]
	s_waitcnt lgkmcnt(0)
	v_mfma_f32_16x16x32_bf16 v[32:35], v[40:43], v[44:47], v[32:35]
	ds_read_b128 v[44:47], v170 offset:63488
	ds_read_b128 v[146:149], v170 offset:64512
	v_pk_add_f32 v[48:49], v[48:49], 1.0 op_sel_hi:[1,0] neg_lo:[1,0] neg_hi:[1,0]
	s_mov_b64 s[38:39], -1
	s_waitcnt lgkmcnt(1)
	v_mfma_f32_16x16x32_bf16 v[36:39], v[36:39], v[44:47], 0
	s_and_b64 vcc, exec, s[20:21]
	s_waitcnt lgkmcnt(0)
	v_mfma_f32_16x16x32_bf16 v[36:39], v[40:43], v[146:149], v[36:39]
	ds_read2st64_b64 v[40:43], v181 offset1:1
	s_waitcnt lgkmcnt(0)
	v_pk_add_f32 v[40:41], v[40:41], 0 op_sel_hi:[1,0]
	s_nop 0
	v_cndmask_b32_e64 v45, 0, v41, s[4:5]
	v_cndmask_b32_e64 v44, 0, v40, s[4:5]
	v_pk_add_f32 v[46:47], v[42:43], v[44:45]
	s_nop 0
	v_cndmask_b32_e64 v45, v45, v47, s[6:7]
	v_cndmask_b32_e64 v44, v44, v46, s[6:7]
	v_pk_add_f32 v[46:47], v[40:41], v[42:43]
	ds_read2st64_b64 v[40:43], v181 offset0:2 offset1:3
	s_waitcnt lgkmcnt(0)
	v_pk_add_f32 v[54:55], v[40:41], v[44:45]
	s_nop 0
	v_cndmask_b32_e64 v45, v45, v55, s[8:9]
	v_cndmask_b32_e64 v44, v44, v54, s[8:9]
	v_pk_add_f32 v[40:41], v[46:47], v[40:41]
	v_pk_add_f32 v[46:47], v[42:43], v[44:45]
	v_pk_add_f32 v[54:55], v[40:41], v[42:43]
	ds_read2st64_b64 v[40:43], v181 offset0:4 offset1:5
	v_cndmask_b32_e64 v45, v45, v47, s[10:11]
	v_cndmask_b32_e64 v44, v44, v46, s[10:11]
	s_waitcnt lgkmcnt(0)
	v_pk_add_f32 v[46:47], v[40:41], v[44:45]
	s_nop 0
	v_cndmask_b32_e64 v45, v45, v47, s[12:13]
	v_cndmask_b32_e64 v44, v44, v46, s[12:13]
	v_pk_add_f32 v[46:47], v[42:43], v[44:45]
	v_pk_add_f32 v[40:41], v[54:55], v[40:41]
	v_cndmask_b32_e64 v85, v45, v47, s[14:15]
	v_cndmask_b32_e64 v84, v44, v46, s[14:15]
	ds_read2st64_b64 v[44:47], v181 offset0:6 offset1:7
	v_pk_add_f32 v[40:41], v[40:41], v[42:43]
	s_waitcnt lgkmcnt(0)
	v_pk_add_f32 v[146:147], v[44:45], v[84:85]
	s_nop 0
	v_cndmask_b32_e64 v85, v85, v147, s[16:17]
	v_cndmask_b32_e64 v84, v84, v146, s[16:17]
	v_pk_add_f32 v[146:147], v[46:47], v[84:85]
	v_pk_add_f32 v[40:41], v[40:41], v[44:45]
	v_cndmask_b32_e64 v85, v85, v147, s[18:19]
	v_cndmask_b32_e64 v84, v84, v146, s[18:19]
	v_pk_add_f32 v[84:85], v[84:85], v[54:55] neg_lo:[0,1] neg_hi:[0,1]
	v_pk_add_f32 v[146:147], v[40:41], v[46:47]
	v_pk_mul_f32 v[84:85], v[84:85], s[94:95] op_sel_hi:[1,0]
	s_nop 0
	v_pk_fma_f32 v[82:83], v[82:83], s[94:95], v[84:85] op_sel_hi:[1,0,1]
	v_pk_fma_f32 v[78:79], v[78:79], s[94:95], v[84:85] op_sel_hi:[1,0,1]
	v_pk_fma_f32 v[74:75], v[74:75], s[94:95], v[84:85] op_sel_hi:[1,0,1]
	v_pk_fma_f32 v[70:71], v[70:71], s[94:95], v[84:85] op_sel_hi:[1,0,1]
	v_pk_fma_f32 v[66:67], v[66:67], s[94:95], v[84:85] op_sel_hi:[1,0,1]
	v_pk_fma_f32 v[60:61], v[60:61], s[94:95], v[84:85] op_sel_hi:[1,0,1]
	v_pk_fma_f32 v[56:57], v[56:57], s[94:95], v[84:85] op_sel_hi:[1,0,1]
	v_med3_f32 v82, -v82, s29, v207
	v_med3_f32 v83, -v83, s29, v207
	v_med3_f32 v78, -v78, s29, v207
	v_med3_f32 v79, -v79, s29, v207
	v_med3_f32 v74, -v74, s29, v207
	v_med3_f32 v75, -v75, s29, v207
	v_med3_f32 v70, -v70, s29, v207
	v_med3_f32 v71, -v71, s29, v207
	v_med3_f32 v66, -v66, s29, v207
	v_med3_f32 v67, -v67, s29, v207
	v_med3_f32 v60, -v60, s29, v207
	v_med3_f32 v61, -v61, s29, v207
	v_med3_f32 v56, -v56, s29, v207
	v_med3_f32 v57, -v57, s29, v207
	v_pk_fma_f32 v[50:51], v[50:51], s[94:95], v[84:85] op_sel_hi:[1,0,1]
	v_exp_f32_e32 v82, v82
	v_exp_f32_e32 v83, v83
	v_exp_f32_e32 v78, v78
	v_exp_f32_e32 v79, v79
	v_exp_f32_e32 v74, v74
	v_exp_f32_e32 v75, v75
	v_exp_f32_e32 v70, v70
	v_exp_f32_e32 v71, v71
	v_exp_f32_e32 v66, v66
	v_exp_f32_e32 v67, v67
	v_exp_f32_e32 v60, v60
	v_exp_f32_e32 v61, v61
	v_exp_f32_e32 v56, v56
	v_exp_f32_e32 v57, v57
	v_med3_f32 v50, -v50, s29, v207
	v_med3_f32 v51, -v51, s29, v207
	v_exp_f32_e32 v50, v50
	v_exp_f32_e32 v51, v51
	v_pk_mul_f32 v[80:81], v[80:81], v[82:83]
	v_pk_mul_f32 v[76:77], v[76:77], v[78:79]
	v_pk_mul_f32 v[72:73], v[72:73], v[74:75]
	v_pk_mul_f32 v[68:69], v[68:69], v[70:71]
	v_pk_mul_f32 v[62:63], v[62:63], v[66:67]
	v_pk_mul_f32 v[58:59], v[58:59], v[60:61]
	v_pk_mul_f32 v[52:53], v[52:53], v[56:57]
	v_cvt_pk_bf16_f32 v80, v80, v81
	v_cvt_pk_bf16_f32 v76, v76, v77
	v_cvt_pk_bf16_f32 v72, v72, v73
	v_cvt_pk_bf16_f32 v68, v68, v69
	v_cvt_pk_bf16_f32 v62, v62, v63
	v_cvt_pk_bf16_f32 v58, v58, v59
	s_nop 0
	v_cvt_pk_bf16_f32 v52, v52, v53
	v_pk_mul_f32 v[48:49], v[48:49], v[50:51]
	v_cvt_pk_bf16_f32 v48, v48, v49
	v_perm_b32 v40, v76, v80, s100
	v_perm_b32 v41, v68, v72, s100
	v_perm_b32 v42, v58, v62, s100
	v_perm_b32 v43, v48, v52, s100
	v_perm_b32 v44, v76, v80, s101
	v_perm_b32 v45, v68, v72, s101
	v_perm_b32 v46, v58, v62, s101
	v_perm_b32 v47, v48, v52, s101
	ds_write_b128 v171, v[40:43]
	ds_write_b128 v171, v[44:47] offset:64
	v_perm_b32 v40, v106, v90, s100
	v_perm_b32 v41, v109, v108, s100
	v_perm_b32 v42, v114, v113, s100
	s_waitcnt vmcnt(32)
	v_perm_b32 v43, v116, v115, s100
	v_perm_b32 v44, v106, v90, s101
	v_perm_b32 v45, v109, v108, s101
	v_perm_b32 v46, v114, v113, s101
	v_perm_b32 v47, v116, v115, s101
	ds_write_b128 v171, v[40:43] offset:16384
	ds_write_b128 v171, v[44:47] offset:16448
	s_cbranch_vccnz .LBB0_482
	s_mov_b64 s[38:39], 0

.LBB0_484:
	s_waitcnt vmcnt(31)
	v_lshlrev_b32_e32 v154, 16, v89
	v_and_b32_e32 v155, 0xffff0000, v89
	v_pk_add_f32 v[156:157], v[154:155], 0 op_sel_hi:[1,0]
	s_waitcnt vmcnt(29)
	v_lshlrev_b32_e32 v158, 16, v88
	v_and_b32_e32 v159, 0xffff0000, v88
	v_pk_add_f32 v[188:189], v[156:157], v[158:159]
	s_waitcnt vmcnt(27)
	v_lshlrev_b32_e32 v190, 16, v87
	v_and_b32_e32 v191, 0xffff0000, v87
	v_pk_add_f32 v[192:193], v[188:189], v[190:191]
	s_waitcnt vmcnt(25)
	v_lshlrev_b32_e32 v194, 16, v86
	v_and_b32_e32 v195, 0xffff0000, v86
	v_pk_add_f32 v[212:213], v[192:193], v[194:195]
	s_waitcnt vmcnt(23)
	v_lshlrev_b32_e32 v214, 16, v111
	v_and_b32_e32 v215, 0xffff0000, v111
	v_pk_add_f32 v[216:217], v[212:213], v[214:215]
	s_waitcnt vmcnt(21)
	v_lshlrev_b32_e32 v218, 16, v107
	v_and_b32_e32 v219, 0xffff0000, v107
	v_pk_add_f32 v[220:221], v[216:217], v[218:219]
	s_waitcnt vmcnt(19)
	v_lshlrev_b32_e32 v90, 16, v91
	v_and_b32_e32 v91, 0xffff0000, v91
	v_pk_add_f32 v[88:89], v[220:221], v[90:91]
	s_waitcnt vmcnt(17)
	v_lshlrev_b32_e32 v84, 16, v104
	v_and_b32_e32 v85, 0xffff0000, v104
	v_pk_add_f32 v[86:87], v[88:89], v[84:85]
	ds_write_b64 v117, v[86:87]
	s_waitcnt lgkmcnt(0)
	s_barrier
	ds_read_b128 v[60:63], v172
	ds_read_b128 v[78:81], v172 offset:1024
	ds_read_b128 v[40:43], v170 offset:16384
	ds_read_b128 v[44:47], v170 offset:17408
	s_waitcnt lgkmcnt(1)
	v_mfma_f32_16x16x32_bf16 v[40:43], v[60:63], v[40:43], 0
	v_add_u32_e32 v183, s25, v64
	v_add_u32_e32 v184, s26, v64
	v_pk_mul_f32 v[84:85], v[84:85], s[94:95] op_sel_hi:[1,0]
	s_waitcnt lgkmcnt(0)
	v_mfma_f32_16x16x32_bf16 v[66:69], v[78:81], v[44:47], v[40:43]
	s_nop 2
	ds_read_b128 v[40:43], v170 offset:18432
	ds_read_b128 v[44:47], v170 offset:19456
	v_pk_mul_f32 v[90:91], v[90:91], s[94:95] op_sel_hi:[1,0]
	v_exp_f32_e32 v84, v84
	s_waitcnt lgkmcnt(1)
	v_mfma_f32_16x16x32_bf16 v[40:43], v[60:63], v[40:43], 0
	v_exp_f32_e32 v85, v85
	v_exp_f32_e32 v90, v90
	v_exp_f32_e32 v91, v91
	s_waitcnt lgkmcnt(0)
	v_mfma_f32_16x16x32_bf16 v[40:43], v[78:81], v[44:47], v[40:43]
	ds_read_b128 v[44:47], v170 offset:20480
	ds_read_b128 v[48:51], v170 offset:21504
	v_pk_add_f32 v[84:85], v[84:85], 1.0 op_sel_hi:[1,0] neg_lo:[1,0] neg_hi:[1,0]
	v_pk_add_f32 v[90:91], v[90:91], 1.0 op_sel_hi:[1,0] neg_lo:[1,0] neg_hi:[1,0]
	s_waitcnt lgkmcnt(1)
	v_mfma_f32_16x16x32_bf16 v[44:47], v[60:63], v[44:47], 0
	s_and_b64 vcc, exec, s[20:21]
	s_mov_b64 s[38:39], -1
	s_waitcnt lgkmcnt(0)
	v_mfma_f32_16x16x32_bf16 v[44:47], v[78:81], v[48:51], v[44:47]
	ds_read_b128 v[48:51], v170 offset:22528
	ds_read_b128 v[52:55], v170 offset:23552
	s_waitcnt lgkmcnt(1)
	v_mfma_f32_16x16x32_bf16 v[48:51], v[60:63], v[48:51], 0
	s_waitcnt lgkmcnt(0)
	v_mfma_f32_16x16x32_bf16 v[48:51], v[78:81], v[52:55], v[48:51]
	ds_read_b128 v[52:55], v170 offset:24576
	ds_read_b128 v[56:59], v170 offset:25600
	s_waitcnt lgkmcnt(1)
	v_mfma_f32_16x16x32_bf16 v[52:55], v[60:63], v[52:55], 0
	s_waitcnt lgkmcnt(0)
	v_mfma_f32_16x16x32_bf16 v[52:55], v[78:81], v[56:59], v[52:55]
	ds_read_b128 v[56:59], v170 offset:26624
	ds_read_b128 v[70:73], v170 offset:27648
	s_waitcnt lgkmcnt(1)
	v_mfma_f32_16x16x32_bf16 v[56:59], v[60:63], v[56:59], 0
	s_waitcnt lgkmcnt(0)
	v_mfma_f32_16x16x32_bf16 v[56:59], v[78:81], v[70:73], v[56:59]
	ds_read_b128 v[70:73], v170 offset:28672
	ds_read_b128 v[74:77], v170 offset:29696
	ds_read_b128 v[106:109], v170 offset:30720
	ds_read_b128 v[114:117], v170 offset:31744
	s_waitcnt lgkmcnt(3)
	v_mfma_f32_16x16x32_bf16 v[70:73], v[60:63], v[70:73], 0
	s_waitcnt lgkmcnt(1)
	v_mfma_f32_16x16x32_bf16 v[106:109], v[60:63], v[106:109], 0
	v_mfma_f32_16x16x32_bf16 v[70:73], v[78:81], v[74:77], v[70:73]
	ds_read2st64_b64 v[148:151], v100 offset1:1
	ds_read_b128 v[60:63], v183
	ds_read_b128 v[74:77], v184
	s_waitcnt lgkmcnt(2)
	v_pk_add_f32 v[82:83], v[148:149], 0 op_sel_hi:[1,0]
	v_mfma_f32_16x16x32_bf16 v[78:81], v[78:81], v[114:117], v[106:109]
	v_cndmask_b32_e64 v115, 0, v83, s[4:5]
	v_cndmask_b32_e64 v114, 0, v82, s[4:5]
	v_pk_add_f32 v[116:117], v[150:151], v[114:115]
	ds_read2st64_b64 v[106:109], v100 offset0:2 offset1:3
	v_cndmask_b32_e64 v115, v115, v117, s[6:7]
	v_cndmask_b32_e64 v114, v114, v116, s[6:7]
	v_pk_add_f32 v[82:83], v[82:83], v[150:151]
	s_waitcnt lgkmcnt(0)
	v_pk_add_f32 v[116:117], v[106:107], v[114:115]
	s_nop 0
	v_cndmask_b32_e64 v149, v115, v117, s[8:9]
	v_cndmask_b32_e64 v148, v114, v116, s[8:9]
	ds_read2st64_b64 v[114:117], v100 offset0:4 offset1:5
	v_pk_add_f32 v[82:83], v[82:83], v[106:107]
	v_pk_add_f32 v[106:107], v[108:109], v[148:149]
	v_pk_add_f32 v[82:83], v[82:83], v[108:109]
	v_cndmask_b32_e64 v149, v149, v107, s[10:11]
	v_cndmask_b32_e64 v148, v148, v106, s[10:11]
	ds_read2st64_b64 v[106:109], v100 offset0:6 offset1:7
	s_waitcnt lgkmcnt(1)
	v_pk_add_f32 v[150:151], v[114:115], v[148:149]
	s_nop 0
	v_cndmask_b32_e64 v149, v149, v151, s[12:13]
	v_cndmask_b32_e64 v148, v148, v150, s[12:13]
	v_pk_add_f32 v[150:151], v[116:117], v[148:149]
	s_nop 0
	v_cndmask_b32_e64 v149, v149, v151, s[14:15]
	v_cndmask_b32_e64 v148, v148, v150, s[14:15]
	s_waitcnt lgkmcnt(0)
	v_pk_add_f32 v[150:151], v[106:107], v[148:149]
	s_nop 0
	v_cndmask_b32_e64 v149, v149, v151, s[16:17]
	v_cndmask_b32_e64 v148, v148, v150, s[16:17]
	v_pk_add_f32 v[150:151], v[108:109], v[148:149]
	s_nop 0
	v_cndmask_b32_e64 v149, v149, v151, s[18:19]
	v_cndmask_b32_e64 v148, v148, v150, s[18:19]
	v_pk_add_f32 v[148:149], v[148:149], v[82:83] neg_lo:[0,1] neg_hi:[0,1]
	v_pk_mul_f32 v[150:151], v[154:155], s[94:95] op_sel_hi:[1,0]
	v_pk_mul_f32 v[148:149], v[148:149], s[94:95] op_sel_hi:[1,0]
	v_exp_f32_e32 v150, v150
	v_pk_fma_f32 v[154:155], v[156:157], s[94:95], v[148:149] op_sel_hi:[1,0,1]
	v_exp_f32_e32 v151, v151
	v_med3_f32 v100, -v154, s29, v207
	v_exp_f32_e32 v154, v100
	v_med3_f32 v100, -v155, s29, v207
	v_exp_f32_e32 v155, v100
	v_pk_add_f32 v[150:151], v[150:151], 1.0 op_sel_hi:[1,0] neg_lo:[1,0] neg_hi:[1,0]
	v_pk_mul_f32 v[156:157], v[158:159], s[94:95] op_sel_hi:[1,0]
	v_pk_fma_f32 v[86:87], v[86:87], s[94:95], v[148:149] op_sel_hi:[1,0,1]
	v_pk_mul_f32 v[150:151], v[150:151], v[154:155]
	v_exp_f32_e32 v156, v156
	v_cvt_pk_bf16_f32 v100, v150, v151
	v_pk_fma_f32 v[150:151], v[188:189], s[94:95], v[148:149] op_sel_hi:[1,0,1]
	v_exp_f32_e32 v157, v157
	v_med3_f32 v104, -v150, s29, v207
	v_exp_f32_e32 v150, v104
	v_med3_f32 v104, -v151, s29, v207
	v_exp_f32_e32 v151, v104
	v_pk_add_f32 v[154:155], v[156:157], 1.0 op_sel_hi:[1,0] neg_lo:[1,0] neg_hi:[1,0]
	v_pk_mul_f32 v[156:157], v[190:191], s[94:95] op_sel_hi:[1,0]
	v_pk_fma_f32 v[88:89], v[88:89], s[94:95], v[148:149] op_sel_hi:[1,0,1]
	v_pk_mul_f32 v[150:151], v[154:155], v[150:151]
	v_exp_f32_e32 v156, v156
	v_cvt_pk_bf16_f32 v104, v150, v151
	v_pk_fma_f32 v[150:151], v[192:193], s[94:95], v[148:149] op_sel_hi:[1,0,1]
	v_exp_f32_e32 v157, v157
	v_med3_f32 v111, -v150, s29, v207
	v_exp_f32_e32 v150, v111
	v_med3_f32 v111, -v151, s29, v207
	v_exp_f32_e32 v151, v111
	v_pk_add_f32 v[154:155], v[156:157], 1.0 op_sel_hi:[1,0] neg_lo:[1,0] neg_hi:[1,0]
	v_pk_mul_f32 v[156:157], v[194:195], s[94:95] op_sel_hi:[1,0]
	v_med3_f32 v86, -v86, s29, v207
	v_pk_mul_f32 v[150:151], v[154:155], v[150:151]
	v_exp_f32_e32 v156, v156
	v_cvt_pk_bf16_f32 v111, v150, v151
	v_pk_fma_f32 v[150:151], v[212:213], s[94:95], v[148:149] op_sel_hi:[1,0,1]
	v_exp_f32_e32 v157, v157
	v_med3_f32 v113, -v150, s29, v207
	v_exp_f32_e32 v150, v113
	v_med3_f32 v113, -v151, s29, v207
	v_exp_f32_e32 v151, v113
	v_pk_add_f32 v[154:155], v[156:157], 1.0 op_sel_hi:[1,0] neg_lo:[1,0] neg_hi:[1,0]
	v_pk_mul_f32 v[156:157], v[214:215], s[94:95] op_sel_hi:[1,0]
	v_med3_f32 v87, -v87, s29, v207
	v_pk_mul_f32 v[150:151], v[154:155], v[150:151]
	v_exp_f32_e32 v156, v156
	v_cvt_pk_bf16_f32 v113, v150, v151
	v_pk_fma_f32 v[150:151], v[216:217], s[94:95], v[148:149] op_sel_hi:[1,0,1]
	v_exp_f32_e32 v157, v157
	v_med3_f32 v150, -v150, s29, v207
	v_med3_f32 v151, -v151, s29, v207
	v_exp_f32_e32 v150, v150
	v_exp_f32_e32 v151, v151
	v_pk_add_f32 v[154:155], v[156:157], 1.0 op_sel_hi:[1,0] neg_lo:[1,0] neg_hi:[1,0]
	v_pk_mul_f32 v[156:157], v[218:219], s[94:95] op_sel_hi:[1,0]
	v_med3_f32 v88, -v88, s29, v207
	v_pk_mul_f32 v[150:151], v[154:155], v[150:151]
	v_exp_f32_e32 v156, v156
	v_cvt_pk_bf16_f32 v158, v150, v151
	v_pk_fma_f32 v[150:151], v[220:221], s[94:95], v[148:149] op_sel_hi:[1,0,1]
	v_exp_f32_e32 v157, v157
	v_med3_f32 v150, -v150, s29, v207
	v_med3_f32 v151, -v151, s29, v207
	v_exp_f32_e32 v150, v150
	v_exp_f32_e32 v151, v151
	v_med3_f32 v89, -v89, s29, v207
	v_exp_f32_e32 v86, v86
	v_exp_f32_e32 v87, v87
	v_exp_f32_e32 v88, v88
	v_exp_f32_e32 v89, v89
	v_pk_add_f32 v[154:155], v[156:157], 1.0 op_sel_hi:[1,0] neg_lo:[1,0] neg_hi:[1,0]
	v_pk_mul_f32 v[84:85], v[84:85], v[86:87]
	v_pk_mul_f32 v[150:151], v[154:155], v[150:151]
	v_pk_mul_f32 v[88:89], v[90:91], v[88:89]
	v_cvt_pk_bf16_f32 v150, v150, v151
	v_cvt_pk_bf16_f32 v91, v88, v89
	v_cvt_pk_bf16_f32 v151, v84, v85
	v_pk_add_f32 v[84:85], v[82:83], v[114:115]
	v_pk_add_f32 v[84:85], v[84:85], v[116:117]
	v_perm_b32 v86, v150, v158, s100
	v_pk_add_f32 v[84:85], v[84:85], v[106:107]
	v_perm_b32 v87, v151, v91, s100
	v_pk_add_f32 v[148:149], v[84:85], v[108:109]
	v_perm_b32 v84, v104, v100, s100
	v_perm_b32 v85, v113, v111, s100
	v_perm_b32 v88, v104, v100, s101
	v_perm_b32 v89, v113, v111, s101
	v_perm_b32 v90, v150, v158, s101
	v_perm_b32 v91, v151, v91, s101
	ds_write_b128 v171, v[84:87] offset:32768
	ds_write_b128 v171, v[88:91] offset:32832
	v_perm_b32 v84, v93, v92, s100
	v_perm_b32 v85, v95, v94, s100
	v_perm_b32 v86, v97, v96, s100
	s_waitcnt vmcnt(16)
	v_perm_b32 v87, v99, v98, s100
	v_perm_b32 v88, v93, v92, s101
	v_perm_b32 v89, v95, v94, s101
	v_perm_b32 v90, v97, v96, s101
	v_perm_b32 v91, v99, v98, s101
	ds_write_b128 v171, v[84:87] offset:49152
	ds_write_b128 v171, v[88:91] offset:49216
	s_cbranch_vccnz .LBB0_486
	s_mov_b64 s[38:39], 0

.LBB0_488:
	s_waitcnt vmcnt(15)
	v_lshlrev_b32_e32 v216, 16, v103
	v_and_b32_e32 v217, 0xffff0000, v103
	v_pk_add_f32 v[218:219], v[216:217], 0 op_sel_hi:[1,0]
	s_waitcnt vmcnt(13)
	v_lshlrev_b32_e32 v220, 16, v105
	v_and_b32_e32 v221, 0xffff0000, v105
	v_pk_add_f32 v[222:223], v[218:219], v[220:221]
	s_waitcnt vmcnt(11)
	v_lshlrev_b32_e32 v224, 16, v110
	v_and_b32_e32 v225, 0xffff0000, v110
	v_pk_add_f32 v[226:227], v[222:223], v[224:225]
	s_waitcnt vmcnt(9)
	v_lshlrev_b32_e32 v228, 16, v112
	v_and_b32_e32 v229, 0xffff0000, v112
	v_pk_add_f32 v[230:231], v[226:227], v[228:229]
	s_waitcnt vmcnt(7)
	v_lshlrev_b32_e32 v232, 16, v118
	v_and_b32_e32 v233, 0xffff0000, v118
	v_pk_add_f32 v[234:235], v[230:231], v[232:233]
	s_waitcnt vmcnt(5)
	v_lshlrev_b32_e32 v236, 16, v119
	v_and_b32_e32 v237, 0xffff0000, v119
	v_pk_add_f32 v[238:239], v[234:235], v[236:237]
	s_waitcnt vmcnt(3)
	v_lshlrev_b32_e32 v158, 16, v120
	v_and_b32_e32 v159, 0xffff0000, v120
	v_pk_add_f32 v[156:157], v[238:239], v[158:159]
	s_waitcnt vmcnt(1)
	v_lshlrev_b32_e32 v150, 16, v121
	v_and_b32_e32 v151, 0xffff0000, v121
	v_pk_add_f32 v[154:155], v[156:157], v[150:151]
	ds_write_b64 v182, v[154:155]
	s_waitcnt lgkmcnt(0)
	s_barrier
	ds_read_b128 v[82:85], v172 offset:32768
	ds_read_b128 v[90:93], v172 offset:33792
	ds_read_b128 v[86:89], v170 offset:49152
	ds_read_b128 v[94:97], v170 offset:50176
	s_waitcnt lgkmcnt(1)
	v_mfma_f32_16x16x32_bf16 v[86:89], v[82:85], v[86:89], 0
	v_mul_f32_e64 v150, v150, s94
	v_mul_f32_e64 v151, v151, s94
	v_pk_mul_f32 v[158:159], v[158:159], s[94:95] op_sel_hi:[1,0]
	v_exp_f32_e32 v150, v150
	s_waitcnt lgkmcnt(0)
	v_mfma_f32_16x16x32_bf16 v[118:121], v[90:93], v[94:97], v[86:89]
	s_nop 2
	ds_read_b128 v[86:89], v170 offset:51200
	ds_read_b128 v[94:97], v170 offset:52224
	v_exp_f32_e32 v151, v151
	v_exp_f32_e32 v158, v158
	s_waitcnt lgkmcnt(1)
	v_mfma_f32_16x16x32_bf16 v[86:89], v[82:85], v[86:89], 0
	v_exp_f32_e32 v159, v159
	v_pk_add_f32 v[150:151], v[150:151], 1.0 op_sel_hi:[1,0] neg_lo:[1,0] neg_hi:[1,0]
	s_and_b64 vcc, exec, s[20:21]
	s_waitcnt lgkmcnt(0)
	v_mfma_f32_16x16x32_bf16 v[94:97], v[90:93], v[94:97], v[86:89]
	s_nop 2
	ds_read_b128 v[86:89], v170 offset:53248
	ds_read_b128 v[98:101], v170 offset:54272
	v_pk_add_f32 v[158:159], v[158:159], 1.0 op_sel_hi:[1,0] neg_lo:[1,0] neg_hi:[1,0]
	s_mov_b64 s[20:21], -1
	s_waitcnt lgkmcnt(1)
	v_mfma_f32_16x16x32_bf16 v[86:89], v[82:85], v[86:89], 0
	s_waitcnt lgkmcnt(0)
	v_mfma_f32_16x16x32_bf16 v[98:101], v[90:93], v[98:101], v[86:89]
	s_nop 5
	ds_read_b128 v[86:89], v170 offset:55296
	ds_read_b128 v[102:105], v170 offset:56320
	s_waitcnt lgkmcnt(1)
	v_mfma_f32_16x16x32_bf16 v[86:89], v[82:85], v[86:89], 0
	s_waitcnt lgkmcnt(0)
	v_mfma_f32_16x16x32_bf16 v[102:105], v[90:93], v[102:105], v[86:89]
	s_nop 5
	ds_read_b128 v[86:89], v170 offset:57344
	ds_read_b128 v[106:109], v170 offset:58368
	s_waitcnt lgkmcnt(1)
	v_mfma_f32_16x16x32_bf16 v[86:89], v[82:85], v[86:89], 0
	s_waitcnt lgkmcnt(0)
	v_mfma_f32_16x16x32_bf16 v[106:109], v[90:93], v[106:109], v[86:89]
	s_nop 5
	ds_read_b128 v[86:89], v170 offset:59392
	ds_read_b128 v[110:113], v170 offset:60416
	s_waitcnt lgkmcnt(1)
	v_mfma_f32_16x16x32_bf16 v[86:89], v[82:85], v[86:89], 0
	s_waitcnt lgkmcnt(0)
	v_mfma_f32_16x16x32_bf16 v[110:113], v[90:93], v[110:113], v[86:89]
	s_nop 5
	ds_read_b128 v[86:89], v170 offset:61440
	ds_read_b128 v[114:117], v170 offset:62464
	s_waitcnt lgkmcnt(1)
	v_mfma_f32_16x16x32_bf16 v[86:89], v[82:85], v[86:89], 0
	s_waitcnt lgkmcnt(0)
	v_mfma_f32_16x16x32_bf16 v[114:117], v[90:93], v[114:117], v[86:89]
	s_nop 5
	ds_read_b128 v[86:89], v170 offset:63488
	ds_read_b128 v[188:191], v170 offset:64512
	s_waitcnt lgkmcnt(1)
	v_mfma_f32_16x16x32_bf16 v[192:195], v[82:85], v[86:89], 0
	ds_read2st64_b64 v[212:215], v181 offset1:1
	ds_read_b128 v[82:85], v152
	ds_read_b128 v[86:89], v153
	s_waitcnt lgkmcnt(2)
	v_pk_add_f32 v[152:153], v[212:213], 0 op_sel_hi:[1,0]
	v_mfma_f32_16x16x32_bf16 v[90:93], v[90:93], v[188:191], v[192:195]
	ds_read2st64_b64 v[188:191], v181 offset0:2 offset1:3
	s_nop 1
	v_cndmask_b32_e64 v193, 0, v153, s[4:5]
	v_cndmask_b32_e64 v192, 0, v152, s[4:5]
	v_pk_add_f32 v[194:195], v[214:215], v[192:193]
	v_pk_add_f32 v[152:153], v[152:153], v[214:215]
	v_cndmask_b32_e64 v193, v193, v195, s[6:7]
	v_cndmask_b32_e64 v192, v192, v194, s[6:7]
	s_waitcnt lgkmcnt(0)
	v_pk_add_f32 v[194:195], v[188:189], v[192:193]
	v_pk_add_f32 v[152:153], v[152:153], v[188:189]
	v_cndmask_b32_e64 v213, v193, v195, s[8:9]
	v_cndmask_b32_e64 v212, v192, v194, s[8:9]
	ds_read2st64_b64 v[192:195], v181 offset0:4 offset1:5
	v_pk_add_f32 v[188:189], v[190:191], v[212:213]
	v_pk_add_f32 v[152:153], v[152:153], v[190:191]
	v_cndmask_b32_e64 v213, v213, v189, s[10:11]
	v_cndmask_b32_e64 v212, v212, v188, s[10:11]
	ds_read2st64_b64 v[188:191], v181 offset0:6 offset1:7
	s_waitcnt lgkmcnt(1)
	v_pk_add_f32 v[214:215], v[192:193], v[212:213]
	s_nop 0
	v_cndmask_b32_e64 v213, v213, v215, s[12:13]
	v_cndmask_b32_e64 v212, v212, v214, s[12:13]
	v_pk_add_f32 v[214:215], v[194:195], v[212:213]
	s_nop 0
	v_cndmask_b32_e64 v213, v213, v215, s[14:15]
	v_cndmask_b32_e64 v212, v212, v214, s[14:15]
	s_waitcnt lgkmcnt(0)
	v_pk_add_f32 v[214:215], v[188:189], v[212:213]
	s_nop 0
	v_cndmask_b32_e64 v213, v213, v215, s[16:17]
	v_cndmask_b32_e64 v212, v212, v214, s[16:17]
	v_pk_add_f32 v[214:215], v[190:191], v[212:213]
	s_nop 0
	v_cndmask_b32_e64 v213, v213, v215, s[18:19]
	v_cndmask_b32_e64 v212, v212, v214, s[18:19]
	v_pk_add_f32 v[212:213], v[212:213], v[152:153] neg_lo:[0,1] neg_hi:[0,1]
	v_pk_mul_f32 v[214:215], v[216:217], s[94:95] op_sel_hi:[1,0]
	v_pk_mul_f32 v[212:213], v[212:213], s[94:95] op_sel_hi:[1,0]
	v_exp_f32_e32 v214, v214
	v_pk_fma_f32 v[216:217], v[218:219], s[94:95], v[212:213] op_sel_hi:[1,0,1]
	v_exp_f32_e32 v215, v215
	v_med3_f32 v181, -v216, s29, v207
	v_exp_f32_e32 v216, v181
	v_med3_f32 v181, -v217, s29, v207
	v_exp_f32_e32 v217, v181
	v_pk_add_f32 v[214:215], v[214:215], 1.0 op_sel_hi:[1,0] neg_lo:[1,0] neg_hi:[1,0]
	v_pk_mul_f32 v[218:219], v[220:221], s[94:95] op_sel_hi:[1,0]
	v_pk_fma_f32 v[154:155], v[154:155], s[94:95], v[212:213] op_sel_hi:[1,0,1]
	v_pk_mul_f32 v[214:215], v[214:215], v[216:217]
	v_exp_f32_e32 v218, v218
	v_cvt_pk_bf16_f32 v181, v214, v215
	v_pk_fma_f32 v[214:215], v[222:223], s[94:95], v[212:213] op_sel_hi:[1,0,1]
	v_exp_f32_e32 v219, v219
	v_med3_f32 v182, -v214, s29, v207
	v_exp_f32_e32 v214, v182
	v_med3_f32 v182, -v215, s29, v207
	v_exp_f32_e32 v215, v182
	v_pk_add_f32 v[216:217], v[218:219], 1.0 op_sel_hi:[1,0] neg_lo:[1,0] neg_hi:[1,0]
	v_pk_mul_f32 v[218:219], v[224:225], s[94:95] op_sel_hi:[1,0]
	v_pk_fma_f32 v[156:157], v[156:157], s[94:95], v[212:213] op_sel_hi:[1,0,1]
	v_pk_mul_f32 v[214:215], v[216:217], v[214:215]
	v_exp_f32_e32 v218, v218
	v_cvt_pk_bf16_f32 v182, v214, v215
	v_pk_fma_f32 v[214:215], v[226:227], s[94:95], v[212:213] op_sel_hi:[1,0,1]
	v_exp_f32_e32 v219, v219
	v_med3_f32 v187, -v214, s29, v207
	v_exp_f32_e32 v214, v187
	v_med3_f32 v187, -v215, s29, v207
	v_exp_f32_e32 v215, v187
	v_pk_add_f32 v[216:217], v[218:219], 1.0 op_sel_hi:[1,0] neg_lo:[1,0] neg_hi:[1,0]
	v_pk_mul_f32 v[218:219], v[228:229], s[94:95] op_sel_hi:[1,0]
	v_med3_f32 v154, -v154, s29, v207
	v_pk_mul_f32 v[214:215], v[216:217], v[214:215]
	v_exp_f32_e32 v218, v218
	v_cvt_pk_bf16_f32 v187, v214, v215
	v_pk_fma_f32 v[214:215], v[230:231], s[94:95], v[212:213] op_sel_hi:[1,0,1]
	v_exp_f32_e32 v219, v219
	v_med3_f32 v211, -v214, s29, v207
	v_exp_f32_e32 v214, v211
	v_med3_f32 v211, -v215, s29, v207
	v_exp_f32_e32 v215, v211
	v_pk_add_f32 v[216:217], v[218:219], 1.0 op_sel_hi:[1,0] neg_lo:[1,0] neg_hi:[1,0]
	v_pk_mul_f32 v[218:219], v[232:233], s[94:95] op_sel_hi:[1,0]
	v_med3_f32 v155, -v155, s29, v207
	v_pk_mul_f32 v[214:215], v[216:217], v[214:215]
	v_exp_f32_e32 v218, v218
	v_cvt_pk_bf16_f32 v211, v214, v215
	v_pk_fma_f32 v[214:215], v[234:235], s[94:95], v[212:213] op_sel_hi:[1,0,1]
	v_exp_f32_e32 v219, v219
	v_med3_f32 v214, -v214, s29, v207
	v_med3_f32 v215, -v215, s29, v207
	v_exp_f32_e32 v214, v214
	v_exp_f32_e32 v215, v215
	v_pk_add_f32 v[216:217], v[218:219], 1.0 op_sel_hi:[1,0] neg_lo:[1,0] neg_hi:[1,0]
	v_pk_mul_f32 v[218:219], v[236:237], s[94:95] op_sel_hi:[1,0]
	v_med3_f32 v156, -v156, s29, v207
	v_pk_mul_f32 v[214:215], v[216:217], v[214:215]
	v_exp_f32_e32 v218, v218
	v_cvt_pk_bf16_f32 v220, v214, v215
	v_pk_fma_f32 v[214:215], v[238:239], s[94:95], v[212:213] op_sel_hi:[1,0,1]
	v_exp_f32_e32 v219, v219
	v_med3_f32 v214, -v214, s29, v207
	v_med3_f32 v215, -v215, s29, v207
	v_exp_f32_e32 v214, v214
	v_exp_f32_e32 v215, v215
	v_med3_f32 v157, -v157, s29, v207
	v_exp_f32_e32 v154, v154
	v_exp_f32_e32 v155, v155
	v_exp_f32_e32 v156, v156
	v_exp_f32_e32 v157, v157
	v_pk_add_f32 v[216:217], v[218:219], 1.0 op_sel_hi:[1,0] neg_lo:[1,0] neg_hi:[1,0]
	v_pk_mul_f32 v[150:151], v[150:151], v[154:155]
	v_pk_mul_f32 v[214:215], v[216:217], v[214:215]
	v_pk_mul_f32 v[156:157], v[158:159], v[156:157]
	v_cvt_pk_bf16_f32 v214, v214, v215
	v_and_b32_e32 v154, 0xffff, v181
	v_cvt_pk_bf16_f32 v158, v156, v157
	v_cvt_pk_bf16_f32 v159, v150, v151
	v_pk_add_f32 v[150:151], v[152:153], v[192:193]
	v_lshrrev_b32_e32 v181, 16, v181
	v_pk_add_f32 v[150:151], v[150:151], v[194:195]
	v_pk_add_f32 v[150:151], v[150:151], v[188:189]
	v_and_or_b32 v188, v182, s95, v181
	v_lshrrev_b32_e32 v181, 16, v187
	v_lshl_or_b32 v154, v182, 16, v154
	v_perm_b32 v155, v211, v187, s100
	v_perm_b32 v156, v214, v220, s100
	v_perm_b32 v157, v159, v158, s100
	v_and_or_b32 v189, v211, s95, v181
	v_lshrrev_b32_e32 v181, 16, v220
	v_lshrrev_b32_e32 v158, 16, v158
	v_pk_add_f32 v[150:151], v[150:151], v[190:191]
	v_and_or_b32 v190, v214, s95, v181
	v_and_or_b32 v191, v159, s95, v158
	ds_write_b128 v171, v[154:157]
	ds_write_b128 v171, v[188:191] offset:64
	v_lshrrev_b32_e32 v158, 16, v173
	v_perm_b32 v154, v174, v173, s100
	v_and_or_b32 v174, v174, s95, v158
	v_lshrrev_b32_e32 v158, 16, v175
	v_and_b32_e32 v155, 0xffff, v175
	v_and_or_b32 v175, v176, s95, v158
	v_lshrrev_b32_e32 v158, 16, v177
	v_lshl_or_b32 v155, v176, 16, v155
	v_perm_b32 v156, v178, v177, s100
	s_waitcnt vmcnt(0)
	v_perm_b32 v157, v180, v179, s100
	v_and_or_b32 v176, v178, s95, v158
	v_lshrrev_b32_e32 v158, 16, v179
	v_and_or_b32 v177, v180, s95, v158
	ds_write_b128 v171, v[154:157] offset:16384
	ds_write_b128 v171, v[174:177] offset:16448
	s_cbranch_vccnz .LBB0_490
	s_mov_b64 s[20:21], 0

.LBB0_507:
	s_waitcnt vmcnt(23)
	v_lshlrev_b32_e32 v8, 16, v146
	v_mov_b32_e32 v93, v160
	v_mul_f32_e32 v8, v156, v8
	v_and_b32_e32 v9, 0xffff0000, v146
	v_mul_f32_e32 v9, v156, v9
	v_cvt_pk_bf16_f32 v12, v8, v9
	v_add_u32_e32 v8, s65, v163
	s_waitcnt vmcnt(21)
	ds_write2st64_b32 v8, v148, v146 offset1:64
	s_waitcnt vmcnt(20)
	v_lshlrev_b32_e32 v8, 16, v149
	v_mul_f32_e32 v8, v157, v8
	v_and_b32_e32 v9, 0xffff0000, v149
	v_mul_f32_e32 v9, v157, v9
	v_cvt_pk_bf16_f32 v13, v8, v9
	s_waitcnt vmcnt(17)
	v_lshlrev_b32_e32 v8, 16, v153
	v_mul_f32_e32 v8, v179, v8
	v_and_b32_e32 v9, 0xffff0000, v153
	ds_write2st64_b32 v125, v151, v149 offset1:64
	v_mul_f32_e32 v9, v179, v9
	v_cvt_pk_bf16_f32 v14, v8, v9
	s_waitcnt vmcnt(14)
	v_lshlrev_b32_e32 v8, 16, v182
	v_mul_f32_e32 v8, v180, v8
	v_and_b32_e32 v9, 0xffff0000, v182
	ds_write2st64_b32 v173, v155, v153 offset1:64
	v_mul_f32_e32 v9, v180, v9
	v_cvt_pk_bf16_f32 v15, v8, v9
	s_waitcnt vmcnt(11)
	v_lshlrev_b32_e32 v8, 16, v188
	v_mul_f32_e32 v8, v181, v8
	v_and_b32_e32 v9, 0xffff0000, v188
	ds_write2st64_b32 v174, v187, v182 offset1:64
	v_mul_f32_e32 v9, v181, v9
	v_cvt_pk_bf16_f32 v16, v8, v9
	s_waitcnt vmcnt(8)
	v_lshlrev_b32_e32 v8, 16, v191
	v_mul_f32_e32 v8, v183, v8
	v_and_b32_e32 v9, 0xffff0000, v191
	ds_write2st64_b32 v175, v190, v188 offset1:64
	v_mul_f32_e32 v9, v183, v9
	v_cvt_pk_bf16_f32 v17, v8, v9
	s_waitcnt vmcnt(5)
	v_lshlrev_b32_e32 v8, 16, v194
	v_mul_f32_e32 v8, v184, v8
	v_and_b32_e32 v9, 0xffff0000, v194
	ds_write2st64_b32 v176, v193, v191 offset1:64
	v_mul_f32_e32 v9, v184, v9
	v_cvt_pk_bf16_f32 v18, v8, v9
	s_waitcnt vmcnt(2)
	v_lshlrev_b32_e32 v8, 16, v212
	v_mul_f32_e32 v8, v186, v8
	v_and_b32_e32 v9, 0xffff0000, v212
	ds_write2st64_b32 v177, v211, v194 offset1:64
	v_mul_f32_e32 v9, v186, v9
	v_cvt_pk_bf16_f32 v19, v8, v9
	v_and_b32_e32 v8, 0xffff, v12
	v_lshl_or_b32 v8, v13, 16, v8
	v_perm_b32 v12, v13, v12, s101
	v_perm_b32 v9, v15, v14, s100
	v_perm_b32 v13, v15, v14, s101
	v_perm_b32 v10, v17, v16, s100
	v_perm_b32 v11, v19, v18, s100
	v_perm_b32 v14, v17, v16, s101
	v_perm_b32 v15, v19, v18, s101
	v_add_u32_e32 v16, v172, v171
	s_add_i32 s62, s35, -1
	s_waitcnt vmcnt(0)
	ds_write2st64_b32 v178, v214, v212 offset1:64
	ds_write_b128 v16, v[8:11] offset:32768
	ds_write_b128 v16, v[12:15] offset:32832
	v_perm_b32 v8, v150, v147, s100
	v_perm_b32 v9, v185, v154, s100
	v_perm_b32 v10, v192, v189, s100
	v_perm_b32 v11, v213, v195, s100
	v_perm_b32 v12, v150, v147, s101
	v_perm_b32 v13, v185, v154, s101
	v_perm_b32 v14, v192, v189, s101
	v_perm_b32 v15, v213, v195, s101
	s_cmp_gt_u32 s62, 2
	ds_write_b128 v16, v[8:11] offset:49152
	ds_write_b128 v16, v[12:15] offset:49216
	s_cbranch_scc1 .LBB0_509
	s_and_b64 vcc, s[20:21], exec
	s_cselect_b32 s55, s35, s87
	s_lshl_b32 s55, s55, 6
	s_add_i32 s63, s55, s3
	s_add_i32 s55, s63, s75
	v_mad_i64_i32 v[8:9], vcc, s55, v205, v[66:67]
	v_lshl_add_u64 v[10:11], v[8:9], 0, s[78:79]
	s_mov_b32 s55, s79
	s_mov_b32 s57, s79
	global_load_dword v146, v[10:11], off
	v_lshl_add_u64 v[10:11], v[8:9], 0, s[54:55]
	v_lshl_add_u64 v[8:9], v[8:9], 0, s[56:57]
	s_add_i32 vcc_lo, s63, s76
	global_load_dword v147, v[10:11], off
	global_load_dword v148, v[8:9], off
	v_mad_i64_i32 v[8:9], vcc, vcc_lo, v205, v[66:67]
	v_lshl_add_u64 v[10:11], v[8:9], 0, s[78:79]
	global_load_dword v149, v[10:11], off
	v_lshl_add_u64 v[10:11], v[8:9], 0, s[54:55]
	v_lshl_add_u64 v[8:9], v[8:9], 0, s[56:57]
	s_add_i32 vcc_lo, s63, s77
	global_load_dword v150, v[10:11], off
	global_load_dword v151, v[8:9], off
	v_mad_i64_i32 v[8:9], vcc, vcc_lo, v205, v[66:67]
	v_lshl_add_u64 v[10:11], v[8:9], 0, s[78:79]
	global_load_dword v153, v[10:11], off
	v_lshl_add_u64 v[10:11], v[8:9], 0, s[54:55]
	v_lshl_add_u64 v[8:9], v[8:9], 0, s[56:57]
	s_add_i32 vcc_lo, s63, s80
	global_load_dword v154, v[10:11], off
	global_load_dword v155, v[8:9], off
	v_mad_i64_i32 v[8:9], vcc, vcc_lo, v205, v[66:67]
	v_lshl_add_u64 v[10:11], v[8:9], 0, s[78:79]
	global_load_dword v182, v[10:11], off
	v_lshl_add_u64 v[10:11], v[8:9], 0, s[54:55]
	v_lshl_add_u64 v[8:9], v[8:9], 0, s[56:57]
	s_add_i32 vcc_lo, s63, s82
	global_load_dword v185, v[10:11], off
	global_load_dword v187, v[8:9], off
	v_mad_i64_i32 v[8:9], vcc, vcc_lo, v205, v[66:67]
	v_lshl_add_u64 v[10:11], v[8:9], 0, s[78:79]
	global_load_dword v188, v[10:11], off
	v_lshl_add_u64 v[10:11], v[8:9], 0, s[54:55]
	v_lshl_add_u64 v[8:9], v[8:9], 0, s[56:57]
	s_add_i32 vcc_lo, s63, s83
	global_load_dword v189, v[10:11], off
	global_load_dword v190, v[8:9], off
	v_mad_i64_i32 v[8:9], vcc, vcc_lo, v205, v[66:67]
	v_lshl_add_u64 v[10:11], v[8:9], 0, s[78:79]
	global_load_dword v191, v[10:11], off
	v_lshl_add_u64 v[10:11], v[8:9], 0, s[54:55]
	v_lshl_add_u64 v[8:9], v[8:9], 0, s[56:57]
	s_add_i32 vcc_lo, s63, s85
	global_load_dword v192, v[10:11], off
	global_load_dword v193, v[8:9], off
	v_mad_i64_i32 v[8:9], vcc, vcc_lo, v205, v[66:67]
	v_lshl_add_u64 v[10:11], v[8:9], 0, s[78:79]
	global_load_dword v194, v[10:11], off
	v_lshl_add_u64 v[10:11], v[8:9], 0, s[54:55]
	v_lshl_add_u64 v[8:9], v[8:9], 0, s[56:57]
	s_add_i32 s63, s63, s86
	global_load_dword v195, v[10:11], off
	global_load_dword v211, v[8:9], off
	v_mad_i64_i32 v[8:9], vcc, s63, v205, v[66:67]
	v_lshl_add_u64 v[10:11], v[8:9], 0, s[78:79]
	global_load_dword v212, v[10:11], off
	v_lshl_add_u64 v[10:11], v[8:9], 0, s[54:55]
	v_lshl_add_u64 v[8:9], v[8:9], 0, s[56:57]
	global_load_dword v213, v[10:11], off
	global_load_dword v214, v[8:9], off

.LBB0_531:
	s_waitcnt vmcnt(23)
	v_lshlrev_b32_e32 v32, 16, v143
	v_and_b32_e32 v33, 0xffff0000, v143
	v_pk_add_f32 v[34:35], v[32:33], 0 op_sel_hi:[1,0]
	s_waitcnt vmcnt(20)
	v_lshlrev_b32_e32 v36, 16, v181
	v_and_b32_e32 v37, 0xffff0000, v181
	v_pk_add_f32 v[38:39], v[34:35], v[36:37]
	s_waitcnt vmcnt(17)
	v_lshlrev_b32_e32 v40, 16, v184
	v_and_b32_e32 v41, 0xffff0000, v184
	v_pk_add_f32 v[42:43], v[38:39], v[40:41]
	s_waitcnt vmcnt(14)
	v_lshlrev_b32_e32 v44, 16, v187
	v_and_b32_e32 v45, 0xffff0000, v187
	v_pk_add_f32 v[46:47], v[42:43], v[44:45]
	s_waitcnt vmcnt(11)
	v_lshlrev_b32_e32 v48, 16, v190
	v_and_b32_e32 v49, 0xffff0000, v190
	v_pk_add_f32 v[50:51], v[46:47], v[48:49]
	s_waitcnt vmcnt(8)
	v_lshlrev_b32_e32 v26, 16, v193
	v_and_b32_e32 v27, 0xffff0000, v193
	v_pk_add_f32 v[28:29], v[50:51], v[26:27]
	s_waitcnt vmcnt(5)
	v_lshlrev_b32_e32 v22, 16, v211
	v_and_b32_e32 v23, 0xffff0000, v211
	v_pk_add_f32 v[24:25], v[28:29], v[22:23]
	s_waitcnt vmcnt(2)
	v_lshlrev_b32_e32 v18, 16, v214
	v_and_b32_e32 v19, 0xffff0000, v214
	v_mov_b32_e32 v217, v160
	v_pk_add_f32 v[20:21], v[24:25], v[18:19]
	v_add_u32_e32 v8, s29, v124
	ds_write_b64 v8, v[20:21]
	s_waitcnt lgkmcnt(0)
	s_barrier
	v_add_u32_e32 v52, s28, v124
	ds_read2st64_b64 v[8:11], v52 offset1:1
	ds_read2st64_b64 v[12:15], v52 offset0:2 offset1:3
	v_pk_mul_f32 v[32:33], v[32:33], s[94:95] op_sel_hi:[1,0]
	v_pk_mul_f32 v[26:27], v[26:27], s[94:95] op_sel_hi:[1,0]
	v_exp_f32_e32 v32, v32
	s_waitcnt lgkmcnt(1)
	v_pk_add_f32 v[8:9], v[8:9], 0 op_sel_hi:[1,0]
	v_exp_f32_e32 v33, v33
	v_cndmask_b32_e64 v17, 0, v9, s[4:5]
	v_cndmask_b32_e64 v16, 0, v8, s[4:5]
	v_pk_add_f32 v[30:31], v[10:11], v[16:17]
	v_pk_add_f32 v[8:9], v[8:9], v[10:11]
	v_cndmask_b32_e64 v17, v17, v31, s[6:7]
	v_cndmask_b32_e64 v16, v16, v30, s[6:7]
	s_waitcnt lgkmcnt(0)
	v_pk_add_f32 v[10:11], v[12:13], v[16:17]
	v_pk_add_f32 v[12:13], v[8:9], v[12:13]
	v_cndmask_b32_e64 v17, v17, v11, s[8:9]
	v_cndmask_b32_e64 v16, v16, v10, s[8:9]
	ds_read2st64_b64 v[8:11], v52 offset0:4 offset1:5
	v_pk_add_f32 v[30:31], v[14:15], v[16:17]
	v_pk_add_f32 v[32:33], v[32:33], 1.0 op_sel_hi:[1,0] neg_lo:[1,0] neg_hi:[1,0]
	v_cndmask_b32_e64 v31, v17, v31, s[10:11]
	v_cndmask_b32_e64 v30, v16, v30, s[10:11]
	v_pk_add_f32 v[16:17], v[12:13], v[14:15]
	ds_read2st64_b64 v[12:15], v52 offset0:6 offset1:7
	s_waitcnt lgkmcnt(1)
	v_pk_add_f32 v[52:53], v[8:9], v[30:31]
	v_exp_f32_e32 v26, v26
	v_cndmask_b32_e64 v31, v31, v53, s[12:13]
	v_cndmask_b32_e64 v30, v30, v52, s[12:13]
	v_pk_add_f32 v[52:53], v[10:11], v[30:31]
	v_exp_f32_e32 v27, v27
	v_cndmask_b32_e64 v31, v31, v53, s[14:15]
	v_cndmask_b32_e64 v30, v30, v52, s[14:15]
	s_waitcnt lgkmcnt(0)
	v_pk_add_f32 v[52:53], v[12:13], v[30:31]
	v_pk_add_f32 v[26:27], v[26:27], 1.0 op_sel_hi:[1,0] neg_lo:[1,0] neg_hi:[1,0]
	v_cndmask_b32_e64 v31, v31, v53, s[16:17]
	v_cndmask_b32_e64 v30, v30, v52, s[16:17]
	v_pk_add_f32 v[52:53], v[14:15], v[30:31]
	v_pk_mul_f32 v[22:23], v[22:23], s[94:95] op_sel_hi:[1,0]
	v_cndmask_b32_e64 v31, v31, v53, s[18:19]
	v_cndmask_b32_e64 v30, v30, v52, s[18:19]
	v_pk_add_f32 v[30:31], v[30:31], v[16:17] neg_lo:[0,1] neg_hi:[0,1]
	v_exp_f32_e32 v22, v22
	v_pk_mul_f32 v[30:31], v[30:31], s[94:95] op_sel_hi:[1,0]
	v_exp_f32_e32 v23, v23
	v_pk_fma_f32 v[34:35], v[34:35], s[94:95], v[30:31] op_sel_hi:[1,0,1]
	v_pk_fma_f32 v[28:29], v[28:29], s[94:95], v[30:31] op_sel_hi:[1,0,1]
	v_med3_f32 v52, v35, s81, v206
	v_med3_f32 v53, v34, s81, v206
	v_exp_f32_e64 v34, -v53
	v_exp_f32_e64 v35, -v52
	v_pk_fma_f32 v[24:25], v[24:25], s[94:95], v[30:31] op_sel_hi:[1,0,1]
	v_pk_add_f32 v[22:23], v[22:23], 1.0 op_sel_hi:[1,0] neg_lo:[1,0] neg_hi:[1,0]
	v_pk_fma_f32 v[20:21], v[20:21], s[94:95], v[30:31] op_sel_hi:[1,0,1]
	v_pk_mul_f32 v[32:33], v[32:33], v[34:35]
	v_exp_f32_e32 v34, v53
	v_exp_f32_e32 v35, v52
	v_cvt_pk_bf16_f32 v52, v32, v33
	v_lshlrev_b32_e32 v32, 16, v180
	v_and_b32_e32 v33, 0xffff0000, v180
	v_pk_mul_f32 v[32:33], v[34:35], v[32:33]
	v_pk_mul_f32 v[18:19], v[18:19], s[94:95] op_sel_hi:[1,0]
	v_cvt_pk_bf16_f32 v53, v32, v33
	v_pk_fma_f32 v[32:33], v[38:39], s[94:95], v[30:31] op_sel_hi:[1,0,1]
	v_exp_f32_e32 v18, v18
	v_med3_f32 v38, v33, s81, v206
	v_med3_f32 v39, v32, s81, v206
	v_pk_mul_f32 v[32:33], v[36:37], s[94:95] op_sel_hi:[1,0]
	v_exp_f32_e64 v34, -v39
	v_exp_f32_e32 v32, v32
	v_exp_f32_e32 v33, v33
	v_exp_f32_e64 v35, -v38
	v_add_u32_e32 v36, s65, v163
	ds_write2st64_b32 v36, v53, v52 offset1:64
	v_pk_add_f32 v[32:33], v[32:33], 1.0 op_sel_hi:[1,0] neg_lo:[1,0] neg_hi:[1,0]
	v_exp_f32_e32 v19, v19
	v_pk_mul_f32 v[32:33], v[32:33], v[34:35]
	v_exp_f32_e32 v34, v39
	v_exp_f32_e32 v35, v38
	v_cvt_pk_bf16_f32 v37, v32, v33
	v_lshlrev_b32_e32 v32, 16, v183
	v_and_b32_e32 v33, 0xffff0000, v183
	v_pk_mul_f32 v[32:33], v[34:35], v[32:33]
	v_pk_add_f32 v[18:19], v[18:19], 1.0 op_sel_hi:[1,0] neg_lo:[1,0] neg_hi:[1,0]
	v_cvt_pk_bf16_f32 v38, v32, v33
	v_pk_fma_f32 v[32:33], v[42:43], s[94:95], v[30:31] op_sel_hi:[1,0,1]
	v_add_u32_e32 v43, 0x80, v36
	v_med3_f32 v39, v33, s81, v206
	v_med3_f32 v42, v32, s81, v206
	v_pk_mul_f32 v[32:33], v[40:41], s[94:95] op_sel_hi:[1,0]
	v_exp_f32_e64 v34, -v42
	v_exp_f32_e32 v32, v32
	v_exp_f32_e32 v33, v33
	v_exp_f32_e64 v35, -v39
	v_add_u32_e32 v40, 64, v36
	ds_write2st64_b32 v40, v38, v37 offset1:64
	v_pk_add_f32 v[32:33], v[32:33], 1.0 op_sel_hi:[1,0] neg_lo:[1,0] neg_hi:[1,0]
	v_pk_add_f32 v[8:9], v[16:17], v[8:9]
	v_pk_mul_f32 v[32:33], v[32:33], v[34:35]
	v_exp_f32_e32 v34, v42
	v_exp_f32_e32 v35, v39
	v_cvt_pk_bf16_f32 v38, v32, v33
	v_lshlrev_b32_e32 v32, 16, v185
	v_and_b32_e32 v33, 0xffff0000, v185
	v_pk_mul_f32 v[32:33], v[34:35], v[32:33]
	v_pk_add_f32 v[8:9], v[8:9], v[10:11]
	v_cvt_pk_bf16_f32 v39, v32, v33
	v_pk_fma_f32 v[32:33], v[46:47], s[94:95], v[30:31] op_sel_hi:[1,0,1]
	ds_write2st64_b32 v43, v39, v38 offset1:64
	v_med3_f32 v41, v33, s81, v206
	v_med3_f32 v42, v32, s81, v206
	v_pk_mul_f32 v[32:33], v[44:45], s[94:95] op_sel_hi:[1,0]
	v_exp_f32_e64 v34, -v42
	v_exp_f32_e32 v32, v32
	v_exp_f32_e32 v33, v33
	v_exp_f32_e64 v35, -v41
	v_add_u32_e32 v45, 0xc0, v36
	v_pk_add_f32 v[8:9], v[8:9], v[12:13]
	v_pk_add_f32 v[32:33], v[32:33], 1.0 op_sel_hi:[1,0] neg_lo:[1,0] neg_hi:[1,0]
	v_pk_add_f32 v[132:133], v[8:9], v[14:15]
	v_pk_mul_f32 v[32:33], v[32:33], v[34:35]
	v_exp_f32_e32 v34, v42
	v_exp_f32_e32 v35, v41
	v_cvt_pk_bf16_f32 v39, v32, v33
	v_lshlrev_b32_e32 v32, 16, v189
	v_and_b32_e32 v33, 0xffff0000, v189
	v_pk_mul_f32 v[32:33], v[34:35], v[32:33]
	v_cvt_pk_bf16_f32 v41, v32, v33
	v_pk_fma_f32 v[32:33], v[50:51], s[94:95], v[30:31] op_sel_hi:[1,0,1]
	ds_write2st64_b32 v45, v41, v39 offset1:64
	v_med3_f32 v42, v33, s81, v206
	v_med3_f32 v44, v32, s81, v206
	v_pk_mul_f32 v[32:33], v[48:49], s[94:95] op_sel_hi:[1,0]
	v_exp_f32_e64 v34, -v44
	v_exp_f32_e32 v32, v32
	v_exp_f32_e32 v33, v33
	v_exp_f32_e64 v35, -v42
	v_perm_b32 v8, v37, v52, s100
	v_pk_add_f32 v[32:33], v[32:33], 1.0 op_sel_hi:[1,0] neg_lo:[1,0] neg_hi:[1,0]
	v_perm_b32 v9, v39, v38, s100
	v_pk_mul_f32 v[32:33], v[32:33], v[34:35]
	v_exp_f32_e32 v34, v44
	v_exp_f32_e32 v35, v42
	v_cvt_pk_bf16_f32 v41, v32, v33
	v_lshlrev_b32_e32 v32, 16, v192
	v_and_b32_e32 v33, 0xffff0000, v192
	v_pk_mul_f32 v[32:33], v[34:35], v[32:33]
	v_med3_f32 v34, v29, s81, v206
	v_med3_f32 v35, v28, s81, v206
	v_exp_f32_e64 v28, -v35
	v_exp_f32_e64 v29, -v34
	v_cvt_pk_bf16_f32 v32, v32, v33
	ds_write2st64_b32 v36, v32, v41 offset0:1 offset1:65
	v_pk_mul_f32 v[26:27], v[26:27], v[28:29]
	v_exp_f32_e32 v28, v35
	v_exp_f32_e32 v29, v34
	v_cvt_pk_bf16_f32 v32, v26, v27
	s_waitcnt vmcnt(0)
	v_lshlrev_b32_e32 v26, 16, v195
	v_and_b32_e32 v27, 0xffff0000, v195
	v_pk_mul_f32 v[26:27], v[28:29], v[26:27]
	v_med3_f32 v28, v25, s81, v206
	v_med3_f32 v29, v24, s81, v206
	v_exp_f32_e64 v24, -v29
	v_exp_f32_e64 v25, -v28
	v_cvt_pk_bf16_f32 v26, v26, v27
	ds_write2st64_b32 v40, v26, v32 offset0:1 offset1:65
	v_perm_b32 v10, v32, v41, s100
	v_pk_mul_f32 v[22:23], v[22:23], v[24:25]
	v_exp_f32_e32 v24, v29
	v_exp_f32_e32 v25, v28
	v_cvt_pk_bf16_f32 v26, v22, v23
	v_lshlrev_b32_e32 v22, 16, v213
	v_and_b32_e32 v23, 0xffff0000, v213
	v_pk_mul_f32 v[22:23], v[24:25], v[22:23]
	v_med3_f32 v24, v21, s81, v206
	v_med3_f32 v25, v20, s81, v206
	v_exp_f32_e64 v20, -v25
	v_exp_f32_e64 v21, -v24
	v_cvt_pk_bf16_f32 v22, v22, v23
	ds_write2st64_b32 v43, v22, v26 offset0:1 offset1:65
	v_pk_mul_f32 v[18:19], v[18:19], v[20:21]
	v_exp_f32_e32 v20, v25
	v_exp_f32_e32 v21, v24
	v_cvt_pk_bf16_f32 v22, v18, v19
	v_lshlrev_b32_e32 v18, 16, v216
	v_and_b32_e32 v19, 0xffff0000, v216
	v_pk_mul_f32 v[18:19], v[20:21], v[18:19]
	v_perm_b32 v11, v22, v26, s100
	v_cvt_pk_bf16_f32 v18, v18, v19
	ds_write2st64_b32 v45, v18, v22 offset0:1 offset1:65
	v_add_u32_e32 v18, v172, v171
	v_perm_b32 v12, v37, v52, s101
	v_perm_b32 v13, v39, v38, s101
	v_perm_b32 v14, v32, v41, s101
	v_perm_b32 v15, v22, v26, s101
	ds_write_b128 v18, v[8:11] offset:32768
	ds_write_b128 v18, v[12:15] offset:32832
	v_perm_b32 v8, v182, v179, s100
	v_perm_b32 v9, v188, v186, s100
	v_perm_b32 v10, v194, v191, s100
	v_perm_b32 v11, v215, v212, s100
	s_andn2_b64 vcc, exec, s[36:37]
	s_mov_b64 s[60:61], -1
	v_perm_b32 v12, v182, v179, s101
	v_perm_b32 v13, v188, v186, s101
	v_perm_b32 v14, v194, v191, s101
	v_perm_b32 v15, v215, v212, s101
	ds_write_b128 v18, v[8:11] offset:49152
	ds_write_b128 v18, v[12:15] offset:49216
	s_cbranch_vccnz .LBB0_549
	s_cbranch_execz .LBB0_550

.LBB0_556:
	s_and_b32 s24, s58, 63
	s_cmp_lg_u32 s24, 0
	v_readlane_b32 s26, v241, 10
	s_cselect_b64 s[20:21], -1, 0
	v_readlane_b32 s27, v241, 11
	s_or_b64 s[26:27], s[26:27], s[20:21]
	s_andn2_b64 vcc, exec, s[26:27]
	s_cbranch_vccnz .LBB0_555
	s_ashr_i32 s26, s58, 6
	s_and_b32 s25, s58, 64
	s_sub_i32 s27, 0x41, s24
	s_and_b64 s[20:21], s[20:21], exec
	s_cselect_b32 s20, s27, 0
	s_cmp_eq_u32 s25, 0
	s_cselect_b32 s24, s24, s20
	s_bitcmp0_b32 s58, 9
	v_add_u32_e32 v170, s53, v64
	s_mul_i32 s25, s26, 0x41
	s_cbranch_scc1 .LBB0_560
	s_bfe_u32 s61, s58, 0x10006
	s_bfe_u32 s21, s26, 0x20001
	s_lshl_b32 s26, s21, 2
	s_lshl_b32 s27, s61, 4
	s_or_b32 s26, s27, s26
	v_mov_b32_e32 v0, s26
	v_readlane_b32 s26, v241, 6
	v_readlane_b32 s27, v241, 7
	s_bfe_i32 s20, s58, 0x10006
	s_lshl_b32 s39, s24, 8
	s_and_b32 s20, s20, 0xc0
	s_lshl_b32 s63, s21, 8
	s_nop 0
	global_load_dword v0, v0, s[26:27]
	s_mov_b32 s26, 0xc2ce8ed0
	s_waitcnt vmcnt(0)
	v_mul_f32_e32 v1, 0x3fb8aa3b, v0
	v_fma_f32 v2, v0, s94, -v1
	v_rndne_f32_e32 v3, v1
	v_fmac_f32_e32 v2, 0x32a5705f, v0
	v_sub_f32_e32 v1, v1, v3
	v_add_f32_e32 v1, v1, v2
	v_exp_f32_e32 v1, v1
	v_cvt_i32_f32_e32 v2, v3
	v_cmp_ngt_f32_e32 vcc, s26, v0
	s_mov_b32 s26, 0x42b17218
	v_ldexp_f32 v1, v1, v2
	v_cndmask_b32_e32 v1, 0, v1, vcc
	v_cmp_nlt_f32_e32 vcc, s26, v0
	s_ashr_i32 s26, s58, 10
	s_mulk_i32 s26, 0x4100
	s_add_i32 s39, s39, s26
	s_or_b32 s62, s39, s20
	v_cndmask_b32_e32 v9, v204, v1, vcc
	s_cmp_eq_u32 s61, 0
	v_mul_f32_e32 v0, 0xc2800000, v9
	s_cselect_b32 s59, s2, s3
	v_mul_f32_e32 v0, 0x3fb8aa3b, v0
	s_cselect_b32 s38, s33, s40
	s_cselect_b32 s37, s41, s42
	s_cselect_b32 s36, s43, s44
	s_cselect_b32 s35, s45, s46
	s_cselect_b32 s34, s47, s48
	s_cselect_b32 s27, s49, s50
	s_cselect_b32 s26, s51, s52
	s_cselect_b32 s60, 0xc0, 0
	s_add_i32 s20, s62, s59
	v_exp_f32_e32 v8, v0
	v_mad_i64_i32 v[0:1], s[20:21], s20, v205, v[126:127]
	s_or_b32 s78, s63, 0x1800
	v_lshl_add_u64 v[2:3], v[0:1], 0, s[78:79]
	global_load_dword v3, v[2:3], off
	s_or_b32 s20, s63, 0x1c00
	s_add_i32 s63, s62, s38
	v_mad_i64_i32 v[4:5], s[64:65], s63, v205, v[126:127]
	v_lshl_add_u64 v[6:7], v[4:5], 0, s[78:79]
	global_load_dword v30, v[6:7], off
	s_mov_b32 s21, s79
	v_lshl_add_u64 v[0:1], v[0:1], 0, s[20:21]
	v_lshl_add_u64 v[4:5], v[4:5], 0, s[20:21]
	s_add_i32 s63, s62, s37
	global_load_dword v0, v[0:1], off
	s_lshl_b32 s61, s61, 6
	global_load_dword v1, v[4:5], off
	v_mad_i64_i32 v[4:5], s[64:65], s63, v205, v[126:127]
	v_lshl_add_u64 v[6:7], v[4:5], 0, s[78:79]
	global_load_dword v31, v[6:7], off
	v_lshl_add_u64 v[4:5], v[4:5], 0, s[20:21]
	s_add_i32 s63, s62, s36
	global_load_dword v2, v[4:5], off
	v_mad_i64_i32 v[4:5], s[64:65], s63, v205, v[126:127]
	v_lshl_add_u64 v[6:7], v[4:5], 0, s[78:79]
	global_load_dword v32, v[6:7], off
	v_lshl_add_u64 v[4:5], v[4:5], 0, s[20:21]
	s_add_i32 s63, s62, s35
	global_load_dword v14, v[4:5], off
	v_mad_i64_i32 v[4:5], s[64:65], s63, v205, v[126:127]
	v_lshl_add_u64 v[6:7], v[4:5], 0, s[78:79]
	global_load_dword v33, v[6:7], off
	v_lshl_add_u64 v[4:5], v[4:5], 0, s[20:21]
	s_add_i32 s63, s62, s34
	global_load_dword v21, v[4:5], off
	v_mad_i64_i32 v[4:5], s[64:65], s63, v205, v[126:127]
	v_lshl_add_u64 v[6:7], v[4:5], 0, s[78:79]
	global_load_dword v34, v[6:7], off
	v_lshl_add_u64 v[4:5], v[4:5], 0, s[20:21]
	s_add_i32 s63, s62, s27
	global_load_dword v23, v[4:5], off
	v_mad_i64_i32 v[4:5], s[64:65], s63, v205, v[126:127]
	v_lshl_add_u64 v[6:7], v[4:5], 0, s[78:79]
	v_lshl_add_u64 v[4:5], v[4:5], 0, s[20:21]
	s_add_i32 s62, s62, s26
	global_load_dword v35, v[6:7], off
	global_load_dword v28, v[4:5], off
	v_mad_i64_i32 v[4:5], s[62:63], s62, v205, v[126:127]
	s_or_b32 s62, s61, s39
	s_add_i32 s64, s62, 64
	v_lshl_add_u64 v[6:7], v[4:5], 0, s[78:79]
	v_lshl_add_u64 v[4:5], v[4:5], 0, s[20:21]
	s_add_i32 s62, s64, s59
	global_load_dword v36, v[6:7], off
	global_load_dword v37, v[4:5], off
	v_mad_i64_i32 v[4:5], s[62:63], s62, v205, v[126:127]
	v_lshl_add_u64 v[6:7], v[4:5], 0, s[78:79]
	v_lshl_add_u64 v[4:5], v[4:5], 0, s[20:21]
	s_add_i32 s62, s64, s38
	global_load_dword v16, v[6:7], off
	global_load_dword v10, v[4:5], off
	v_mad_i64_i32 v[4:5], s[62:63], s62, v205, v[126:127]
	v_lshl_add_u64 v[6:7], v[4:5], 0, s[78:79]
	v_lshl_add_u64 v[4:5], v[4:5], 0, s[20:21]
	s_add_i32 s62, s64, s37
	global_load_dword v18, v[6:7], off
	global_load_dword v11, v[4:5], off
	v_mad_i64_i32 v[4:5], s[62:63], s62, v205, v[126:127]
	v_lshl_add_u64 v[6:7], v[4:5], 0, s[78:79]
	v_lshl_add_u64 v[4:5], v[4:5], 0, s[20:21]
	s_add_i32 s62, s64, s36
	global_load_dword v20, v[6:7], off
	global_load_dword v12, v[4:5], off
	v_mad_i64_i32 v[4:5], s[62:63], s62, v205, v[126:127]
	v_lshl_add_u64 v[6:7], v[4:5], 0, s[78:79]
	v_lshl_add_u64 v[4:5], v[4:5], 0, s[20:21]
	s_add_i32 s62, s64, s35
	global_load_dword v22, v[6:7], off
	global_load_dword v13, v[4:5], off
	v_mad_i64_i32 v[4:5], s[62:63], s62, v205, v[126:127]
	v_lshl_add_u64 v[6:7], v[4:5], 0, s[78:79]
	v_lshl_add_u64 v[4:5], v[4:5], 0, s[20:21]
	s_add_i32 s62, s64, s34
	global_load_dword v25, v[6:7], off
	global_load_dword v15, v[4:5], off
	v_mad_i64_i32 v[4:5], s[62:63], s62, v205, v[126:127]
	v_lshl_add_u64 v[6:7], v[4:5], 0, s[78:79]
	v_lshl_add_u64 v[4:5], v[4:5], 0, s[20:21]
	s_add_i32 s62, s64, s27
	global_load_dword v26, v[6:7], off
	global_load_dword v17, v[4:5], off
	v_mad_i64_i32 v[4:5], s[62:63], s62, v205, v[126:127]
	v_lshl_add_u64 v[6:7], v[4:5], 0, s[78:79]
	v_lshl_add_u64 v[4:5], v[4:5], 0, s[20:21]
	s_add_i32 s64, s64, s26
	s_sub_i32 s61, s39, s61
	global_load_dword v27, v[6:7], off
	global_load_dword v19, v[4:5], off
	v_mad_i64_i32 v[4:5], s[62:63], s64, v205, v[126:127]
	s_addk_i32 s61, 0x80
	v_lshl_add_u64 v[6:7], v[4:5], 0, s[78:79]
	v_lshl_add_u64 v[4:5], v[4:5], 0, s[20:21]
	s_add_i32 s62, s61, s59
	global_load_dword v29, v[6:7], off
	global_load_dword v24, v[4:5], off
	v_mad_i64_i32 v[4:5], s[62:63], s62, v205, v[126:127]
	v_lshl_add_u64 v[6:7], v[4:5], 0, s[78:79]
	v_lshl_add_u64 v[4:5], v[4:5], 0, s[20:21]
	s_add_i32 s62, s61, s38
	global_load_dword v41, v[6:7], off
	s_nop 0
	global_load_dword v4, v[4:5], off
	v_mad_i64_i32 v[6:7], s[62:63], s62, v205, v[126:127]
	v_lshl_add_u64 v[38:39], v[6:7], 0, s[78:79]
	v_lshl_add_u64 v[6:7], v[6:7], 0, s[20:21]
	s_add_i32 s62, s61, s37
	global_load_dword v45, v[38:39], off
	global_load_dword v5, v[6:7], off
	v_mad_i64_i32 v[6:7], s[62:63], s62, v205, v[126:127]
	v_lshl_add_u64 v[38:39], v[6:7], 0, s[78:79]
	v_lshl_add_u64 v[6:7], v[6:7], 0, s[20:21]
	s_add_i32 s62, s61, s36
	global_load_dword v68, v[38:39], off
	s_nop 0
	global_load_dword v6, v[6:7], off
	v_mad_i64_i32 v[38:39], s[62:63], s62, v205, v[126:127]
	v_lshl_add_u64 v[42:43], v[38:39], 0, s[78:79]
	v_lshl_add_u64 v[38:39], v[38:39], 0, s[20:21]
	s_add_i32 s62, s61, s35
	global_load_dword v69, v[42:43], off
	global_load_dword v7, v[38:39], off
	v_mad_i64_i32 v[38:39], s[62:63], s62, v205, v[126:127]
	v_lshl_add_u64 v[42:43], v[38:39], 0, s[78:79]
	v_lshl_add_u64 v[38:39], v[38:39], 0, s[20:21]
	s_add_i32 s62, s61, s34
	global_load_dword v75, v[42:43], off
	global_load_dword v40, v[38:39], off
	v_mad_i64_i32 v[38:39], s[62:63], s62, v205, v[126:127]
	v_lshl_add_u64 v[42:43], v[38:39], 0, s[78:79]
	v_lshl_add_u64 v[38:39], v[38:39], 0, s[20:21]
	s_add_i32 s62, s61, s27
	global_load_dword v77, v[42:43], off
	global_load_dword v44, v[38:39], off
	v_mad_i64_i32 v[38:39], s[62:63], s62, v205, v[126:127]
	v_lshl_add_u64 v[42:43], v[38:39], 0, s[78:79]
	v_lshl_add_u64 v[38:39], v[38:39], 0, s[20:21]
	s_add_i32 s61, s61, s26
	global_load_dword v78, v[42:43], off
	global_load_dword v67, v[38:39], off
	v_mad_i64_i32 v[38:39], s[62:63], s61, v205, v[126:127]
	v_lshl_add_u64 v[42:43], v[38:39], 0, s[78:79]
	v_lshl_add_u64 v[38:39], v[38:39], 0, s[20:21]
	global_load_dword v79, v[42:43], off
	global_load_dword v74, v[38:39], off
	v_mul_f32_e64 v38, v162, -v9
	v_mul_f32_e32 v38, 0x3fb8aa3b, v38
	v_exp_f32_e32 v46, v38
	s_waitcnt vmcnt(47)
	v_lshlrev_b32_e32 v38, 16, v3
	v_and_b32_e32 v3, 0xffff0000, v3
	s_waitcnt lgkmcnt(0)
	v_mul_f32_e32 v38, v46, v38
	v_mul_f32_e32 v3, v46, v3
	s_barrier
	v_cvt_pk_bf16_f32 v3, v38, v3
	v_mul_f32_e64 v38, v163, -v9
	v_mul_f32_e32 v38, 0x3fb8aa3b, v38
	v_exp_f32_e32 v47, v38
	s_waitcnt vmcnt(46)
	v_lshlrev_b32_e32 v38, 16, v30
	v_and_b32_e32 v30, 0xffff0000, v30
	s_or_b32 s62, s39, s60
	v_mul_f32_e32 v38, v47, v38
	v_mul_f32_e32 v30, v47, v30
	v_cvt_pk_bf16_f32 v38, v38, v30
	v_mul_f32_e64 v30, v164, -v9
	v_mul_f32_e32 v30, 0x3fb8aa3b, v30
	v_exp_f32_e32 v48, v30
	s_waitcnt vmcnt(43)
	v_lshlrev_b32_e32 v30, 16, v31
	v_and_b32_e32 v31, 0xffff0000, v31
	s_add_i32 s39, s62, s59
	v_mul_f32_e32 v30, v48, v30
	v_mul_f32_e32 v31, v48, v31
	v_cvt_pk_bf16_f32 v39, v30, v31
	v_mul_f32_e64 v30, v165, -v9
	v_mul_f32_e32 v30, 0x3fb8aa3b, v30
	v_exp_f32_e32 v49, v30
	s_waitcnt vmcnt(41)
	v_lshlrev_b32_e32 v30, 16, v32
	v_and_b32_e32 v31, 0xffff0000, v32
	s_add_i32 s38, s62, s38
	v_mul_f32_e32 v30, v49, v30
	v_mul_f32_e32 v31, v49, v31
	v_cvt_pk_bf16_f32 v42, v30, v31
	v_mul_f32_e64 v30, v166, -v9
	v_mul_f32_e32 v30, 0x3fb8aa3b, v30
	v_exp_f32_e32 v50, v30
	s_waitcnt vmcnt(39)
	v_lshlrev_b32_e32 v30, 16, v33
	v_and_b32_e32 v31, 0xffff0000, v33
	s_add_i32 s37, s62, s37
	v_mul_f32_e32 v30, v50, v30
	v_mul_f32_e32 v31, v50, v31
	v_cvt_pk_bf16_f32 v43, v30, v31
	v_mul_f32_e64 v30, v167, -v9
	v_mul_f32_e32 v30, 0x3fb8aa3b, v30
	v_exp_f32_e32 v51, v30
	s_waitcnt vmcnt(37)
	v_lshlrev_b32_e32 v30, 16, v34
	v_and_b32_e32 v31, 0xffff0000, v34
	v_mul_f32_e32 v30, v51, v30
	v_mul_f32_e32 v31, v51, v31
	v_cvt_pk_bf16_f32 v34, v30, v31
	v_mul_f32_e64 v30, v168, -v9
	v_mul_f32_e32 v30, 0x3fb8aa3b, v30
	v_exp_f32_e32 v52, v30
	s_waitcnt vmcnt(35)
	v_lshlrev_b32_e32 v30, 16, v35
	v_and_b32_e32 v31, 0xffff0000, v35
	v_perm_b32 v32, v34, v43, s100
	v_mul_f32_e32 v30, v52, v30
	v_mul_f32_e32 v31, v52, v31
	v_cvt_pk_bf16_f32 v35, v30, v31
	v_mul_f32_e64 v30, v169, -v9
	v_mul_f32_e32 v30, 0x3fb8aa3b, v30
	v_exp_f32_e32 v53, v30
	s_waitcnt vmcnt(33)
	v_lshlrev_b32_e32 v30, 16, v36
	v_and_b32_e32 v31, 0xffff0000, v36
	v_mul_f32_e32 v30, v53, v30
	v_mul_f32_e32 v31, v53, v31
	v_cvt_pk_bf16_f32 v36, v30, v31
	v_and_b32_e32 v30, 0xffff, v3
	v_lshrrev_b32_e32 v3, 16, v3
	v_and_or_b32 v54, v38, s95, v3
	v_lshrrev_b32_e32 v3, 16, v39
	v_and_or_b32 v55, v42, s95, v3
	v_lshrrev_b32_e32 v3, 16, v43
	v_and_or_b32 v56, v34, s95, v3
	v_lshrrev_b32_e32 v3, 16, v35
	v_lshl_or_b32 v30, v38, 16, v30
	v_perm_b32 v31, v42, v39, s100
	v_perm_b32 v33, v36, v35, s100
	v_and_or_b32 v57, v36, s95, v3
	v_and_b32_e32 v3, 0xffff, v0
	ds_write_b128 v161, v[30:33] offset:32768
	ds_write_b128 v161, v[54:57] offset:32832
	v_lshl_or_b32 v30, v1, 16, v3
	v_and_b32_e32 v3, 0xffff, v2
	v_lshl_or_b32 v31, v14, 16, v3
	v_and_b32_e32 v3, 0xffff, v21
	v_lshl_or_b32 v32, v23, 16, v3
	v_and_b32_e32 v3, 0xffff, v28
	v_perm_b32 v0, v1, v0, s101
	s_waitcnt vmcnt(32)
	v_lshl_or_b32 v33, v37, 16, v3
	v_perm_b32 v1, v14, v2, s101
	v_perm_b32 v2, v23, v21, s101
	v_perm_b32 v3, v37, v28, s101
	ds_write_b128 v161, v[30:33] offset:49152
	ds_write_b128 v161, v[0:3] offset:49216
	v_mad_i64_i32 v[0:1], s[60:61], s39, v205, v[126:127]
	v_lshl_add_u64 v[2:3], v[0:1], 0, s[78:79]
	v_lshl_add_u64 v[0:1], v[0:1], 0, s[20:21]
	global_load_dword v59, v[2:3], off
	global_load_dword v54, v[0:1], off
	v_mad_i64_i32 v[0:1], s[38:39], s38, v205, v[126:127]
	v_lshl_add_u64 v[2:3], v[0:1], 0, s[78:79]
	v_lshl_add_u64 v[0:1], v[0:1], 0, s[20:21]
	global_load_dword v61, v[2:3], off
	global_load_dword v55, v[0:1], off
	v_mad_i64_i32 v[0:1], s[38:39], s37, v205, v[126:127]
	v_lshl_add_u64 v[2:3], v[0:1], 0, s[78:79]
	v_lshl_add_u64 v[0:1], v[0:1], 0, s[20:21]
	s_add_i32 s36, s62, s36
	global_load_dword v63, v[2:3], off
	global_load_dword v56, v[0:1], off
	v_mad_i64_i32 v[0:1], s[36:37], s36, v205, v[126:127]
	v_lshl_add_u64 v[2:3], v[0:1], 0, s[78:79]
	v_lshl_add_u64 v[0:1], v[0:1], 0, s[20:21]
	s_add_i32 s35, s62, s35
	global_load_dword v66, v[2:3], off
	global_load_dword v57, v[0:1], off
	v_mad_i64_i32 v[0:1], s[36:37], s35, v205, v[126:127]
	v_lshl_add_u64 v[2:3], v[0:1], 0, s[78:79]
	v_lshl_add_u64 v[0:1], v[0:1], 0, s[20:21]
	s_add_i32 s34, s62, s34
	global_load_dword v71, v[2:3], off
	global_load_dword v58, v[0:1], off
	v_mad_i64_i32 v[0:1], s[34:35], s34, v205, v[126:127]
	v_lshl_add_u64 v[2:3], v[0:1], 0, s[78:79]
	v_lshl_add_u64 v[0:1], v[0:1], 0, s[20:21]
	s_add_i32 s27, s62, s27
	global_load_dword v72, v[2:3], off
	global_load_dword v60, v[0:1], off
	v_mad_i64_i32 v[0:1], s[34:35], s27, v205, v[126:127]
	v_lshl_add_u64 v[2:3], v[0:1], 0, s[78:79]
	v_lshl_add_u64 v[0:1], v[0:1], 0, s[20:21]
	s_add_i32 s62, s62, s26
	global_load_dword v73, v[2:3], off
	global_load_dword v62, v[0:1], off
	v_mad_i64_i32 v[0:1], s[26:27], s62, v205, v[126:127]
	v_lshl_add_u64 v[2:3], v[0:1], 0, s[78:79]
	v_lshl_add_u64 v[0:1], v[0:1], 0, s[20:21]
	global_load_dword v76, v[2:3], off
	global_load_dword v70, v[0:1], off
	s_waitcnt lgkmcnt(0)
	s_barrier
	ds_read_b128 v[0:3], v170 offset:32768
	ds_read_b128 v[30:33], v170 offset:33792
	ds_read_b128 v[244:247], v160 offset:49152
	ds_read_b128 v[248:251], v160 offset:50176
	ds_read_b128 v[252:255], v160 offset:51200
	ds_read_b128 v[196:199], v160 offset:52224
	s_waitcnt lgkmcnt(3)
	v_mfma_f32_16x16x32_bf16 v[34:37], v[0:3], v[244:247], 0
	s_waitcnt vmcnt(47)
	v_lshlrev_b32_e32 v14, 16, v16
	v_and_b32_e32 v16, 0xffff0000, v16
	v_mul_f32_e32 v14, v46, v14
	s_waitcnt lgkmcnt(2)
	v_mfma_f32_16x16x32_bf16 v[34:37], v[30:33], v[248:251], v[34:37]
	ds_read_b128 v[244:247], v160 offset:53248
	ds_read_b128 v[248:251], v160 offset:54272
	v_mul_f32_e32 v16, v46, v16
	s_waitcnt vmcnt(41)
	v_and_b32_e32 v21, 0xffff0000, v22
	v_mul_f32_e32 v21, v49, v21
	s_add_i32 s20, s24, s25
	s_ashr_i32 s21, s20, 31
	s_nop 1
	v_pk_fma_f32 v[38:39], v[8:9], 0, v[34:35] op_sel_hi:[0,0,1]
	v_pk_fma_f32 v[42:43], v[8:9], 0, v[36:37] op_sel_hi:[0,0,1]
	s_waitcnt lgkmcnt(3)
	v_mfma_f32_16x16x32_bf16 v[34:37], v[0:3], v[252:255], 0
	s_lshl_b64 s[26:27], s[20:21], 15
	v_readlane_b32 s34, v242, 58
	s_add_u32 s26, s34, s26
	s_waitcnt lgkmcnt(2)
	v_mfma_f32_16x16x32_bf16 v[34:37], v[30:33], v[196:199], v[34:37]
	ds_read_b128 v[252:255], v160 offset:55296
	ds_read_b128 v[196:199], v160 offset:56320
	v_readlane_b32 s34, v242, 60
	s_addc_u32 s27, s34, s27
	s_mov_b64 s[34:35], 0
	s_and_b64 vcc, exec, s[28:29]
	s_nop 3
	v_pk_fma_f32 v[88:89], v[8:9], 0, v[34:35] op_sel_hi:[0,0,1]
	v_pk_fma_f32 v[90:91], v[8:9], 0, v[36:37] op_sel_hi:[0,0,1]
	s_waitcnt lgkmcnt(3)
	v_mfma_f32_16x16x32_bf16 v[34:37], v[0:3], v[244:247], 0
	s_waitcnt lgkmcnt(2)
	v_mfma_f32_16x16x32_bf16 v[34:37], v[30:33], v[248:251], v[34:37]
	ds_read_b128 v[244:247], v160 offset:57344
	ds_read_b128 v[248:251], v160 offset:58368
	s_nop 7
	v_pk_fma_f32 v[92:93], v[8:9], 0, v[34:35] op_sel_hi:[0,0,1]
	v_pk_fma_f32 v[94:95], v[8:9], 0, v[36:37] op_sel_hi:[0,0,1]
	s_waitcnt lgkmcnt(3)
	v_mfma_f32_16x16x32_bf16 v[34:37], v[0:3], v[252:255], 0
	s_waitcnt lgkmcnt(2)
	v_mfma_f32_16x16x32_bf16 v[34:37], v[30:33], v[196:199], v[34:37]
	ds_read_b128 v[252:255], v160 offset:59392
	ds_read_b128 v[196:199], v160 offset:60416
	s_nop 7
	v_pk_fma_f32 v[96:97], v[8:9], 0, v[34:35] op_sel_hi:[0,0,1]
	v_pk_fma_f32 v[98:99], v[8:9], 0, v[36:37] op_sel_hi:[0,0,1]
	s_waitcnt lgkmcnt(3)
	v_mfma_f32_16x16x32_bf16 v[34:37], v[0:3], v[244:247], 0
	s_waitcnt lgkmcnt(2)
	v_mfma_f32_16x16x32_bf16 v[34:37], v[30:33], v[248:251], v[34:37]
	ds_read_b128 v[244:247], v160 offset:61440
	ds_read_b128 v[248:251], v160 offset:62464
	s_nop 7
	v_pk_fma_f32 v[100:101], v[8:9], 0, v[34:35] op_sel_hi:[0,0,1]
	v_pk_fma_f32 v[102:103], v[8:9], 0, v[36:37] op_sel_hi:[0,0,1]
	s_waitcnt lgkmcnt(3)
	v_mfma_f32_16x16x32_bf16 v[34:37], v[0:3], v[252:255], 0
	s_waitcnt lgkmcnt(2)
	v_mfma_f32_16x16x32_bf16 v[34:37], v[30:33], v[196:199], v[34:37]
	ds_read_b128 v[252:255], v160 offset:63488
	ds_read_b128 v[196:199], v160 offset:64512
	s_nop 7
	v_pk_fma_f32 v[104:105], v[8:9], 0, v[34:35] op_sel_hi:[0,0,1]
	v_pk_fma_f32 v[106:107], v[8:9], 0, v[36:37] op_sel_hi:[0,0,1]
	s_waitcnt lgkmcnt(3)
	v_mfma_f32_16x16x32_bf16 v[34:37], v[0:3], v[244:247], 0
	s_waitcnt lgkmcnt(2)
	v_mfma_f32_16x16x32_bf16 v[34:37], v[30:33], v[248:251], v[34:37]
	s_nop 7
	v_pk_fma_f32 v[108:109], v[8:9], 0, v[34:35] op_sel_hi:[0,0,1]
	v_pk_fma_f32 v[110:111], v[8:9], 0, v[36:37] op_sel_hi:[0,0,1]
	v_cvt_pk_bf16_f32 v14, v14, v16
	v_lshlrev_b32_e32 v16, 16, v18
	v_and_b32_e32 v18, 0xffff0000, v18
	v_mul_f32_e32 v16, v47, v16
	v_mul_f32_e32 v18, v47, v18
	v_cvt_pk_bf16_f32 v16, v16, v18
	v_lshlrev_b32_e32 v18, 16, v20
	v_and_b32_e32 v20, 0xffff0000, v20
	v_mul_f32_e32 v18, v48, v18
	v_mul_f32_e32 v20, v48, v20
	v_cvt_pk_bf16_f32 v18, v18, v20
	v_lshlrev_b32_e32 v20, 16, v22
	v_mul_f32_e32 v20, v49, v20
	s_waitcnt lgkmcnt(1)
	v_mfma_f32_16x16x32_bf16 v[0:3], v[0:3], v[252:255], 0
	v_cvt_pk_bf16_f32 v28, v20, v21
	s_waitcnt vmcnt(39)
	v_lshlrev_b32_e32 v20, 16, v25
	v_mul_f32_e32 v20, v50, v20
	v_and_b32_e32 v21, 0xffff0000, v25
	v_mul_f32_e32 v21, v50, v21
	v_cvt_pk_bf16_f32 v25, v20, v21
	s_waitcnt vmcnt(37)
	v_lshlrev_b32_e32 v20, 16, v26
	v_mul_f32_e32 v20, v51, v20
	v_and_b32_e32 v21, 0xffff0000, v26
	s_waitcnt lgkmcnt(0)
	v_mfma_f32_16x16x32_bf16 v[0:3], v[30:33], v[196:199], v[0:3]
	v_mul_f32_e32 v21, v51, v21
	v_cvt_pk_bf16_f32 v30, v20, v21
	s_waitcnt vmcnt(35)
	v_lshlrev_b32_e32 v20, 16, v27
	v_mul_f32_e32 v20, v52, v20
	v_and_b32_e32 v21, 0xffff0000, v27
	v_mul_f32_e32 v21, v52, v21
	v_cvt_pk_bf16_f32 v31, v20, v21
	s_waitcnt vmcnt(33)
	v_lshlrev_b32_e32 v20, 16, v29
	v_mul_f32_e32 v20, v53, v20
	v_and_b32_e32 v21, 0xffff0000, v29
	v_mul_f32_e32 v21, v53, v21
	v_cvt_pk_bf16_f32 v29, v20, v21
	v_and_b32_e32 v20, 0xffff, v14
	v_lshrrev_b32_e32 v14, 16, v14
	v_and_or_b32 v26, v16, s95, v14
	v_lshrrev_b32_e32 v14, 16, v18
	v_and_or_b32 v27, v28, s95, v14
	v_lshrrev_b32_e32 v14, 16, v25
	v_perm_b32 v21, v28, v18, s100
	v_and_or_b32 v28, v30, s95, v14
	v_lshrrev_b32_e32 v14, 16, v31
	v_lshl_or_b32 v20, v16, 16, v20
	v_perm_b32 v22, v30, v25, s100
	v_perm_b32 v23, v29, v31, s100
	v_and_or_b32 v29, v29, s95, v14
	v_and_b32_e32 v14, 0xffff, v10
	ds_write_b128 v161, v[20:23]
	ds_write_b128 v161, v[26:29] offset:64
	v_lshl_or_b32 v20, v11, 16, v14
	v_and_b32_e32 v14, 0xffff, v12
	v_lshl_or_b32 v21, v13, 16, v14
	v_and_b32_e32 v14, 0xffff, v15
	v_lshl_or_b32 v22, v17, 16, v14
	v_and_b32_e32 v14, 0xffff, v19
	v_perm_b32 v10, v11, v10, s101
	s_waitcnt vmcnt(32)
	v_lshl_or_b32 v23, v24, 16, v14
	v_perm_b32 v11, v13, v12, s101
	v_perm_b32 v12, v17, v15, s101
	v_perm_b32 v13, v24, v19, s101
	ds_write_b128 v161, v[20:23] offset:16384
	ds_write_b128 v161, v[10:13] offset:16448
	s_waitcnt lgkmcnt(0)
	s_barrier
	ds_read_b128 v[80:83], v170
	ds_read_b128 v[84:87], v170 offset:1024
	ds_read_b128 v[244:247], v160 offset:16384
	ds_read_b128 v[248:251], v160 offset:17408
	ds_read_b128 v[252:255], v160 offset:18432
	ds_read_b128 v[196:199], v160 offset:19456
	s_waitcnt lgkmcnt(3)
	v_mfma_f32_16x16x32_bf16 v[10:13], v[80:83], v[244:247], 0
	v_fma_f32 v0, v8, 0, v0
	v_fma_f32 v1, v8, 0, v1
	v_pk_fma_f32 v[2:3], v[8:9], 0, v[2:3] op_sel_hi:[0,0,1]
	s_waitcnt lgkmcnt(2)
	v_mfma_f32_16x16x32_bf16 v[10:13], v[84:87], v[248:251], v[10:13]
	ds_read_b128 v[244:247], v160 offset:20480
	ds_read_b128 v[248:251], v160 offset:21504
	s_nop 7
	v_pk_fma_f32 v[26:27], v[8:9], v[42:43], v[12:13] op_sel_hi:[0,1,1]
	v_pk_fma_f32 v[14:15], v[8:9], v[38:39], v[10:11] op_sel_hi:[0,1,1]
	s_waitcnt lgkmcnt(3)
	v_mfma_f32_16x16x32_bf16 v[10:13], v[80:83], v[252:255], 0
	s_waitcnt lgkmcnt(2)
	v_mfma_f32_16x16x32_bf16 v[10:13], v[84:87], v[196:199], v[10:13]
	ds_read_b128 v[252:255], v160 offset:22528
	ds_read_b128 v[196:199], v160 offset:23552
	s_nop 7
	v_pk_fma_f32 v[28:29], v[8:9], v[90:91], v[12:13] op_sel_hi:[0,1,1]
	v_pk_fma_f32 v[16:17], v[8:9], v[88:89], v[10:11] op_sel_hi:[0,1,1]
	s_waitcnt lgkmcnt(3)
	v_mfma_f32_16x16x32_bf16 v[10:13], v[80:83], v[244:247], 0
	s_waitcnt lgkmcnt(2)
	v_mfma_f32_16x16x32_bf16 v[10:13], v[84:87], v[248:251], v[10:13]
	ds_read_b128 v[244:247], v160 offset:24576
	ds_read_b128 v[248:251], v160 offset:25600
	s_nop 7
	v_pk_fma_f32 v[30:31], v[8:9], v[94:95], v[12:13] op_sel_hi:[0,1,1]
	v_pk_fma_f32 v[18:19], v[8:9], v[92:93], v[10:11] op_sel_hi:[0,1,1]
	s_waitcnt lgkmcnt(3)
	v_mfma_f32_16x16x32_bf16 v[10:13], v[80:83], v[252:255], 0
	s_waitcnt lgkmcnt(2)
	v_mfma_f32_16x16x32_bf16 v[10:13], v[84:87], v[196:199], v[10:13]
	ds_read_b128 v[252:255], v160 offset:26624
	ds_read_b128 v[196:199], v160 offset:27648
	s_nop 7
	v_pk_fma_f32 v[32:33], v[8:9], v[98:99], v[12:13] op_sel_hi:[0,1,1]
	v_pk_fma_f32 v[20:21], v[8:9], v[96:97], v[10:11] op_sel_hi:[0,1,1]
	s_waitcnt lgkmcnt(3)
	v_mfma_f32_16x16x32_bf16 v[10:13], v[80:83], v[244:247], 0
	s_waitcnt lgkmcnt(2)
	v_mfma_f32_16x16x32_bf16 v[10:13], v[84:87], v[248:251], v[10:13]
	ds_read_b128 v[244:247], v160 offset:28672
	ds_read_b128 v[248:251], v160 offset:29696
	s_nop 7
	v_pk_fma_f32 v[34:35], v[8:9], v[102:103], v[12:13] op_sel_hi:[0,1,1]
	v_pk_fma_f32 v[22:23], v[8:9], v[100:101], v[10:11] op_sel_hi:[0,1,1]
	s_waitcnt lgkmcnt(3)
	v_mfma_f32_16x16x32_bf16 v[10:13], v[80:83], v[252:255], 0
	s_waitcnt lgkmcnt(2)
	v_mfma_f32_16x16x32_bf16 v[10:13], v[84:87], v[196:199], v[10:13]
	ds_read_b128 v[252:255], v160 offset:30720
	ds_read_b128 v[196:199], v160 offset:31744
	s_nop 7
	v_pk_fma_f32 v[36:37], v[8:9], v[106:107], v[12:13] op_sel_hi:[0,1,1]
	v_pk_fma_f32 v[24:25], v[8:9], v[104:105], v[10:11] op_sel_hi:[0,1,1]
	s_waitcnt lgkmcnt(3)
	v_mfma_f32_16x16x32_bf16 v[10:13], v[80:83], v[244:247], 0
	s_waitcnt lgkmcnt(2)
	v_mfma_f32_16x16x32_bf16 v[88:91], v[84:87], v[248:251], v[10:13]
	s_nop 7
	v_pk_fma_f32 v[10:11], v[8:9], v[110:111], v[90:91] op_sel_hi:[0,1,1]
	v_pk_fma_f32 v[12:13], v[8:9], v[108:109], v[88:89] op_sel_hi:[0,1,1]
	s_waitcnt lgkmcnt(1)
	v_mfma_f32_16x16x32_bf16 v[80:83], v[80:83], v[252:255], 0
	s_waitcnt lgkmcnt(0)
	v_mfma_f32_16x16x32_bf16 v[80:83], v[84:87], v[196:199], v[80:83]
	s_nop 7
	v_pk_fma_f32 v[42:43], v[8:9], v[0:1], v[80:81] op_sel_hi:[0,1,1]
	s_waitcnt vmcnt(31)
	v_lshlrev_b32_e32 v0, 16, v41
	v_mul_f32_e32 v0, v46, v0
	v_and_b32_e32 v1, 0xffff0000, v41
	v_mul_f32_e32 v1, v46, v1
	v_cvt_pk_bf16_f32 v41, v0, v1
	s_waitcnt vmcnt(29)
	v_lshlrev_b32_e32 v0, 16, v45
	v_mul_f32_e32 v0, v47, v0
	v_and_b32_e32 v1, 0xffff0000, v45
	v_mul_f32_e32 v1, v47, v1
	v_cvt_pk_bf16_f32 v45, v0, v1
	s_waitcnt vmcnt(27)
	v_lshlrev_b32_e32 v0, 16, v68
	v_mul_f32_e32 v0, v48, v0
	v_and_b32_e32 v1, 0xffff0000, v68
	v_mul_f32_e32 v1, v48, v1
	v_cvt_pk_bf16_f32 v68, v0, v1
	s_waitcnt vmcnt(25)
	v_lshlrev_b32_e32 v0, 16, v69
	v_mul_f32_e32 v0, v49, v0
	v_and_b32_e32 v1, 0xffff0000, v69
	v_mul_f32_e32 v1, v49, v1
	v_cvt_pk_bf16_f32 v69, v0, v1
	s_waitcnt vmcnt(23)
	v_lshlrev_b32_e32 v0, 16, v75
	v_mul_f32_e32 v0, v50, v0
	v_and_b32_e32 v1, 0xffff0000, v75
	v_mul_f32_e32 v1, v50, v1
	v_cvt_pk_bf16_f32 v75, v0, v1
	s_waitcnt vmcnt(21)
	v_lshlrev_b32_e32 v0, 16, v77
	v_mul_f32_e32 v0, v51, v0
	v_and_b32_e32 v1, 0xffff0000, v77
	v_mul_f32_e32 v1, v51, v1
	v_cvt_pk_bf16_f32 v77, v0, v1
	s_waitcnt vmcnt(19)
	v_lshlrev_b32_e32 v0, 16, v78
	v_mul_f32_e32 v0, v52, v0
	v_and_b32_e32 v1, 0xffff0000, v78
	v_mul_f32_e32 v1, v52, v1
	v_cvt_pk_bf16_f32 v81, v0, v1
	s_waitcnt vmcnt(17)
	v_lshlrev_b32_e32 v0, 16, v79
	v_mul_f32_e32 v0, v53, v0
	v_and_b32_e32 v1, 0xffff0000, v79
	v_pk_fma_f32 v[38:39], v[8:9], v[2:3], v[82:83] op_sel_hi:[0,1,1]
	v_mul_f32_e32 v1, v53, v1
	v_cvt_pk_bf16_f32 v82, v0, v1
	v_and_b32_e32 v0, 0xffff, v41
	v_lshrrev_b32_e32 v41, 16, v41
	v_and_or_b32 v78, v45, s95, v41
	v_lshrrev_b32_e32 v41, 16, v68
	v_and_or_b32 v79, v69, s95, v41
	v_lshrrev_b32_e32 v41, 16, v75
	v_lshl_or_b32 v0, v45, 16, v0
	v_perm_b32 v1, v69, v68, s100
	v_perm_b32 v2, v77, v75, s100
	v_perm_b32 v3, v82, v81, s100
	v_and_or_b32 v80, v77, s95, v41
	v_lshrrev_b32_e32 v41, 16, v81
	v_and_or_b32 v81, v82, s95, v41
	ds_write_b128 v161, v[0:3] offset:32768
	ds_write_b128 v161, v[78:81] offset:32832
	v_and_b32_e32 v0, 0xffff, v4
	v_lshl_or_b32 v0, v5, 16, v0
	v_perm_b32 v4, v5, v4, s101
	v_perm_b32 v1, v7, v6, s100
	v_perm_b32 v2, v44, v40, s100
	s_waitcnt vmcnt(16)
	v_perm_b32 v3, v74, v67, s100
	v_perm_b32 v5, v7, v6, s101
	v_perm_b32 v6, v44, v40, s101
	v_perm_b32 v7, v74, v67, s101
	ds_write_b128 v161, v[0:3] offset:49152
	ds_write_b128 v161, v[4:7] offset:49216
	s_waitcnt lgkmcnt(0)
	s_barrier
	ds_read_b128 v[0:3], v170 offset:32768
	ds_read_b128 v[4:7], v170 offset:33792
	ds_read_b128 v[244:247], v160 offset:49152
	ds_read_b128 v[248:251], v160 offset:50176
	ds_read_b128 v[252:255], v160 offset:51200
	ds_read_b128 v[196:199], v160 offset:52224
	s_waitcnt lgkmcnt(3)
	v_mfma_f32_16x16x32_bf16 v[78:81], v[0:3], v[244:247], 0
	s_waitcnt lgkmcnt(2)
	v_mfma_f32_16x16x32_bf16 v[78:81], v[4:7], v[248:251], v[78:81]
	ds_read_b128 v[244:247], v160 offset:53248
	ds_read_b128 v[248:251], v160 offset:54272
	s_nop 7
	v_pk_fma_f32 v[14:15], v[8:9], v[14:15], v[78:79] op_sel_hi:[0,1,1]
	v_pk_fma_f32 v[26:27], v[8:9], v[26:27], v[80:81] op_sel_hi:[0,1,1]
	s_waitcnt lgkmcnt(3)
	v_mfma_f32_16x16x32_bf16 v[78:81], v[0:3], v[252:255], 0
	s_waitcnt lgkmcnt(2)
	v_mfma_f32_16x16x32_bf16 v[78:81], v[4:7], v[196:199], v[78:81]
	ds_read_b128 v[252:255], v160 offset:55296
	ds_read_b128 v[196:199], v160 offset:56320
	s_nop 7
	v_pk_fma_f32 v[16:17], v[8:9], v[16:17], v[78:79] op_sel_hi:[0,1,1]
	v_pk_fma_f32 v[28:29], v[8:9], v[28:29], v[80:81] op_sel_hi:[0,1,1]
	s_waitcnt lgkmcnt(3)
	v_mfma_f32_16x16x32_bf16 v[78:81], v[0:3], v[244:247], 0
	s_waitcnt lgkmcnt(2)
	v_mfma_f32_16x16x32_bf16 v[78:81], v[4:7], v[248:251], v[78:81]
	ds_read_b128 v[244:247], v160 offset:57344
	ds_read_b128 v[248:251], v160 offset:58368
	s_nop 7
	v_pk_fma_f32 v[18:19], v[8:9], v[18:19], v[78:79] op_sel_hi:[0,1,1]
	v_pk_fma_f32 v[30:31], v[8:9], v[30:31], v[80:81] op_sel_hi:[0,1,1]
	s_waitcnt lgkmcnt(3)
	v_mfma_f32_16x16x32_bf16 v[78:81], v[0:3], v[252:255], 0
	s_waitcnt lgkmcnt(2)
	v_mfma_f32_16x16x32_bf16 v[78:81], v[4:7], v[196:199], v[78:81]
	ds_read_b128 v[252:255], v160 offset:59392
	ds_read_b128 v[196:199], v160 offset:60416
	s_nop 7
	v_pk_fma_f32 v[20:21], v[8:9], v[20:21], v[78:79] op_sel_hi:[0,1,1]
	v_pk_fma_f32 v[32:33], v[8:9], v[32:33], v[80:81] op_sel_hi:[0,1,1]
	s_waitcnt lgkmcnt(3)
	v_mfma_f32_16x16x32_bf16 v[78:81], v[0:3], v[244:247], 0
	s_waitcnt lgkmcnt(2)
	v_mfma_f32_16x16x32_bf16 v[78:81], v[4:7], v[248:251], v[78:81]
	ds_read_b128 v[244:247], v160 offset:61440
	ds_read_b128 v[248:251], v160 offset:62464
	s_nop 7
	v_pk_fma_f32 v[22:23], v[8:9], v[22:23], v[78:79] op_sel_hi:[0,1,1]
	v_pk_fma_f32 v[34:35], v[8:9], v[34:35], v[80:81] op_sel_hi:[0,1,1]
	s_waitcnt lgkmcnt(3)
	v_mfma_f32_16x16x32_bf16 v[78:81], v[0:3], v[252:255], 0
	s_waitcnt lgkmcnt(2)
	v_mfma_f32_16x16x32_bf16 v[78:81], v[4:7], v[196:199], v[78:81]
	ds_read_b128 v[252:255], v160 offset:63488
	ds_read_b128 v[196:199], v160 offset:64512
	s_nop 7
	v_pk_fma_f32 v[24:25], v[8:9], v[24:25], v[78:79] op_sel_hi:[0,1,1]
	v_pk_fma_f32 v[36:37], v[8:9], v[36:37], v[80:81] op_sel_hi:[0,1,1]
	s_waitcnt lgkmcnt(3)
	v_mfma_f32_16x16x32_bf16 v[78:81], v[0:3], v[244:247], 0
	s_waitcnt lgkmcnt(2)
	v_mfma_f32_16x16x32_bf16 v[78:81], v[4:7], v[248:251], v[78:81]
	s_nop 7
	v_pk_fma_f32 v[40:41], v[8:9], v[12:13], v[78:79] op_sel_hi:[0,1,1]
	v_pk_fma_f32 v[44:45], v[8:9], v[10:11], v[80:81] op_sel_hi:[0,1,1]
	s_waitcnt lgkmcnt(1)
	v_mfma_f32_16x16x32_bf16 v[0:3], v[0:3], v[252:255], 0
	s_waitcnt lgkmcnt(0)
	v_mfma_f32_16x16x32_bf16 v[0:3], v[4:7], v[196:199], v[0:3]
	s_nop 7
	v_pk_fma_f32 v[10:11], v[8:9], v[42:43], v[0:1] op_sel_hi:[0,1,1]
	s_waitcnt vmcnt(15)
	v_lshlrev_b32_e32 v0, 16, v59
	v_mul_f32_e32 v0, v46, v0
	v_and_b32_e32 v1, 0xffff0000, v59
	v_mul_f32_e32 v1, v46, v1
	v_cvt_pk_bf16_f32 v4, v0, v1
	s_waitcnt vmcnt(13)
	v_lshlrev_b32_e32 v0, 16, v61
	v_mul_f32_e32 v0, v47, v0
	v_and_b32_e32 v1, 0xffff0000, v61
	v_mul_f32_e32 v1, v47, v1
	v_cvt_pk_bf16_f32 v5, v0, v1
	s_waitcnt vmcnt(11)
	v_lshlrev_b32_e32 v0, 16, v63
	v_mul_f32_e32 v0, v48, v0
	v_and_b32_e32 v1, 0xffff0000, v63
	v_mul_f32_e32 v1, v48, v1
	v_cvt_pk_bf16_f32 v6, v0, v1
	s_waitcnt vmcnt(9)
	v_lshlrev_b32_e32 v0, 16, v66
	v_mul_f32_e32 v0, v49, v0
	v_and_b32_e32 v1, 0xffff0000, v66
	v_mul_f32_e32 v1, v49, v1
	v_cvt_pk_bf16_f32 v7, v0, v1
	s_waitcnt vmcnt(7)
	v_lshlrev_b32_e32 v0, 16, v71
	v_mul_f32_e32 v0, v50, v0
	v_and_b32_e32 v1, 0xffff0000, v71
	v_pk_fma_f32 v[12:13], v[8:9], v[38:39], v[2:3] op_sel_hi:[0,1,1]
	v_mul_f32_e32 v1, v50, v1
	v_cvt_pk_bf16_f32 v38, v0, v1
	s_waitcnt vmcnt(5)
	v_lshlrev_b32_e32 v0, 16, v72
	v_mul_f32_e32 v0, v51, v0
	v_and_b32_e32 v1, 0xffff0000, v72
	v_mul_f32_e32 v1, v51, v1
	v_cvt_pk_bf16_f32 v39, v0, v1
	s_waitcnt vmcnt(3)
	v_lshlrev_b32_e32 v0, 16, v73
	v_mul_f32_e32 v0, v52, v0
	v_and_b32_e32 v1, 0xffff0000, v73
	v_mul_f32_e32 v1, v52, v1
	v_cvt_pk_bf16_f32 v42, v0, v1
	s_waitcnt vmcnt(1)
	v_lshlrev_b32_e32 v0, 16, v76
	v_mul_f32_e32 v0, v53, v0
	v_and_b32_e32 v1, 0xffff0000, v76
	v_mul_f32_e32 v1, v53, v1
	v_cvt_pk_bf16_f32 v43, v0, v1
	v_and_b32_e32 v0, 0xffff, v4
	v_lshl_or_b32 v0, v5, 16, v0
	v_perm_b32 v4, v5, v4, s101
	v_perm_b32 v1, v7, v6, s100
	v_perm_b32 v2, v39, v38, s100
	v_perm_b32 v3, v43, v42, s100
	v_perm_b32 v5, v7, v6, s101
	v_perm_b32 v6, v39, v38, s101
	v_perm_b32 v7, v43, v42, s101
	ds_write_b128 v161, v[0:3]
	ds_write_b128 v161, v[4:7] offset:64
	v_perm_b32 v0, v55, v54, s100
	v_perm_b32 v1, v57, v56, s100
	v_perm_b32 v2, v60, v58, s100
	s_waitcnt vmcnt(0)
	v_perm_b32 v3, v70, v62, s100
	v_perm_b32 v4, v55, v54, s101
	v_perm_b32 v5, v57, v56, s101
	v_perm_b32 v6, v60, v58, s101
	v_perm_b32 v7, v70, v62, s101
	ds_write_b128 v161, v[0:3] offset:16384
	ds_write_b128 v161, v[4:7] offset:16448
	s_waitcnt lgkmcnt(0)
	s_barrier
	ds_read_b128 v[4:7], v170
	ds_read_b128 v[0:3], v170 offset:1024
	ds_read_b128 v[244:247], v160 offset:16384
	ds_read_b128 v[248:251], v160 offset:17408
	ds_read_b128 v[252:255], v160 offset:18432
	ds_read_b128 v[196:199], v160 offset:19456
	s_waitcnt lgkmcnt(3)
	v_mfma_f32_16x16x32_bf16 v[46:49], v[4:7], v[244:247], 0
	s_waitcnt lgkmcnt(2)
	v_mfma_f32_16x16x32_bf16 v[46:49], v[0:3], v[248:251], v[46:49]
	ds_read_b128 v[244:247], v160 offset:20480
	ds_read_b128 v[248:251], v160 offset:21504
	s_nop 7
	v_pk_fma_f32 v[26:27], v[8:9], v[26:27], v[48:49] op_sel_hi:[0,1,1]
	v_pk_fma_f32 v[14:15], v[8:9], v[14:15], v[46:47] op_sel_hi:[0,1,1]
	s_waitcnt lgkmcnt(3)
	v_mfma_f32_16x16x32_bf16 v[46:49], v[4:7], v[252:255], 0
	s_waitcnt lgkmcnt(2)
	v_mfma_f32_16x16x32_bf16 v[46:49], v[0:3], v[196:199], v[46:49]
	ds_read_b128 v[252:255], v160 offset:22528
	ds_read_b128 v[196:199], v160 offset:23552
	s_nop 7
	v_pk_fma_f32 v[28:29], v[8:9], v[28:29], v[48:49] op_sel_hi:[0,1,1]
	v_pk_fma_f32 v[16:17], v[8:9], v[16:17], v[46:47] op_sel_hi:[0,1,1]
	s_waitcnt lgkmcnt(3)
	v_mfma_f32_16x16x32_bf16 v[46:49], v[4:7], v[244:247], 0
	s_waitcnt lgkmcnt(2)
	v_mfma_f32_16x16x32_bf16 v[46:49], v[0:3], v[248:251], v[46:49]
	ds_read_b128 v[244:247], v160 offset:24576
	ds_read_b128 v[248:251], v160 offset:25600
	s_nop 7
	v_pk_fma_f32 v[38:39], v[8:9], v[30:31], v[48:49] op_sel_hi:[0,1,1]
	v_pk_fma_f32 v[42:43], v[8:9], v[18:19], v[46:47] op_sel_hi:[0,1,1]
	s_waitcnt lgkmcnt(3)
	v_mfma_f32_16x16x32_bf16 v[46:49], v[4:7], v[252:255], 0
	s_waitcnt lgkmcnt(2)
	v_mfma_f32_16x16x32_bf16 v[46:49], v[0:3], v[196:199], v[46:49]
	ds_read_b128 v[252:255], v160 offset:26624
	ds_read_b128 v[196:199], v160 offset:27648
	s_nop 7
	v_pk_fma_f32 v[48:49], v[8:9], v[32:33], v[48:49] op_sel_hi:[0,1,1]
	v_pk_fma_f32 v[46:47], v[8:9], v[20:21], v[46:47] op_sel_hi:[0,1,1]
	s_waitcnt lgkmcnt(3)
	v_mfma_f32_16x16x32_bf16 v[18:21], v[4:7], v[244:247], 0
	s_waitcnt lgkmcnt(2)
	v_mfma_f32_16x16x32_bf16 v[18:21], v[0:3], v[248:251], v[18:21]
	ds_read_b128 v[244:247], v160 offset:28672
	ds_read_b128 v[248:251], v160 offset:29696
	s_nop 7
	v_pk_fma_f32 v[34:35], v[8:9], v[34:35], v[20:21] op_sel_hi:[0,1,1]
	v_pk_fma_f32 v[50:51], v[8:9], v[22:23], v[18:19] op_sel_hi:[0,1,1]
	s_waitcnt lgkmcnt(3)
	v_mfma_f32_16x16x32_bf16 v[18:21], v[4:7], v[252:255], 0
	s_waitcnt lgkmcnt(2)
	v_mfma_f32_16x16x32_bf16 v[18:21], v[0:3], v[196:199], v[18:21]
	ds_read_b128 v[252:255], v160 offset:30720
	ds_read_b128 v[196:199], v160 offset:31744
	s_nop 7
	v_pk_fma_f32 v[30:31], v[8:9], v[36:37], v[20:21] op_sel_hi:[0,1,1]
	v_pk_fma_f32 v[32:33], v[8:9], v[24:25], v[18:19] op_sel_hi:[0,1,1]
	s_waitcnt lgkmcnt(3)
	v_mfma_f32_16x16x32_bf16 v[18:21], v[4:7], v[244:247], 0
	s_waitcnt lgkmcnt(2)
	v_mfma_f32_16x16x32_bf16 v[18:21], v[0:3], v[248:251], v[18:21]
	s_nop 7
	v_pk_fma_f32 v[36:37], v[8:9], v[44:45], v[20:21] op_sel_hi:[0,1,1]
	v_pk_fma_f32 v[40:41], v[8:9], v[40:41], v[18:19] op_sel_hi:[0,1,1]
	s_waitcnt lgkmcnt(1)
	v_mfma_f32_16x16x32_bf16 v[4:7], v[4:7], v[252:255], 0
	s_waitcnt lgkmcnt(0)
	v_mfma_f32_16x16x32_bf16 v[0:3], v[0:3], v[196:199], v[4:7]
	v_cvt_pk_bf16_f32 v4, v14, v15
	v_cvt_pk_bf16_f32 v5, v26, v27
	s_nop 5
	v_lshl_add_u64 v[6:7], s[26:27], 0, v[122:123]
	global_store_dwordx2 v[6:7], v[4:5], off
	v_lshl_add_u64 v[6:7], s[26:27], 0, v[128:129]
	v_cvt_pk_bf16_f32 v4, v16, v17
	v_cvt_pk_bf16_f32 v5, v28, v29
	global_store_dwordx2 v[6:7], v[4:5], off
	v_lshl_add_u64 v[6:7], s[26:27], 0, v[130:131]
	v_cvt_pk_bf16_f32 v4, v42, v43
	v_cvt_pk_bf16_f32 v5, v38, v39
	global_store_dwordx2 v[6:7], v[4:5], off
	v_lshl_add_u64 v[6:7], s[26:27], 0, v[132:133]
	v_cvt_pk_bf16_f32 v4, v46, v47
	v_cvt_pk_bf16_f32 v5, v48, v49
	global_store_dwordx2 v[6:7], v[4:5], off
	v_lshl_add_u64 v[6:7], s[26:27], 0, v[134:135]
	v_cvt_pk_bf16_f32 v4, v50, v51
	v_cvt_pk_bf16_f32 v5, v34, v35
	global_store_dwordx2 v[6:7], v[4:5], off
	v_lshl_add_u64 v[6:7], s[26:27], 0, v[136:137]
	v_pk_fma_f32 v[2:3], v[8:9], v[12:13], v[2:3] op_sel_hi:[0,1,1]
	v_pk_fma_f32 v[0:1], v[8:9], v[10:11], v[0:1] op_sel_hi:[0,1,1]
	v_cvt_pk_bf16_f32 v4, v32, v33
	v_cvt_pk_bf16_f32 v5, v30, v31
	global_store_dwordx2 v[6:7], v[4:5], off
	v_lshl_add_u64 v[6:7], s[26:27], 0, v[138:139]
	v_cvt_pk_bf16_f32 v4, v40, v41
	v_cvt_pk_bf16_f32 v5, v36, v37
	global_store_dwordx2 v[6:7], v[4:5], off
	v_cvt_pk_bf16_f32 v0, v0, v1
	v_cvt_pk_bf16_f32 v1, v2, v3
	v_lshl_add_u64 v[2:3], s[26:27], 0, v[140:141]
	s_mov_b64 s[26:27], 0
	global_store_dwordx2 v[2:3], v[0:1], off
	s_cbranch_vccz .LBB0_561
	v_mul_f32_e32 v0, 0xc3800000, v9
	v_mul_f32_e32 v0, 0x3fb8aa3b, v0
	v_exp_f32_e32 v0, v0
	s_mov_b64 s[26:27], -1
	v_mov_b32_e32 v1, v0
	s_branch .LBB0_561

.LBB0_561:
	s_and_b64 vcc, exec, s[34:35]
	s_cbranch_vccz .LBB0_580
	s_bfe_i32 s34, s58, 0x10006
	s_bfe_u32 s38, s58, 0x10006
	s_and_b32 s35, s58, 0x180
	s_lshl_b32 s67, s24, 8
	s_ashr_i32 s39, s58, 10
	s_cmp_eq_u32 s38, 0
	s_cselect_b64 s[36:37], -1, 0
	s_and_b64 s[20:21], s[36:37], exec
	s_movk_i32 s20, 0x400
	s_cselect_b32 s20, 0x200, s20
	s_mulk_i32 s39, 0x4100
	s_cselect_b32 s66, s2, s3
	s_cselect_b32 s65, s33, s40
	s_cselect_b32 s64, s41, s42
	s_cselect_b32 s63, s43, s44
	s_cselect_b32 s62, s45, s46
	s_cselect_b32 s61, s47, s48
	s_cselect_b32 s60, s49, s50
	s_cselect_b32 s59, s51, s52
	s_or_b32 s68, s20, s35
	s_add_i32 s67, s67, s39
	s_and_b32 s20, s34, 0xc0
	s_or_b32 s39, s67, s20
	s_add_i32 s20, s39, s66
	v_mad_i64_i32 v[0:1], s[20:21], s20, v205, v[126:127]
	s_add_i32 s20, s39, s65
	s_nop 0
	v_mad_i64_i32 v[4:5], s[20:21], s20, v205, v[126:127]
	s_add_i32 s20, s39, s64
	s_nop 0
	v_mad_i64_i32 v[8:9], s[20:21], s20, v205, v[126:127]
	s_add_i32 s20, s39, s63
	s_lshl_b32 s78, s68, 1
	s_lshl_b32 s34, s35, 1
	s_mov_b32 s35, s79
	v_mad_i64_i32 v[12:13], s[20:21], s20, v205, v[126:127]
	v_lshl_add_u64 v[2:3], v[0:1], 0, s[78:79]
	v_lshl_add_u64 v[0:1], v[0:1], 0, s[34:35]
	s_add_i32 s20, s39, s62
	v_lshl_add_u64 v[6:7], v[4:5], 0, s[78:79]
	v_lshl_add_u64 v[4:5], v[4:5], 0, s[34:35]
	v_lshl_add_u64 v[10:11], v[8:9], 0, s[78:79]
	v_lshl_add_u64 v[8:9], v[8:9], 0, s[34:35]
	v_lshl_add_u64 v[14:15], v[12:13], 0, s[78:79]
	v_lshl_add_u64 v[12:13], v[12:13], 0, s[34:35]
	global_load_dword v24, v[2:3], off
	global_load_dword v54, v[0:1], off offset:3072
	global_load_dword v25, v[6:7], off
	global_load_dword v55, v[4:5], off offset:3072
	global_load_dword v27, v[10:11], off
	global_load_dword v56, v[8:9], off offset:3072
	global_load_dword v31, v[14:15], off
	global_load_dword v57, v[12:13], off offset:3072
	v_mad_i64_i32 v[0:1], s[20:21], s20, v205, v[126:127]
	s_add_i32 s20, s39, s61
	s_nop 0
	v_mad_i64_i32 v[4:5], s[20:21], s20, v205, v[126:127]
	s_add_i32 s20, s39, s60
	s_add_i32 s39, s39, s59
	v_lshl_add_u64 v[2:3], v[0:1], 0, s[78:79]
	v_mad_i64_i32 v[8:9], s[20:21], s20, v205, v[126:127]
	v_mad_i64_i32 v[12:13], s[20:21], s39, v205, v[126:127]
	v_lshl_add_u64 v[0:1], v[0:1], 0, s[34:35]
	v_lshl_add_u64 v[6:7], v[4:5], 0, s[78:79]
	v_lshl_add_u64 v[4:5], v[4:5], 0, s[34:35]
	v_lshl_add_u64 v[10:11], v[8:9], 0, s[78:79]
	v_lshl_add_u64 v[8:9], v[8:9], 0, s[34:35]
	v_lshl_add_u64 v[14:15], v[12:13], 0, s[78:79]
	v_lshl_add_u64 v[12:13], v[12:13], 0, s[34:35]
	global_load_dword v35, v[2:3], off
	global_load_dword v58, v[0:1], off offset:3072
	global_load_dword v39, v[6:7], off
	global_load_dword v59, v[4:5], off offset:3072
	global_load_dword v43, v[10:11], off
	global_load_dword v60, v[8:9], off offset:3072
	global_load_dword v47, v[14:15], off
	global_load_dword v61, v[12:13], off offset:3072
	s_lshl_b32 s38, s38, 6
	s_or_b32 s20, s38, s67
	s_add_i32 s39, s20, 64
	s_add_i32 s20, s39, s66
	v_mad_i64_i32 v[0:1], s[20:21], s20, v205, v[126:127]
	s_add_i32 s20, s39, s65
	s_nop 0
	v_mad_i64_i32 v[4:5], s[20:21], s20, v205, v[126:127]
	s_add_i32 s20, s39, s64
	v_lshl_add_u64 v[6:7], v[4:5], 0, s[78:79]
	v_lshl_add_u64 v[8:9], v[4:5], 0, s[34:35]
	v_mad_i64_i32 v[4:5], s[20:21], s20, v205, v[126:127]
	s_add_i32 s20, s39, s63
	v_lshl_add_u64 v[10:11], v[4:5], 0, s[78:79]
	v_lshl_add_u64 v[12:13], v[4:5], 0, s[34:35]
	v_mad_i64_i32 v[4:5], s[20:21], s20, v205, v[126:127]
	v_lshl_add_u64 v[2:3], v[0:1], 0, s[78:79]
	v_lshl_add_u64 v[0:1], v[0:1], 0, s[34:35]
	s_add_i32 s20, s39, s62
	v_lshl_add_u64 v[14:15], v[4:5], 0, s[78:79]
	v_lshl_add_u64 v[16:17], v[4:5], 0, s[34:35]
	global_load_dword v5, v[2:3], off
	global_load_dword v90, v[0:1], off offset:3072
	global_load_dword v4, v[6:7], off
	global_load_dword v107, v[8:9], off offset:3072
	s_nop 0
	global_load_dword v3, v[10:11], off
	global_load_dword v108, v[12:13], off offset:3072
	global_load_dword v2, v[14:15], off
	global_load_dword v110, v[16:17], off offset:3072
	v_mad_i64_i32 v[0:1], s[20:21], s20, v205, v[126:127]
	s_add_i32 s20, s39, s61
	s_nop 0
	v_mad_i64_i32 v[8:9], s[20:21], s20, v205, v[126:127]
	s_add_i32 s20, s39, s60
	v_lshl_add_u64 v[10:11], v[8:9], 0, s[78:79]
	v_lshl_add_u64 v[12:13], v[8:9], 0, s[34:35]
	v_mad_i64_i32 v[8:9], s[20:21], s20, v205, v[126:127]
	s_add_i32 s39, s39, s59
	v_lshl_add_u64 v[14:15], v[8:9], 0, s[78:79]
	v_lshl_add_u64 v[16:17], v[8:9], 0, s[34:35]
	v_mad_i64_i32 v[8:9], s[20:21], s39, v205, v[126:127]
	s_sub_i32 s20, s67, s38
	s_add_i32 s38, s20, 0x80
	v_lshl_add_u64 v[6:7], v[0:1], 0, s[78:79]
	v_lshl_add_u64 v[0:1], v[0:1], 0, s[34:35]
	s_add_i32 s20, s38, s66
	v_lshl_add_u64 v[18:19], v[8:9], 0, s[78:79]
	v_lshl_add_u64 v[20:21], v[8:9], 0, s[34:35]
	global_load_dword v9, v[6:7], off
	global_load_dword v113, v[0:1], off offset:3072
	global_load_dword v8, v[10:11], off
	global_load_dword v114, v[12:13], off offset:3072
	s_nop 0
	global_load_dword v7, v[14:15], off
	global_load_dword v115, v[16:17], off offset:3072
	global_load_dword v6, v[18:19], off
	global_load_dword v116, v[20:21], off offset:3072
	v_mad_i64_i32 v[0:1], s[20:21], s20, v205, v[126:127]
	s_add_i32 s20, s38, s65
	s_nop 0
	v_mad_i64_i32 v[12:13], s[20:21], s20, v205, v[126:127]
	s_add_i32 s20, s38, s64
	s_nop 0
	v_mad_i64_i32 v[16:17], s[20:21], s20, v205, v[126:127]
	s_add_i32 s20, s38, s63
	s_nop 0
	v_mad_i64_i32 v[20:21], s[20:21], s20, v205, v[126:127]
	v_lshl_add_u64 v[10:11], v[0:1], 0, s[78:79]
	v_lshl_add_u64 v[0:1], v[0:1], 0, s[34:35]
	s_add_i32 s20, s38, s62
	v_lshl_add_u64 v[14:15], v[12:13], 0, s[78:79]
	v_lshl_add_u64 v[12:13], v[12:13], 0, s[34:35]
	v_lshl_add_u64 v[18:19], v[16:17], 0, s[78:79]
	v_lshl_add_u64 v[16:17], v[16:17], 0, s[34:35]
	v_lshl_add_u64 v[22:23], v[20:21], 0, s[78:79]
	v_lshl_add_u64 v[20:21], v[20:21], 0, s[34:35]
	global_load_dword v89, v[10:11], off
	global_load_dword v92, v[0:1], off offset:3072
	global_load_dword v88, v[14:15], off
	global_load_dword v93, v[12:13], off offset:3072
	global_load_dword v87, v[18:19], off
	global_load_dword v94, v[16:17], off offset:3072
	global_load_dword v86, v[22:23], off
	global_load_dword v95, v[20:21], off offset:3072
	v_mad_i64_i32 v[0:1], s[20:21], s20, v205, v[126:127]
	s_add_i32 s20, s38, s61
	s_nop 0
	v_mad_i64_i32 v[12:13], s[20:21], s20, v205, v[126:127]
	s_add_i32 s20, s38, s60
	s_nop 0
	v_mad_i64_i32 v[16:17], s[20:21], s20, v205, v[126:127]
	s_add_i32 s38, s38, s59
	v_lshl_add_u64 v[10:11], v[0:1], 0, s[78:79]
	v_lshl_add_u64 v[18:19], v[16:17], 0, s[78:79]
	v_mad_i64_i32 v[20:21], s[20:21], s38, v205, v[126:127]
	v_lshl_add_u64 v[0:1], v[0:1], 0, s[34:35]
	v_lshl_add_u64 v[14:15], v[12:13], 0, s[78:79]
	v_lshl_add_u64 v[12:13], v[12:13], 0, s[34:35]
	v_lshl_add_u64 v[16:17], v[16:17], 0, s[34:35]
	v_lshl_add_u64 v[22:23], v[20:21], 0, s[78:79]
	v_lshl_add_u64 v[20:21], v[20:21], 0, s[34:35]
	global_load_dword v111, v[10:11], off
	global_load_dword v96, v[0:1], off offset:3072
	global_load_dword v106, v[14:15], off
	global_load_dword v97, v[12:13], off offset:3072
	global_load_dword v91, v[18:19], off
	global_load_dword v98, v[16:17], off offset:3072
	global_load_dword v104, v[22:23], off
	global_load_dword v99, v[20:21], off offset:3072
	s_waitcnt vmcnt(47)
	v_lshlrev_b32_e32 v18, 16, v24
	v_and_b32_e32 v19, 0xffff0000, v24
	v_pk_add_f32 v[20:21], v[18:19], 0 op_sel_hi:[1,0]
	s_waitcnt vmcnt(45)
	v_lshlrev_b32_e32 v22, 16, v25
	v_and_b32_e32 v23, 0xffff0000, v25
	v_pk_add_f32 v[24:25], v[20:21], v[22:23]
	s_waitcnt vmcnt(43)
	v_lshlrev_b32_e32 v26, 16, v27
	v_and_b32_e32 v27, 0xffff0000, v27
	v_pk_add_f32 v[28:29], v[24:25], v[26:27]
	s_waitcnt vmcnt(41)
	v_lshlrev_b32_e32 v30, 16, v31
	v_and_b32_e32 v31, 0xffff0000, v31
	v_pk_add_f32 v[32:33], v[28:29], v[30:31]
	s_waitcnt vmcnt(39)
	v_lshlrev_b32_e32 v34, 16, v35
	v_and_b32_e32 v35, 0xffff0000, v35
	v_pk_add_f32 v[36:37], v[32:33], v[34:35]
	s_waitcnt vmcnt(37)
	v_lshlrev_b32_e32 v38, 16, v39
	v_and_b32_e32 v39, 0xffff0000, v39
	v_pk_add_f32 v[40:41], v[36:37], v[38:39]
	s_waitcnt vmcnt(35)
	v_lshlrev_b32_e32 v42, 16, v43
	v_and_b32_e32 v43, 0xffff0000, v43
	v_pk_add_f32 v[44:45], v[40:41], v[42:43]
	s_waitcnt vmcnt(33)
	v_lshlrev_b32_e32 v46, 16, v47
	v_and_b32_e32 v47, 0xffff0000, v47
	v_pk_add_f32 v[48:49], v[44:45], v[46:47]
	v_add_u32_e32 v117, s55, v124
	ds_write_b64 v117, v[48:49]
	s_waitcnt lgkmcnt(0)
	s_barrier
	v_add_u32_e32 v100, s54, v124
	ds_read2st64_b64 v[10:13], v100 offset1:1
	ds_read2st64_b64 v[14:17], v100 offset0:2 offset1:3
	v_pk_mul_f32 v[18:19], v[18:19], s[94:95] op_sel_hi:[1,0]
	s_mov_b32 s20, 0x42f00000
	v_exp_f32_e32 v18, v18
	s_waitcnt lgkmcnt(1)
	v_pk_add_f32 v[0:1], v[10:11], 0 op_sel_hi:[1,0]
	v_exp_f32_e32 v19, v19
	v_cndmask_b32_e64 v11, 0, v1, s[4:5]
	v_cndmask_b32_e64 v10, 0, v0, s[4:5]
	v_pk_add_f32 v[50:51], v[12:13], v[10:11]
	v_pk_add_f32 v[0:1], v[0:1], v[12:13]
	v_cndmask_b32_e64 v11, v11, v51, s[6:7]
	v_cndmask_b32_e64 v10, v10, v50, s[6:7]
	s_waitcnt lgkmcnt(0)
	v_pk_add_f32 v[12:13], v[14:15], v[10:11]
	v_pk_add_f32 v[0:1], v[0:1], v[14:15]
	v_cndmask_b32_e64 v51, v11, v13, s[8:9]
	v_cndmask_b32_e64 v50, v10, v12, s[8:9]
	ds_read2st64_b64 v[10:13], v100 offset0:4 offset1:5
	v_pk_add_f32 v[14:15], v[16:17], v[50:51]
	v_pk_add_f32 v[0:1], v[0:1], v[16:17]
	v_cndmask_b32_e64 v51, v51, v15, s[10:11]
	v_cndmask_b32_e64 v50, v50, v14, s[10:11]
	ds_read2st64_b64 v[14:17], v100 offset0:6 offset1:7
	s_waitcnt lgkmcnt(1)
	v_pk_add_f32 v[52:53], v[10:11], v[50:51]
	v_pk_add_f32 v[18:19], v[18:19], 1.0 op_sel_hi:[1,0] neg_lo:[1,0] neg_hi:[1,0]
	v_cndmask_b32_e64 v51, v51, v53, s[12:13]
	v_cndmask_b32_e64 v50, v50, v52, s[12:13]
	v_pk_add_f32 v[52:53], v[12:13], v[50:51]
	v_pk_mul_f32 v[22:23], v[22:23], s[94:95] op_sel_hi:[1,0]
	v_cndmask_b32_e64 v51, v51, v53, s[14:15]
	v_cndmask_b32_e64 v50, v50, v52, s[14:15]
	s_waitcnt lgkmcnt(0)
	v_pk_add_f32 v[52:53], v[14:15], v[50:51]
	v_exp_f32_e32 v22, v22
	v_cndmask_b32_e64 v51, v51, v53, s[16:17]
	v_cndmask_b32_e64 v50, v50, v52, s[16:17]
	v_pk_add_f32 v[52:53], v[16:17], v[50:51]
	v_exp_f32_e32 v23, v23
	v_cndmask_b32_e64 v51, v51, v53, s[18:19]
	v_cndmask_b32_e64 v50, v50, v52, s[18:19]
	v_pk_add_f32 v[50:51], v[50:51], v[0:1] neg_lo:[0,1] neg_hi:[0,1]
	v_pk_add_f32 v[10:11], v[0:1], v[10:11]
	v_pk_mul_f32 v[50:51], v[50:51], s[94:95] op_sel_hi:[1,0]
	v_pk_add_f32 v[10:11], v[10:11], v[12:13]
	v_pk_fma_f32 v[20:21], v[20:21], s[94:95], v[50:51] op_sel_hi:[1,0,1]
	v_pk_add_f32 v[10:11], v[10:11], v[14:15]
	v_med3_f32 v20, -v20, s20, v207
	v_med3_f32 v21, -v21, s20, v207
	v_exp_f32_e32 v20, v20
	v_exp_f32_e32 v21, v21
	v_pk_add_f32 v[144:145], v[10:11], v[16:17]
	s_andn2_b64 vcc, exec, s[30:31]
	s_mov_b64 s[38:39], -1
	v_pk_mul_f32 v[18:19], v[18:19], v[20:21]
	v_pk_add_f32 v[20:21], v[22:23], 1.0 op_sel_hi:[1,0] neg_lo:[1,0] neg_hi:[1,0]
	v_cvt_pk_bf16_f32 v52, v18, v19
	v_pk_fma_f32 v[18:19], v[24:25], s[94:95], v[50:51] op_sel_hi:[1,0,1]
	v_pk_mul_f32 v[22:23], v[26:27], s[94:95] op_sel_hi:[1,0]
	v_med3_f32 v18, -v18, s20, v207
	v_med3_f32 v19, -v19, s20, v207
	v_exp_f32_e32 v18, v18
	v_exp_f32_e32 v19, v19
	v_exp_f32_e32 v22, v22
	v_exp_f32_e32 v23, v23
	v_pk_mul_f32 v[24:25], v[46:47], s[94:95] op_sel_hi:[1,0]
	v_pk_mul_f32 v[18:19], v[20:21], v[18:19]
	v_exp_f32_e32 v24, v24
	v_cvt_pk_bf16_f32 v26, v18, v19
	v_pk_fma_f32 v[18:19], v[28:29], s[94:95], v[50:51] op_sel_hi:[1,0,1]
	v_pk_add_f32 v[20:21], v[22:23], 1.0 op_sel_hi:[1,0] neg_lo:[1,0] neg_hi:[1,0]
	v_med3_f32 v18, -v18, s20, v207
	v_med3_f32 v19, -v19, s20, v207
	v_exp_f32_e32 v18, v18
	v_exp_f32_e32 v19, v19
	v_pk_mul_f32 v[22:23], v[30:31], s[94:95] op_sel_hi:[1,0]
	v_exp_f32_e32 v25, v25
	v_exp_f32_e32 v22, v22
	v_pk_mul_f32 v[18:19], v[20:21], v[18:19]
	v_exp_f32_e32 v23, v23
	v_cvt_pk_bf16_f32 v27, v18, v19
	v_pk_fma_f32 v[18:19], v[32:33], s[94:95], v[50:51] op_sel_hi:[1,0,1]
	v_med3_f32 v18, -v18, s20, v207
	v_med3_f32 v19, -v19, s20, v207
	v_exp_f32_e32 v18, v18
	v_exp_f32_e32 v19, v19
	v_pk_add_f32 v[20:21], v[22:23], 1.0 op_sel_hi:[1,0] neg_lo:[1,0] neg_hi:[1,0]
	v_pk_mul_f32 v[22:23], v[34:35], s[94:95] op_sel_hi:[1,0]
	v_pk_mul_f32 v[18:19], v[20:21], v[18:19]
	v_exp_f32_e32 v22, v22
	v_cvt_pk_bf16_f32 v28, v18, v19
	v_pk_fma_f32 v[18:19], v[36:37], s[94:95], v[50:51] op_sel_hi:[1,0,1]
	v_exp_f32_e32 v23, v23
	v_med3_f32 v18, -v18, s20, v207
	v_med3_f32 v19, -v19, s20, v207
	v_exp_f32_e32 v18, v18
	v_exp_f32_e32 v19, v19
	v_pk_add_f32 v[20:21], v[22:23], 1.0 op_sel_hi:[1,0] neg_lo:[1,0] neg_hi:[1,0]
	v_pk_mul_f32 v[22:23], v[38:39], s[94:95] op_sel_hi:[1,0]
	v_perm_b32 v10, v26, v52, s100
	v_pk_mul_f32 v[18:19], v[20:21], v[18:19]
	v_exp_f32_e32 v22, v22
	v_exp_f32_e32 v23, v23
	v_cvt_pk_bf16_f32 v29, v18, v19
	v_pk_fma_f32 v[18:19], v[40:41], s[94:95], v[50:51] op_sel_hi:[1,0,1]
	v_med3_f32 v18, -v18, s20, v207
	v_med3_f32 v19, -v19, s20, v207
	v_exp_f32_e32 v18, v18
	v_exp_f32_e32 v19, v19
	v_pk_add_f32 v[20:21], v[22:23], 1.0 op_sel_hi:[1,0] neg_lo:[1,0] neg_hi:[1,0]
	v_pk_mul_f32 v[22:23], v[42:43], s[94:95] op_sel_hi:[1,0]
	v_perm_b32 v11, v28, v27, s100
	v_exp_f32_e32 v22, v22
	v_exp_f32_e32 v23, v23
	v_pk_mul_f32 v[18:19], v[20:21], v[18:19]
	v_cvt_pk_bf16_f32 v30, v18, v19
	v_pk_fma_f32 v[18:19], v[44:45], s[94:95], v[50:51] op_sel_hi:[1,0,1]
	v_pk_add_f32 v[20:21], v[22:23], 1.0 op_sel_hi:[1,0] neg_lo:[1,0] neg_hi:[1,0]
	v_med3_f32 v18, -v18, s20, v207
	v_med3_f32 v19, -v19, s20, v207
	v_exp_f32_e32 v18, v18
	v_exp_f32_e32 v19, v19
	v_pk_fma_f32 v[22:23], v[48:49], s[94:95], v[50:51] op_sel_hi:[1,0,1]
	v_perm_b32 v12, v30, v29, s100
	v_med3_f32 v22, -v22, s20, v207
	v_med3_f32 v23, -v23, s20, v207
	v_exp_f32_e32 v22, v22
	v_exp_f32_e32 v23, v23
	v_pk_mul_f32 v[18:19], v[20:21], v[18:19]
	v_cvt_pk_bf16_f32 v20, v18, v19
	v_pk_add_f32 v[18:19], v[24:25], 1.0 op_sel_hi:[1,0] neg_lo:[1,0] neg_hi:[1,0]
	v_pk_mul_f32 v[18:19], v[18:19], v[22:23]
	v_cvt_pk_bf16_f32 v18, v18, v19
	v_perm_b32 v13, v18, v20, s100
	v_perm_b32 v14, v26, v52, s101
	v_perm_b32 v15, v28, v27, s101
	v_perm_b32 v16, v30, v29, s101
	v_perm_b32 v17, v18, v20, s101
	ds_write_b128 v161, v[10:13] offset:32768
	ds_write_b128 v161, v[14:17] offset:32832
	v_perm_b32 v10, v55, v54, s100
	v_perm_b32 v11, v57, v56, s100
	v_perm_b32 v12, v59, v58, s100
	s_waitcnt vmcnt(32)
	v_perm_b32 v13, v61, v60, s100
	v_perm_b32 v14, v55, v54, s101
	v_perm_b32 v15, v57, v56, s101
	v_perm_b32 v16, v59, v58, s101
	v_perm_b32 v17, v61, v60, s101
	ds_write_b128 v161, v[10:13] offset:49152
	ds_write_b128 v161, v[14:17] offset:49216
	v_cndmask_b32_e64 v10, 0, 1, s[30:31]
	v_cmp_ne_u32_e64 s[20:21], 1, v10
	s_cbranch_vccnz .LBB0_564
	s_mov_b64 s[38:39], 0

.LBB0_566:
	s_and_b64 s[36:37], s[36:37], exec
	s_cselect_b32 s35, 0xc0, 0
	s_or_b32 s38, s67, s35
	s_add_i32 s35, s38, s66
	v_mad_i64_i32 v[0:1], s[36:37], s35, v205, v[126:127]
	s_mov_b32 s35, s79
	v_lshl_add_u64 v[10:11], v[0:1], 0, s[78:79]
	v_lshl_add_u64 v[0:1], v[0:1], 0, s[34:35]
	s_add_i32 s36, s38, s65
	global_load_dword v103, v[10:11], off
	global_load_dword v171, v[0:1], off offset:3072
	v_mad_i64_i32 v[0:1], s[36:37], s36, v205, v[126:127]
	v_lshl_add_u64 v[10:11], v[0:1], 0, s[78:79]
	v_lshl_add_u64 v[0:1], v[0:1], 0, s[34:35]
	s_add_i32 s36, s38, s64
	global_load_dword v105, v[10:11], off
	global_load_dword v172, v[0:1], off offset:3072
	v_mad_i64_i32 v[0:1], s[36:37], s36, v205, v[126:127]
	v_lshl_add_u64 v[10:11], v[0:1], 0, s[78:79]
	v_lshl_add_u64 v[0:1], v[0:1], 0, s[34:35]
	s_add_i32 s36, s38, s63
	global_load_dword v109, v[10:11], off
	global_load_dword v173, v[0:1], off offset:3072
	v_mad_i64_i32 v[0:1], s[36:37], s36, v205, v[126:127]
	s_waitcnt vmcnt(37)
	v_lshlrev_b32_e32 v80, 16, v5
	v_and_b32_e32 v81, 0xffff0000, v5
	v_lshl_add_u64 v[10:11], v[0:1], 0, s[78:79]
	v_lshl_add_u64 v[0:1], v[0:1], 0, s[34:35]
	s_add_i32 s36, s38, s62
	v_pk_add_f32 v[82:83], v[80:81], 0 op_sel_hi:[1,0]
	s_waitcnt vmcnt(35)
	v_lshlrev_b32_e32 v76, 16, v4
	v_and_b32_e32 v77, 0xffff0000, v4
	global_load_dword v112, v[10:11], off
	global_load_dword v174, v[0:1], off offset:3072
	v_mad_i64_i32 v[0:1], s[36:37], s36, v205, v[126:127]
	v_pk_add_f32 v[78:79], v[82:83], v[76:77]
	s_waitcnt vmcnt(35)
	v_lshlrev_b32_e32 v72, 16, v3
	v_and_b32_e32 v73, 0xffff0000, v3
	v_lshl_add_u64 v[10:11], v[0:1], 0, s[78:79]
	v_lshl_add_u64 v[0:1], v[0:1], 0, s[34:35]
	s_add_i32 s36, s38, s61
	v_pk_add_f32 v[74:75], v[78:79], v[72:73]
	s_waitcnt vmcnt(33)
	v_lshlrev_b32_e32 v68, 16, v2
	v_and_b32_e32 v69, 0xffff0000, v2
	global_load_dword v118, v[10:11], off
	global_load_dword v175, v[0:1], off offset:3072
	v_mad_i64_i32 v[0:1], s[36:37], s36, v205, v[126:127]
	v_pk_add_f32 v[70:71], v[74:75], v[68:69]
	s_waitcnt vmcnt(33)
	v_lshlrev_b32_e32 v62, 16, v9
	v_and_b32_e32 v63, 0xffff0000, v9
	v_lshl_add_u64 v[10:11], v[0:1], 0, s[78:79]
	v_lshl_add_u64 v[0:1], v[0:1], 0, s[34:35]
	s_add_i32 s36, s38, s60
	v_pk_add_f32 v[66:67], v[70:71], v[62:63]
	s_waitcnt vmcnt(31)
	v_lshlrev_b32_e32 v58, 16, v8
	v_and_b32_e32 v59, 0xffff0000, v8
	global_load_dword v119, v[10:11], off
	global_load_dword v176, v[0:1], off offset:3072
	v_mad_i64_i32 v[0:1], s[36:37], s36, v205, v[126:127]
	v_pk_add_f32 v[60:61], v[66:67], v[58:59]
	s_waitcnt vmcnt(31)
	v_lshlrev_b32_e32 v52, 16, v7
	v_and_b32_e32 v53, 0xffff0000, v7
	v_lshl_add_u64 v[10:11], v[0:1], 0, s[78:79]
	v_lshl_add_u64 v[0:1], v[0:1], 0, s[34:35]
	s_add_i32 s38, s38, s59
	v_pk_add_f32 v[56:57], v[60:61], v[52:53]
	s_waitcnt vmcnt(29)
	v_lshlrev_b32_e32 v48, 16, v6
	v_and_b32_e32 v49, 0xffff0000, v6
	global_load_dword v120, v[10:11], off
	global_load_dword v177, v[0:1], off offset:3072
	v_mad_i64_i32 v[0:1], s[36:37], s38, v205, v[126:127]
	v_pk_add_f32 v[50:51], v[56:57], v[48:49]
	v_add_u32_e32 v180, s56, v124
	v_lshl_add_u64 v[10:11], v[0:1], 0, s[78:79]
	v_lshl_add_u64 v[0:1], v[0:1], 0, s[34:35]
	ds_write_b64 v180, v[50:51]
	global_load_dword v121, v[10:11], off
	global_load_dword v178, v[0:1], off offset:3072
	s_waitcnt lgkmcnt(0)
	s_barrier
	v_add_u32_e32 v152, s1, v125
	v_add_u32_e32 v153, s22, v125
	ds_read_b128 v[36:39], v170 offset:32768
	ds_read_b128 v[40:43], v170 offset:33792
	ds_read_b128 v[4:7], v152
	ds_read_b128 v[0:3], v153
	ds_read_b128 v[8:11], v160 offset:49152
	ds_read_b128 v[12:15], v160 offset:50176
	s_waitcnt lgkmcnt(1)
	v_mfma_f32_16x16x32_bf16 v[8:11], v[36:39], v[8:11], 0
	v_add_u32_e32 v179, s23, v124
	v_pk_mul_f32 v[80:81], v[80:81], s[94:95] op_sel_hi:[1,0]
	s_mov_b32 s34, 0x42f00000
	s_waitcnt lgkmcnt(0)
	v_mfma_f32_16x16x32_bf16 v[8:11], v[40:43], v[12:15], v[8:11]
	ds_read_b128 v[12:15], v160 offset:51200
	ds_read_b128 v[16:19], v160 offset:52224
	v_pk_mul_f32 v[76:77], v[76:77], s[94:95] op_sel_hi:[1,0]
	v_pk_mul_f32 v[72:73], v[72:73], s[94:95] op_sel_hi:[1,0]
	s_waitcnt lgkmcnt(1)
	v_mfma_f32_16x16x32_bf16 v[12:15], v[36:39], v[12:15], 0
	v_mul_f32_e64 v68, v68, s94
	v_mul_f32_e64 v69, v69, s94
	v_pk_mul_f32 v[62:63], v[62:63], s[94:95] op_sel_hi:[1,0]
	v_pk_mul_f32 v[58:59], v[58:59], s[94:95] op_sel_hi:[1,0]
	s_waitcnt lgkmcnt(0)
	v_mfma_f32_16x16x32_bf16 v[12:15], v[40:43], v[16:19], v[12:15]
	ds_read_b128 v[16:19], v160 offset:53248
	ds_read_b128 v[20:23], v160 offset:54272
	v_pk_mul_f32 v[52:53], v[52:53], s[94:95] op_sel_hi:[1,0]
	v_exp_f32_e32 v80, v80
	s_waitcnt lgkmcnt(1)
	v_mfma_f32_16x16x32_bf16 v[16:19], v[36:39], v[16:19], 0
	v_exp_f32_e32 v81, v81
	v_exp_f32_e32 v76, v76
	v_exp_f32_e32 v77, v77
	s_waitcnt lgkmcnt(0)
	v_mfma_f32_16x16x32_bf16 v[16:19], v[40:43], v[20:23], v[16:19]
	ds_read_b128 v[20:23], v160 offset:55296
	ds_read_b128 v[24:27], v160 offset:56320
	v_exp_f32_e32 v72, v72
	v_exp_f32_e32 v73, v73
	s_waitcnt lgkmcnt(1)
	v_mfma_f32_16x16x32_bf16 v[20:23], v[36:39], v[20:23], 0
	v_exp_f32_e32 v68, v68
	v_exp_f32_e32 v69, v69
	v_exp_f32_e32 v62, v62
	s_waitcnt lgkmcnt(0)
	v_mfma_f32_16x16x32_bf16 v[20:23], v[40:43], v[24:27], v[20:23]
	ds_read_b128 v[24:27], v160 offset:57344
	ds_read_b128 v[28:31], v160 offset:58368
	v_exp_f32_e32 v63, v63
	v_exp_f32_e32 v58, v58
	s_waitcnt lgkmcnt(1)
	v_mfma_f32_16x16x32_bf16 v[24:27], v[36:39], v[24:27], 0
	v_exp_f32_e32 v59, v59
	v_exp_f32_e32 v52, v52
	v_exp_f32_e32 v53, v53
	s_waitcnt lgkmcnt(0)
	v_mfma_f32_16x16x32_bf16 v[24:27], v[40:43], v[28:31], v[24:27]
	ds_read_b128 v[28:31], v160 offset:59392
	ds_read_b128 v[32:35], v160 offset:60416
	v_pk_mul_f32 v[48:49], v[48:49], s[94:95] op_sel_hi:[1,0]
	v_pk_add_f32 v[80:81], v[80:81], 1.0 op_sel_hi:[1,0] neg_lo:[1,0] neg_hi:[1,0]
	s_waitcnt lgkmcnt(1)
	v_mfma_f32_16x16x32_bf16 v[28:31], v[36:39], v[28:31], 0
	v_exp_f32_e32 v48, v48
	v_exp_f32_e32 v49, v49
	v_pk_add_f32 v[76:77], v[76:77], 1.0 op_sel_hi:[1,0] neg_lo:[1,0] neg_hi:[1,0]
	s_waitcnt lgkmcnt(0)
	v_mfma_f32_16x16x32_bf16 v[28:31], v[40:43], v[32:35], v[28:31]
	ds_read_b128 v[32:35], v160 offset:61440
	ds_read_b128 v[44:47], v160 offset:62464
	v_pk_add_f32 v[72:73], v[72:73], 1.0 op_sel_hi:[1,0] neg_lo:[1,0] neg_hi:[1,0]
	v_pk_add_f32 v[68:69], v[68:69], 1.0 op_sel_hi:[1,0] neg_lo:[1,0] neg_hi:[1,0]
	s_waitcnt lgkmcnt(1)
	v_mfma_f32_16x16x32_bf16 v[32:35], v[36:39], v[32:35], 0
	v_add_f32_e64 v62, -v62, 1.0
	v_add_f32_e64 v63, -v63, 1.0
	v_pk_add_f32 v[58:59], v[58:59], 1.0 op_sel_hi:[1,0] neg_lo:[1,0] neg_hi:[1,0]
	v_pk_add_f32 v[52:53], v[52:53], 1.0 op_sel_hi:[1,0] neg_lo:[1,0] neg_hi:[1,0]
	s_waitcnt lgkmcnt(0)
	v_mfma_f32_16x16x32_bf16 v[32:35], v[40:43], v[44:47], v[32:35]
	ds_read_b128 v[44:47], v160 offset:63488
	ds_read_b128 v[146:149], v160 offset:64512
	v_pk_add_f32 v[48:49], v[48:49], 1.0 op_sel_hi:[1,0] neg_lo:[1,0] neg_hi:[1,0]
	s_and_b64 vcc, exec, s[20:21]
	s_waitcnt lgkmcnt(1)
	v_mfma_f32_16x16x32_bf16 v[36:39], v[36:39], v[44:47], 0
	s_mov_b64 s[68:69], 0x80
	s_waitcnt lgkmcnt(0)
	v_mfma_f32_16x16x32_bf16 v[36:39], v[40:43], v[146:149], v[36:39]
	ds_read2st64_b64 v[40:43], v179 offset1:1
	s_waitcnt lgkmcnt(0)
	v_pk_add_f32 v[40:41], v[40:41], 0 op_sel_hi:[1,0]
	s_nop 0
	v_cndmask_b32_e64 v45, 0, v41, s[4:5]
	v_cndmask_b32_e64 v44, 0, v40, s[4:5]
	v_pk_add_f32 v[46:47], v[42:43], v[44:45]
	s_nop 0
	v_cndmask_b32_e64 v45, v45, v47, s[6:7]
	v_cndmask_b32_e64 v44, v44, v46, s[6:7]
	v_pk_add_f32 v[46:47], v[40:41], v[42:43]
	ds_read2st64_b64 v[40:43], v179 offset0:2 offset1:3
	s_waitcnt lgkmcnt(0)
	v_pk_add_f32 v[54:55], v[40:41], v[44:45]
	s_nop 0
	v_cndmask_b32_e64 v45, v45, v55, s[8:9]
	v_cndmask_b32_e64 v44, v44, v54, s[8:9]
	v_pk_add_f32 v[40:41], v[46:47], v[40:41]
	v_pk_add_f32 v[46:47], v[42:43], v[44:45]
	v_pk_add_f32 v[54:55], v[40:41], v[42:43]
	ds_read2st64_b64 v[40:43], v179 offset0:4 offset1:5
	v_cndmask_b32_e64 v45, v45, v47, s[10:11]
	v_cndmask_b32_e64 v44, v44, v46, s[10:11]
	s_waitcnt lgkmcnt(0)
	v_pk_add_f32 v[46:47], v[40:41], v[44:45]
	s_nop 0
	v_cndmask_b32_e64 v45, v45, v47, s[12:13]
	v_cndmask_b32_e64 v44, v44, v46, s[12:13]
	v_pk_add_f32 v[46:47], v[42:43], v[44:45]
	v_pk_add_f32 v[40:41], v[54:55], v[40:41]
	v_cndmask_b32_e64 v85, v45, v47, s[14:15]
	v_cndmask_b32_e64 v84, v44, v46, s[14:15]
	ds_read2st64_b64 v[44:47], v179 offset0:6 offset1:7
	v_pk_add_f32 v[40:41], v[40:41], v[42:43]
	s_waitcnt lgkmcnt(0)
	v_pk_add_f32 v[146:147], v[44:45], v[84:85]
	s_nop 0
	v_cndmask_b32_e64 v85, v85, v147, s[16:17]
	v_cndmask_b32_e64 v84, v84, v146, s[16:17]
	v_pk_add_f32 v[146:147], v[46:47], v[84:85]
	v_pk_add_f32 v[40:41], v[40:41], v[44:45]
	v_cndmask_b32_e64 v85, v85, v147, s[18:19]
	v_cndmask_b32_e64 v84, v84, v146, s[18:19]
	v_pk_add_f32 v[84:85], v[84:85], v[54:55] neg_lo:[0,1] neg_hi:[0,1]
	v_pk_add_f32 v[146:147], v[40:41], v[46:47]
	v_pk_mul_f32 v[84:85], v[84:85], s[94:95] op_sel_hi:[1,0]
	s_nop 0
	v_pk_fma_f32 v[82:83], v[82:83], s[94:95], v[84:85] op_sel_hi:[1,0,1]
	v_pk_fma_f32 v[78:79], v[78:79], s[94:95], v[84:85] op_sel_hi:[1,0,1]
	v_pk_fma_f32 v[74:75], v[74:75], s[94:95], v[84:85] op_sel_hi:[1,0,1]
	v_pk_fma_f32 v[70:71], v[70:71], s[94:95], v[84:85] op_sel_hi:[1,0,1]
	v_pk_fma_f32 v[66:67], v[66:67], s[94:95], v[84:85] op_sel_hi:[1,0,1]
	v_pk_fma_f32 v[60:61], v[60:61], s[94:95], v[84:85] op_sel_hi:[1,0,1]
	v_pk_fma_f32 v[56:57], v[56:57], s[94:95], v[84:85] op_sel_hi:[1,0,1]
	v_med3_f32 v82, -v82, s34, v207
	v_med3_f32 v83, -v83, s34, v207
	v_med3_f32 v78, -v78, s34, v207
	v_med3_f32 v79, -v79, s34, v207
	v_med3_f32 v74, -v74, s34, v207
	v_med3_f32 v75, -v75, s34, v207
	v_med3_f32 v70, -v70, s34, v207
	v_med3_f32 v71, -v71, s34, v207
	v_med3_f32 v66, -v66, s34, v207
	v_med3_f32 v67, -v67, s34, v207
	v_med3_f32 v60, -v60, s34, v207
	v_med3_f32 v61, -v61, s34, v207
	v_med3_f32 v56, -v56, s34, v207
	v_med3_f32 v57, -v57, s34, v207
	v_pk_fma_f32 v[50:51], v[50:51], s[94:95], v[84:85] op_sel_hi:[1,0,1]
	v_exp_f32_e32 v82, v82
	v_exp_f32_e32 v83, v83
	v_exp_f32_e32 v78, v78
	v_exp_f32_e32 v79, v79
	v_exp_f32_e32 v74, v74
	v_exp_f32_e32 v75, v75
	v_exp_f32_e32 v70, v70
	v_exp_f32_e32 v71, v71
	v_exp_f32_e32 v66, v66
	v_exp_f32_e32 v67, v67
	v_exp_f32_e32 v60, v60
	v_exp_f32_e32 v61, v61
	v_exp_f32_e32 v56, v56
	v_exp_f32_e32 v57, v57
	v_med3_f32 v50, -v50, s34, v207
	v_med3_f32 v51, -v51, s34, v207
	v_exp_f32_e32 v50, v50
	v_exp_f32_e32 v51, v51
	v_pk_mul_f32 v[80:81], v[80:81], v[82:83]
	v_pk_mul_f32 v[76:77], v[76:77], v[78:79]
	v_pk_mul_f32 v[72:73], v[72:73], v[74:75]
	v_pk_mul_f32 v[68:69], v[68:69], v[70:71]
	v_pk_mul_f32 v[62:63], v[62:63], v[66:67]
	v_pk_mul_f32 v[58:59], v[58:59], v[60:61]
	v_pk_mul_f32 v[52:53], v[52:53], v[56:57]
	v_cvt_pk_bf16_f32 v80, v80, v81
	v_cvt_pk_bf16_f32 v76, v76, v77
	v_cvt_pk_bf16_f32 v72, v72, v73
	v_cvt_pk_bf16_f32 v68, v68, v69
	v_cvt_pk_bf16_f32 v62, v62, v63
	v_cvt_pk_bf16_f32 v58, v58, v59
	s_nop 0
	v_cvt_pk_bf16_f32 v52, v52, v53
	v_pk_mul_f32 v[48:49], v[48:49], v[50:51]
	v_cvt_pk_bf16_f32 v48, v48, v49
	v_perm_b32 v40, v76, v80, s100
	v_perm_b32 v41, v68, v72, s100
	v_perm_b32 v42, v58, v62, s100
	v_perm_b32 v43, v48, v52, s100
	v_perm_b32 v44, v76, v80, s101
	v_perm_b32 v45, v68, v72, s101
	v_perm_b32 v46, v58, v62, s101
	v_perm_b32 v47, v48, v52, s101
	ds_write_b128 v161, v[40:43]
	ds_write_b128 v161, v[44:47] offset:64
	v_perm_b32 v40, v107, v90, s100
	v_perm_b32 v41, v110, v108, s100
	v_perm_b32 v42, v114, v113, s100
	s_waitcnt vmcnt(32)
	v_perm_b32 v43, v116, v115, s100
	s_mov_b64 s[34:35], -1
	v_perm_b32 v44, v107, v90, s101
	v_perm_b32 v45, v110, v108, s101
	v_perm_b32 v46, v114, v113, s101
	v_perm_b32 v47, v116, v115, s101
	ds_write_b128 v161, v[40:43] offset:16384
	ds_write_b128 v161, v[44:47] offset:16448
	s_cbranch_vccnz .LBB0_568
	s_mov_b64 s[34:35], 0

.LBB0_570:
	s_waitcnt vmcnt(31)
	v_lshlrev_b32_e32 v158, 16, v89
	v_and_b32_e32 v159, 0xffff0000, v89
	v_pk_add_f32 v[186:187], v[158:159], 0 op_sel_hi:[1,0]
	s_waitcnt vmcnt(29)
	v_lshlrev_b32_e32 v188, 16, v88
	v_and_b32_e32 v189, 0xffff0000, v88
	v_pk_add_f32 v[190:191], v[186:187], v[188:189]
	s_waitcnt vmcnt(27)
	v_lshlrev_b32_e32 v192, 16, v87
	v_and_b32_e32 v193, 0xffff0000, v87
	v_pk_add_f32 v[194:195], v[190:191], v[192:193]
	s_waitcnt vmcnt(25)
	v_lshlrev_b32_e32 v212, 16, v86
	v_and_b32_e32 v213, 0xffff0000, v86
	v_pk_add_f32 v[214:215], v[194:195], v[212:213]
	s_waitcnt vmcnt(23)
	v_lshlrev_b32_e32 v110, 16, v111
	v_and_b32_e32 v111, 0xffff0000, v111
	v_pk_add_f32 v[216:217], v[214:215], v[110:111]
	s_waitcnt vmcnt(21)
	v_lshlrev_b32_e32 v218, 16, v106
	v_and_b32_e32 v219, 0xffff0000, v106
	v_pk_add_f32 v[106:107], v[216:217], v[218:219]
	s_waitcnt vmcnt(19)
	v_lshlrev_b32_e32 v90, 16, v91
	v_and_b32_e32 v91, 0xffff0000, v91
	v_pk_add_f32 v[88:89], v[106:107], v[90:91]
	s_waitcnt vmcnt(17)
	v_lshlrev_b32_e32 v84, 16, v104
	v_and_b32_e32 v85, 0xffff0000, v104
	v_pk_add_f32 v[86:87], v[88:89], v[84:85]
	ds_write_b64 v117, v[86:87]
	s_waitcnt lgkmcnt(0)
	s_barrier
	ds_read_b128 v[60:63], v170
	ds_read_b128 v[78:81], v170 offset:1024
	ds_read_b128 v[40:43], v160 offset:16384
	ds_read_b128 v[44:47], v160 offset:17408
	s_waitcnt lgkmcnt(1)
	v_mfma_f32_16x16x32_bf16 v[40:43], v[60:63], v[40:43], 0
	v_add_u32_e32 v181, s57, v125
	v_add_u32_e32 v182, s0, v125
	s_mov_b32 s34, 0x42f00000
	s_waitcnt lgkmcnt(0)
	v_mfma_f32_16x16x32_bf16 v[66:69], v[78:81], v[44:47], v[40:43]
	s_nop 2
	ds_read_b128 v[40:43], v160 offset:18432
	ds_read_b128 v[44:47], v160 offset:19456
	v_pk_mul_f32 v[110:111], v[110:111], s[94:95] op_sel_hi:[1,0]
	v_pk_mul_f32 v[84:85], v[84:85], s[94:95] op_sel_hi:[1,0]
	s_waitcnt lgkmcnt(1)
	v_mfma_f32_16x16x32_bf16 v[40:43], v[60:63], v[40:43], 0
	v_exp_f32_e32 v110, v110
	v_exp_f32_e32 v111, v111
	v_pk_mul_f32 v[90:91], v[90:91], s[94:95] op_sel_hi:[1,0]
	s_waitcnt lgkmcnt(0)
	v_mfma_f32_16x16x32_bf16 v[40:43], v[78:81], v[44:47], v[40:43]
	ds_read_b128 v[44:47], v160 offset:20480
	ds_read_b128 v[48:51], v160 offset:21504
	v_exp_f32_e32 v84, v84
	v_exp_f32_e32 v85, v85
	s_waitcnt lgkmcnt(1)
	v_mfma_f32_16x16x32_bf16 v[44:47], v[60:63], v[44:47], 0
	v_exp_f32_e32 v90, v90
	v_exp_f32_e32 v91, v91
	v_pk_add_f32 v[110:111], v[110:111], 1.0 op_sel_hi:[1,0] neg_lo:[1,0] neg_hi:[1,0]
	s_waitcnt lgkmcnt(0)
	v_mfma_f32_16x16x32_bf16 v[44:47], v[78:81], v[48:51], v[44:47]
	ds_read_b128 v[48:51], v160 offset:22528
	ds_read_b128 v[52:55], v160 offset:23552
	v_pk_add_f32 v[84:85], v[84:85], 1.0 op_sel_hi:[1,0] neg_lo:[1,0] neg_hi:[1,0]
	v_pk_add_f32 v[90:91], v[90:91], 1.0 op_sel_hi:[1,0] neg_lo:[1,0] neg_hi:[1,0]
	s_waitcnt lgkmcnt(1)
	v_mfma_f32_16x16x32_bf16 v[48:51], v[60:63], v[48:51], 0
	s_and_b64 vcc, exec, s[20:21]
	s_waitcnt lgkmcnt(0)
	v_mfma_f32_16x16x32_bf16 v[48:51], v[78:81], v[52:55], v[48:51]
	ds_read_b128 v[52:55], v160 offset:24576
	ds_read_b128 v[56:59], v160 offset:25600
	s_waitcnt lgkmcnt(1)
	v_mfma_f32_16x16x32_bf16 v[52:55], v[60:63], v[52:55], 0
	s_waitcnt lgkmcnt(0)
	v_mfma_f32_16x16x32_bf16 v[52:55], v[78:81], v[56:59], v[52:55]
	ds_read_b128 v[56:59], v160 offset:26624
	ds_read_b128 v[70:73], v160 offset:27648
	s_waitcnt lgkmcnt(1)
	v_mfma_f32_16x16x32_bf16 v[56:59], v[60:63], v[56:59], 0
	s_waitcnt lgkmcnt(0)
	v_mfma_f32_16x16x32_bf16 v[56:59], v[78:81], v[70:73], v[56:59]
	ds_read_b128 v[70:73], v160 offset:28672
	ds_read_b128 v[74:77], v160 offset:29696
	ds_read_b128 v[114:117], v160 offset:30720
	ds_read_b128 v[148:151], v160 offset:31744
	s_waitcnt lgkmcnt(3)
	v_mfma_f32_16x16x32_bf16 v[70:73], v[60:63], v[70:73], 0
	s_waitcnt lgkmcnt(1)
	v_mfma_f32_16x16x32_bf16 v[114:117], v[60:63], v[114:117], 0
	v_mfma_f32_16x16x32_bf16 v[70:73], v[78:81], v[74:77], v[70:73]
	ds_read2st64_b64 v[154:157], v100 offset1:1
	ds_read_b128 v[60:63], v181
	ds_read_b128 v[74:77], v182
	s_waitcnt lgkmcnt(2)
	v_pk_add_f32 v[82:83], v[154:155], 0 op_sel_hi:[1,0]
	v_mfma_f32_16x16x32_bf16 v[78:81], v[78:81], v[148:151], v[114:117]
	v_cndmask_b32_e64 v149, 0, v83, s[4:5]
	v_cndmask_b32_e64 v148, 0, v82, s[4:5]
	v_pk_add_f32 v[150:151], v[156:157], v[148:149]
	ds_read2st64_b64 v[114:117], v100 offset0:2 offset1:3
	v_cndmask_b32_e64 v149, v149, v151, s[6:7]
	v_cndmask_b32_e64 v148, v148, v150, s[6:7]
	v_pk_add_f32 v[82:83], v[82:83], v[156:157]
	s_waitcnt lgkmcnt(0)
	v_pk_add_f32 v[150:151], v[114:115], v[148:149]
	s_nop 0
	v_cndmask_b32_e64 v155, v149, v151, s[8:9]
	v_cndmask_b32_e64 v154, v148, v150, s[8:9]
	ds_read2st64_b64 v[148:151], v100 offset0:4 offset1:5
	v_pk_add_f32 v[82:83], v[82:83], v[114:115]
	v_pk_add_f32 v[114:115], v[116:117], v[154:155]
	v_pk_add_f32 v[82:83], v[82:83], v[116:117]
	v_cndmask_b32_e64 v155, v155, v115, s[10:11]
	v_cndmask_b32_e64 v154, v154, v114, s[10:11]
	ds_read2st64_b64 v[114:117], v100 offset0:6 offset1:7
	s_waitcnt lgkmcnt(1)
	v_pk_add_f32 v[156:157], v[148:149], v[154:155]
	s_nop 0
	v_cndmask_b32_e64 v155, v155, v157, s[12:13]
	v_cndmask_b32_e64 v154, v154, v156, s[12:13]
	v_pk_add_f32 v[156:157], v[150:151], v[154:155]
	s_nop 0
	v_cndmask_b32_e64 v155, v155, v157, s[14:15]
	v_cndmask_b32_e64 v154, v154, v156, s[14:15]
	s_waitcnt lgkmcnt(0)
	v_pk_add_f32 v[156:157], v[114:115], v[154:155]
	s_nop 0
	v_cndmask_b32_e64 v155, v155, v157, s[16:17]
	v_cndmask_b32_e64 v154, v154, v156, s[16:17]
	v_pk_add_f32 v[156:157], v[116:117], v[154:155]
	s_nop 0
	v_cndmask_b32_e64 v155, v155, v157, s[18:19]
	v_cndmask_b32_e64 v154, v154, v156, s[18:19]
	v_pk_add_f32 v[154:155], v[154:155], v[82:83] neg_lo:[0,1] neg_hi:[0,1]
	v_pk_mul_f32 v[156:157], v[158:159], s[94:95] op_sel_hi:[1,0]
	v_pk_mul_f32 v[154:155], v[154:155], s[94:95] op_sel_hi:[1,0]
	v_exp_f32_e32 v156, v156
	v_pk_fma_f32 v[158:159], v[186:187], s[94:95], v[154:155] op_sel_hi:[1,0,1]
	v_exp_f32_e32 v157, v157
	v_med3_f32 v100, -v158, s34, v207
	v_exp_f32_e32 v158, v100
	v_med3_f32 v100, -v159, s34, v207
	v_exp_f32_e32 v159, v100
	v_pk_add_f32 v[156:157], v[156:157], 1.0 op_sel_hi:[1,0] neg_lo:[1,0] neg_hi:[1,0]
	v_pk_mul_f32 v[186:187], v[188:189], s[94:95] op_sel_hi:[1,0]
	v_pk_fma_f32 v[106:107], v[106:107], s[94:95], v[154:155] op_sel_hi:[1,0,1]
	v_pk_mul_f32 v[156:157], v[156:157], v[158:159]
	v_exp_f32_e32 v186, v186
	v_cvt_pk_bf16_f32 v100, v156, v157
	v_pk_fma_f32 v[156:157], v[190:191], s[94:95], v[154:155] op_sel_hi:[1,0,1]
	v_exp_f32_e32 v187, v187
	v_med3_f32 v104, -v156, s34, v207
	v_exp_f32_e32 v156, v104
	v_med3_f32 v104, -v157, s34, v207
	v_exp_f32_e32 v157, v104
	v_pk_add_f32 v[158:159], v[186:187], 1.0 op_sel_hi:[1,0] neg_lo:[1,0] neg_hi:[1,0]
	v_pk_mul_f32 v[186:187], v[192:193], s[94:95] op_sel_hi:[1,0]
	v_pk_fma_f32 v[86:87], v[86:87], s[94:95], v[154:155] op_sel_hi:[1,0,1]
	v_pk_mul_f32 v[156:157], v[158:159], v[156:157]
	v_exp_f32_e32 v186, v186
	v_cvt_pk_bf16_f32 v104, v156, v157
	v_pk_fma_f32 v[156:157], v[194:195], s[94:95], v[154:155] op_sel_hi:[1,0,1]
	v_exp_f32_e32 v187, v187
	v_med3_f32 v108, -v156, s34, v207
	v_exp_f32_e32 v156, v108
	v_med3_f32 v108, -v157, s34, v207
	v_exp_f32_e32 v157, v108
	v_pk_add_f32 v[158:159], v[186:187], 1.0 op_sel_hi:[1,0] neg_lo:[1,0] neg_hi:[1,0]
	v_pk_mul_f32 v[186:187], v[212:213], s[94:95] op_sel_hi:[1,0]
	v_med3_f32 v106, -v106, s34, v207
	v_pk_mul_f32 v[156:157], v[158:159], v[156:157]
	v_exp_f32_e32 v186, v186
	v_cvt_pk_bf16_f32 v108, v156, v157
	v_pk_fma_f32 v[156:157], v[214:215], s[94:95], v[154:155] op_sel_hi:[1,0,1]
	v_exp_f32_e32 v187, v187
	v_med3_f32 v113, -v156, s34, v207
	v_exp_f32_e32 v156, v113
	v_med3_f32 v113, -v157, s34, v207
	v_exp_f32_e32 v157, v113
	v_pk_add_f32 v[158:159], v[186:187], 1.0 op_sel_hi:[1,0] neg_lo:[1,0] neg_hi:[1,0]
	v_med3_f32 v107, -v107, s34, v207
	v_pk_fma_f32 v[88:89], v[88:89], s[94:95], v[154:155] op_sel_hi:[1,0,1]
	v_pk_mul_f32 v[156:157], v[158:159], v[156:157]
	v_pk_mul_f32 v[158:159], v[218:219], s[94:95] op_sel_hi:[1,0]
	v_cvt_pk_bf16_f32 v113, v156, v157
	v_pk_fma_f32 v[156:157], v[216:217], s[94:95], v[154:155] op_sel_hi:[1,0,1]
	v_exp_f32_e32 v158, v158
	v_med3_f32 v156, -v156, s34, v207
	v_med3_f32 v157, -v157, s34, v207
	v_exp_f32_e32 v156, v156
	v_exp_f32_e32 v157, v157
	v_exp_f32_e32 v159, v159
	v_med3_f32 v86, -v86, s34, v207
	v_med3_f32 v87, -v87, s34, v207
	v_exp_f32_e32 v106, v106
	v_exp_f32_e32 v107, v107
	v_med3_f32 v88, -v88, s34, v207
	v_med3_f32 v89, -v89, s34, v207
	v_exp_f32_e32 v86, v86
	v_exp_f32_e32 v87, v87
	v_exp_f32_e32 v88, v88
	v_exp_f32_e32 v89, v89
	v_pk_mul_f32 v[110:111], v[110:111], v[156:157]
	v_pk_mul_f32 v[84:85], v[84:85], v[86:87]
	v_cvt_pk_bf16_f32 v156, v110, v111
	v_pk_add_f32 v[110:111], v[158:159], 1.0 op_sel_hi:[1,0] neg_lo:[1,0] neg_hi:[1,0]
	v_pk_mul_f32 v[88:89], v[90:91], v[88:89]
	v_pk_mul_f32 v[106:107], v[110:111], v[106:107]
	v_cvt_pk_bf16_f32 v106, v106, v107
	v_cvt_pk_bf16_f32 v91, v88, v89
	v_cvt_pk_bf16_f32 v107, v84, v85
	v_pk_add_f32 v[84:85], v[82:83], v[148:149]
	v_pk_add_f32 v[84:85], v[84:85], v[150:151]
	v_perm_b32 v86, v106, v156, s100
	v_pk_add_f32 v[84:85], v[84:85], v[114:115]
	v_perm_b32 v87, v107, v91, s100
	v_pk_add_f32 v[148:149], v[84:85], v[116:117]
	v_perm_b32 v84, v104, v100, s100
	v_perm_b32 v85, v113, v108, s100
	v_perm_b32 v88, v104, v100, s101
	v_perm_b32 v89, v113, v108, s101
	v_perm_b32 v90, v106, v156, s101
	v_perm_b32 v91, v107, v91, s101
	ds_write_b128 v161, v[84:87] offset:32768
	ds_write_b128 v161, v[88:91] offset:32832
	v_perm_b32 v84, v93, v92, s100
	v_perm_b32 v85, v95, v94, s100
	v_perm_b32 v86, v97, v96, s100
	s_waitcnt vmcnt(16)
	v_perm_b32 v87, v99, v98, s100
	s_mov_b64 s[34:35], -1
	v_perm_b32 v88, v93, v92, s101
	v_perm_b32 v89, v95, v94, s101
	v_perm_b32 v90, v97, v96, s101
	v_perm_b32 v91, v99, v98, s101
	ds_write_b128 v161, v[84:87] offset:49152
	ds_write_b128 v161, v[88:91] offset:49216
	s_cbranch_vccnz .LBB0_572
	s_mov_b64 s[34:35], 0

.LBB0_574:
	s_waitcnt vmcnt(15)
	v_lshlrev_b32_e32 v194, 16, v103
	v_and_b32_e32 v195, 0xffff0000, v103
	v_pk_add_f32 v[216:217], v[194:195], 0 op_sel_hi:[1,0]
	s_waitcnt vmcnt(13)
	v_lshlrev_b32_e32 v218, 16, v105
	v_and_b32_e32 v219, 0xffff0000, v105
	v_pk_add_f32 v[220:221], v[216:217], v[218:219]
	s_waitcnt vmcnt(11)
	v_lshlrev_b32_e32 v222, 16, v109
	v_and_b32_e32 v223, 0xffff0000, v109
	v_pk_add_f32 v[224:225], v[220:221], v[222:223]
	s_waitcnt vmcnt(9)
	v_lshlrev_b32_e32 v226, 16, v112
	v_and_b32_e32 v227, 0xffff0000, v112
	v_pk_add_f32 v[228:229], v[224:225], v[226:227]
	s_waitcnt vmcnt(7)
	v_lshlrev_b32_e32 v230, 16, v118
	v_and_b32_e32 v231, 0xffff0000, v118
	v_pk_add_f32 v[232:233], v[228:229], v[230:231]
	s_waitcnt vmcnt(5)
	v_lshlrev_b32_e32 v234, 16, v119
	v_and_b32_e32 v235, 0xffff0000, v119
	v_pk_add_f32 v[236:237], v[232:233], v[234:235]
	s_waitcnt vmcnt(3)
	v_lshlrev_b32_e32 v158, 16, v120
	v_and_b32_e32 v159, 0xffff0000, v120
	v_pk_add_f32 v[156:157], v[236:237], v[158:159]
	s_waitcnt vmcnt(1)
	v_lshlrev_b32_e32 v150, 16, v121
	v_and_b32_e32 v151, 0xffff0000, v121
	v_pk_add_f32 v[154:155], v[156:157], v[150:151]
	ds_write_b64 v180, v[154:155]
	s_waitcnt lgkmcnt(0)
	s_barrier
	ds_read_b128 v[82:85], v170 offset:32768
	ds_read_b128 v[90:93], v170 offset:33792
	ds_read_b128 v[86:89], v160 offset:49152
	ds_read_b128 v[94:97], v160 offset:50176
	s_waitcnt lgkmcnt(1)
	v_mfma_f32_16x16x32_bf16 v[86:89], v[82:85], v[86:89], 0
	s_mov_b32 s34, 0x42f00000
	v_pk_mul_f32 v[194:195], v[194:195], s[94:95] op_sel_hi:[1,0]
	v_pk_mul_f32 v[150:151], v[150:151], s[94:95] op_sel_hi:[1,0]
	s_waitcnt lgkmcnt(0)
	v_mfma_f32_16x16x32_bf16 v[118:121], v[90:93], v[94:97], v[86:89]
	s_nop 2
	ds_read_b128 v[86:89], v160 offset:51200
	ds_read_b128 v[94:97], v160 offset:52224
	v_exp_f32_e32 v194, v194
	v_exp_f32_e32 v195, v195
	s_waitcnt lgkmcnt(1)
	v_mfma_f32_16x16x32_bf16 v[86:89], v[82:85], v[86:89], 0
	v_mul_f32_e64 v158, v158, s94
	v_mul_f32_e64 v159, v159, s94
	v_pk_add_f32 v[194:195], v[194:195], 1.0 op_sel_hi:[1,0] neg_lo:[1,0] neg_hi:[1,0]
	v_exp_f32_e32 v150, v150
	s_waitcnt lgkmcnt(0)
	v_mfma_f32_16x16x32_bf16 v[94:97], v[90:93], v[94:97], v[86:89]
	s_nop 2
	ds_read_b128 v[86:89], v160 offset:53248
	ds_read_b128 v[98:101], v160 offset:54272
	v_exp_f32_e32 v151, v151
	v_exp_f32_e32 v158, v158
	s_waitcnt lgkmcnt(1)
	v_mfma_f32_16x16x32_bf16 v[86:89], v[82:85], v[86:89], 0
	v_exp_f32_e32 v159, v159
	v_pk_add_f32 v[150:151], v[150:151], 1.0 op_sel_hi:[1,0] neg_lo:[1,0] neg_hi:[1,0]
	s_and_b64 vcc, exec, s[20:21]
	s_waitcnt lgkmcnt(0)
	v_mfma_f32_16x16x32_bf16 v[98:101], v[90:93], v[98:101], v[86:89]
	s_nop 2
	ds_read_b128 v[86:89], v160 offset:55296
	ds_read_b128 v[102:105], v160 offset:56320
	v_pk_add_f32 v[158:159], v[158:159], 1.0 op_sel_hi:[1,0] neg_lo:[1,0] neg_hi:[1,0]
	s_mov_b64 s[20:21], -1
	s_waitcnt lgkmcnt(1)
	v_mfma_f32_16x16x32_bf16 v[86:89], v[82:85], v[86:89], 0
	s_waitcnt lgkmcnt(0)
	v_mfma_f32_16x16x32_bf16 v[102:105], v[90:93], v[102:105], v[86:89]
	s_nop 5
	ds_read_b128 v[86:89], v160 offset:57344
	ds_read_b128 v[106:109], v160 offset:58368
	s_waitcnt lgkmcnt(1)
	v_mfma_f32_16x16x32_bf16 v[86:89], v[82:85], v[86:89], 0
	s_waitcnt lgkmcnt(0)
	v_mfma_f32_16x16x32_bf16 v[106:109], v[90:93], v[106:109], v[86:89]
	s_nop 5
	ds_read_b128 v[86:89], v160 offset:59392
	ds_read_b128 v[110:113], v160 offset:60416
	s_waitcnt lgkmcnt(1)
	v_mfma_f32_16x16x32_bf16 v[86:89], v[82:85], v[86:89], 0
	s_waitcnt lgkmcnt(0)
	v_mfma_f32_16x16x32_bf16 v[110:113], v[90:93], v[110:113], v[86:89]
	s_nop 5
	ds_read_b128 v[86:89], v160 offset:61440
	ds_read_b128 v[114:117], v160 offset:62464
	s_waitcnt lgkmcnt(1)
	v_mfma_f32_16x16x32_bf16 v[86:89], v[82:85], v[86:89], 0
	s_waitcnt lgkmcnt(0)
	v_mfma_f32_16x16x32_bf16 v[114:117], v[90:93], v[114:117], v[86:89]
	s_nop 5
	ds_read_b128 v[86:89], v160 offset:63488
	ds_read_b128 v[186:189], v160 offset:64512
	s_waitcnt lgkmcnt(1)
	v_mfma_f32_16x16x32_bf16 v[190:193], v[82:85], v[86:89], 0
	ds_read2st64_b64 v[212:215], v179 offset1:1
	ds_read_b128 v[82:85], v152
	ds_read_b128 v[86:89], v153
	s_waitcnt lgkmcnt(2)
	v_pk_add_f32 v[152:153], v[212:213], 0 op_sel_hi:[1,0]
	v_mfma_f32_16x16x32_bf16 v[90:93], v[90:93], v[186:189], v[190:193]
	ds_read2st64_b64 v[186:189], v179 offset0:2 offset1:3
	s_nop 1
	v_cndmask_b32_e64 v191, 0, v153, s[4:5]
	v_cndmask_b32_e64 v190, 0, v152, s[4:5]
	v_pk_add_f32 v[192:193], v[214:215], v[190:191]
	v_pk_add_f32 v[152:153], v[152:153], v[214:215]
	v_cndmask_b32_e64 v191, v191, v193, s[6:7]
	v_cndmask_b32_e64 v190, v190, v192, s[6:7]
	s_waitcnt lgkmcnt(0)
	v_pk_add_f32 v[192:193], v[186:187], v[190:191]
	v_pk_add_f32 v[152:153], v[152:153], v[186:187]
	v_cndmask_b32_e64 v213, v191, v193, s[8:9]
	v_cndmask_b32_e64 v212, v190, v192, s[8:9]
	ds_read2st64_b64 v[190:193], v179 offset0:4 offset1:5
	v_pk_add_f32 v[186:187], v[188:189], v[212:213]
	v_pk_add_f32 v[152:153], v[152:153], v[188:189]
	v_cndmask_b32_e64 v213, v213, v187, s[10:11]
	v_cndmask_b32_e64 v212, v212, v186, s[10:11]
	ds_read2st64_b64 v[186:189], v179 offset0:6 offset1:7
	s_waitcnt lgkmcnt(1)
	v_pk_add_f32 v[214:215], v[190:191], v[212:213]
	s_nop 0
	v_cndmask_b32_e64 v213, v213, v215, s[12:13]
	v_cndmask_b32_e64 v212, v212, v214, s[12:13]
	v_pk_add_f32 v[214:215], v[192:193], v[212:213]
	s_nop 0
	v_cndmask_b32_e64 v213, v213, v215, s[14:15]
	v_cndmask_b32_e64 v212, v212, v214, s[14:15]
	s_waitcnt lgkmcnt(0)
	v_pk_add_f32 v[214:215], v[186:187], v[212:213]
	s_nop 0
	v_cndmask_b32_e64 v213, v213, v215, s[16:17]
	v_cndmask_b32_e64 v212, v212, v214, s[16:17]
	v_pk_add_f32 v[214:215], v[188:189], v[212:213]
	s_nop 0
	v_cndmask_b32_e64 v213, v213, v215, s[18:19]
	v_cndmask_b32_e64 v212, v212, v214, s[18:19]
	v_pk_add_f32 v[212:213], v[212:213], v[152:153] neg_lo:[0,1] neg_hi:[0,1]
	s_nop 0
	v_pk_mul_f32 v[212:213], v[212:213], s[94:95] op_sel_hi:[1,0]
	s_nop 0
	v_pk_fma_f32 v[214:215], v[216:217], s[94:95], v[212:213] op_sel_hi:[1,0,1]
	v_pk_mul_f32 v[216:217], v[218:219], s[94:95] op_sel_hi:[1,0]
	v_med3_f32 v179, -v214, s34, v207
	v_exp_f32_e32 v214, v179
	v_med3_f32 v179, -v215, s34, v207
	v_exp_f32_e32 v215, v179
	v_exp_f32_e32 v216, v216
	v_exp_f32_e32 v217, v217
	v_pk_fma_f32 v[154:155], v[154:155], s[94:95], v[212:213] op_sel_hi:[1,0,1]
	v_pk_mul_f32 v[194:195], v[194:195], v[214:215]
	v_pk_fma_f32 v[156:157], v[156:157], s[94:95], v[212:213] op_sel_hi:[1,0,1]
	v_cvt_pk_bf16_f32 v179, v194, v195
	v_pk_fma_f32 v[194:195], v[220:221], s[94:95], v[212:213] op_sel_hi:[1,0,1]
	v_pk_add_f32 v[214:215], v[216:217], 1.0 op_sel_hi:[1,0] neg_lo:[1,0] neg_hi:[1,0]
	v_med3_f32 v180, -v194, s34, v207
	v_exp_f32_e32 v194, v180
	v_med3_f32 v180, -v195, s34, v207
	v_exp_f32_e32 v195, v180
	v_pk_mul_f32 v[216:217], v[222:223], s[94:95] op_sel_hi:[1,0]
	v_med3_f32 v154, -v154, s34, v207
	v_exp_f32_e32 v216, v216
	v_pk_mul_f32 v[194:195], v[214:215], v[194:195]
	v_exp_f32_e32 v217, v217
	v_cvt_pk_bf16_f32 v180, v194, v195
	v_pk_fma_f32 v[194:195], v[224:225], s[94:95], v[212:213] op_sel_hi:[1,0,1]
	v_med3_f32 v155, -v155, s34, v207
	v_med3_f32 v185, -v194, s34, v207
	v_exp_f32_e32 v194, v185
	v_med3_f32 v185, -v195, s34, v207
	v_exp_f32_e32 v195, v185
	v_pk_add_f32 v[214:215], v[216:217], 1.0 op_sel_hi:[1,0] neg_lo:[1,0] neg_hi:[1,0]
	v_pk_mul_f32 v[216:217], v[226:227], s[94:95] op_sel_hi:[1,0]
	v_med3_f32 v156, -v156, s34, v207
	v_pk_mul_f32 v[194:195], v[214:215], v[194:195]
	v_exp_f32_e32 v216, v216
	v_cvt_pk_bf16_f32 v185, v194, v195
	v_pk_fma_f32 v[194:195], v[228:229], s[94:95], v[212:213] op_sel_hi:[1,0,1]
	v_exp_f32_e32 v217, v217
	v_med3_f32 v194, -v194, s34, v207
	v_med3_f32 v195, -v195, s34, v207
	v_exp_f32_e32 v194, v194
	v_exp_f32_e32 v195, v195
	v_pk_add_f32 v[214:215], v[216:217], 1.0 op_sel_hi:[1,0] neg_lo:[1,0] neg_hi:[1,0]
	v_pk_mul_f32 v[216:217], v[230:231], s[94:95] op_sel_hi:[1,0]
	v_med3_f32 v157, -v157, s34, v207
	v_pk_mul_f32 v[194:195], v[214:215], v[194:195]
	v_exp_f32_e32 v216, v216
	v_cvt_pk_bf16_f32 v211, v194, v195
	v_pk_fma_f32 v[194:195], v[232:233], s[94:95], v[212:213] op_sel_hi:[1,0,1]
	v_exp_f32_e32 v217, v217
	v_med3_f32 v194, -v194, s34, v207
	v_med3_f32 v195, -v195, s34, v207
	v_exp_f32_e32 v194, v194
	v_exp_f32_e32 v195, v195
	v_pk_add_f32 v[214:215], v[216:217], 1.0 op_sel_hi:[1,0] neg_lo:[1,0] neg_hi:[1,0]
	v_pk_mul_f32 v[216:217], v[234:235], s[94:95] op_sel_hi:[1,0]
	v_exp_f32_e32 v154, v154
	v_pk_mul_f32 v[194:195], v[214:215], v[194:195]
	v_exp_f32_e32 v216, v216
	v_cvt_pk_bf16_f32 v218, v194, v195
	v_pk_fma_f32 v[194:195], v[236:237], s[94:95], v[212:213] op_sel_hi:[1,0,1]
	v_exp_f32_e32 v217, v217
	v_med3_f32 v194, -v194, s34, v207
	v_med3_f32 v195, -v195, s34, v207
	v_exp_f32_e32 v194, v194
	v_exp_f32_e32 v195, v195
	v_exp_f32_e32 v155, v155
	v_exp_f32_e32 v156, v156
	v_exp_f32_e32 v157, v157
	v_pk_add_f32 v[214:215], v[216:217], 1.0 op_sel_hi:[1,0] neg_lo:[1,0] neg_hi:[1,0]
	v_pk_mul_f32 v[150:151], v[150:151], v[154:155]
	v_pk_mul_f32 v[194:195], v[214:215], v[194:195]
	v_pk_mul_f32 v[156:157], v[158:159], v[156:157]
	v_cvt_pk_bf16_f32 v194, v194, v195
	v_and_b32_e32 v154, 0xffff, v179
	v_cvt_pk_bf16_f32 v158, v156, v157
	v_cvt_pk_bf16_f32 v159, v150, v151
	v_pk_add_f32 v[150:151], v[152:153], v[190:191]
	v_lshrrev_b32_e32 v179, 16, v179
	v_pk_add_f32 v[150:151], v[150:151], v[192:193]
	v_pk_add_f32 v[150:151], v[150:151], v[186:187]
	v_and_or_b32 v186, v180, s95, v179
	v_lshrrev_b32_e32 v179, 16, v185
	v_lshl_or_b32 v154, v180, 16, v154
	v_perm_b32 v155, v211, v185, s100
	v_perm_b32 v156, v194, v218, s100
	v_perm_b32 v157, v159, v158, s100
	v_and_or_b32 v187, v211, s95, v179
	v_lshrrev_b32_e32 v179, 16, v218
	v_lshrrev_b32_e32 v158, 16, v158
	v_pk_add_f32 v[150:151], v[150:151], v[188:189]
	v_and_or_b32 v188, v194, s95, v179
	v_and_or_b32 v189, v159, s95, v158
	ds_write_b128 v161, v[154:157]
	ds_write_b128 v161, v[186:189] offset:64
	v_lshrrev_b32_e32 v158, 16, v171
	v_perm_b32 v154, v172, v171, s100
	v_and_or_b32 v172, v172, s95, v158
	v_lshrrev_b32_e32 v158, 16, v173
	v_and_b32_e32 v155, 0xffff, v173
	v_and_or_b32 v173, v174, s95, v158
	v_lshrrev_b32_e32 v158, 16, v175
	v_lshl_or_b32 v155, v174, 16, v155
	v_perm_b32 v156, v176, v175, s100
	s_waitcnt vmcnt(0)
	v_perm_b32 v157, v178, v177, s100
	v_and_or_b32 v174, v176, s95, v158
	v_lshrrev_b32_e32 v158, 16, v177
	v_and_or_b32 v175, v178, s95, v158
	ds_write_b128 v161, v[154:157] offset:16384
	ds_write_b128 v161, v[172:175] offset:16448
	s_cbranch_vccnz .LBB0_576
	s_mov_b64 s[20:21], 0

.LBB0_693:
	s_or_b64 exec, exec, s[4:5]
	s_mov_b32 s0, s86
	s_waitcnt lgkmcnt(0)
	s_waitcnt vmcnt(0)
	s_barrier
	s_mov_b32 s100, 0x05040100
	s_mov_b32 s101, 0x07060302
	v_mbcnt_lo_u32_b32 v0, -1, 0
	v_mbcnt_hi_u32_b32 v0, -1, v0
	s_mov_b32 s60, s79
	v_lshl_add_u32 v0, s0, 6, v0
	s_mov_b32 s0, s79
	s_add_i32 s0, s0, 0x25f98
	v_mov_b32_e32 v1, s0
	ds_read_b64 v[2:3], v1
	s_mov_b32 s2, s79
	s_add_i32 s2, s2, 0x25f60
	v_mov_b32_e32 v1, s2
	s_waitcnt lgkmcnt(0)
	v_readfirstlane_b32 s0, v2
	v_readfirstlane_b32 s1, v3
	ds_read_b64 v[2:3], v1
	s_mov_b32 s4, s79
	s_add_i32 s4, s4, 0x25f58
	v_mov_b32_e32 v1, s4
	s_waitcnt lgkmcnt(0)
	v_readfirstlane_b32 s2, v2
	v_readfirstlane_b32 s3, v3
	ds_read_b64 v[2:3], v1
	v_readfirstlane_b32 s70, v0
	s_ashr_i32 s18, s70, 6
	s_cmp_gt_i32 s18, 3
	s_cselect_b64 s[4:5], -1, 0
	s_waitcnt lgkmcnt(0)
	v_readfirstlane_b32 s6, v2
	v_readfirstlane_b32 s7, v3
	s_cmp_lt_i32 s18, 4
	s_cbranch_scc1 .LBB0_695
	s_setprio 1

.LBB0_704:
	s_waitcnt vmcnt(23)
	v_lshlrev_b32_e32 v8, 16, v140
	v_mov_b32_e32 v85, v146
	v_mul_f32_e32 v8, v183, v8
	v_and_b32_e32 v9, 0xffff0000, v140
	v_mul_f32_e32 v9, v183, v9
	v_cvt_pk_bf16_f32 v12, v8, v9
	v_add_u32_e32 v8, s60, v148
	s_waitcnt vmcnt(21)
	ds_write2st64_b32 v8, v142, v140 offset1:64
	s_waitcnt vmcnt(20)
	v_lshlrev_b32_e32 v8, 16, v143
	v_mul_f32_e32 v8, v184, v8
	v_and_b32_e32 v9, 0xffff0000, v143
	v_mul_f32_e32 v9, v184, v9
	v_cvt_pk_bf16_f32 v13, v8, v9
	s_waitcnt vmcnt(17)
	v_lshlrev_b32_e32 v8, 16, v166
	v_mul_f32_e32 v8, v185, v8
	v_and_b32_e32 v9, 0xffff0000, v166
	ds_write2st64_b32 v159, v145, v143 offset1:64
	v_mul_f32_e32 v9, v185, v9
	v_cvt_pk_bf16_f32 v14, v8, v9
	s_waitcnt vmcnt(14)
	v_lshlrev_b32_e32 v8, 16, v169
	v_mul_f32_e32 v8, v186, v8
	v_and_b32_e32 v9, 0xffff0000, v169
	ds_write2st64_b32 v160, v168, v166 offset1:64
	v_mul_f32_e32 v9, v186, v9
	v_cvt_pk_bf16_f32 v15, v8, v9
	s_waitcnt vmcnt(11)
	v_lshlrev_b32_e32 v8, 16, v172
	v_mul_f32_e32 v8, v187, v8
	v_and_b32_e32 v9, 0xffff0000, v172
	ds_write2st64_b32 v161, v171, v169 offset1:64
	v_mul_f32_e32 v9, v187, v9
	v_cvt_pk_bf16_f32 v16, v8, v9
	s_waitcnt vmcnt(8)
	v_lshlrev_b32_e32 v8, 16, v175
	v_mul_f32_e32 v8, v188, v8
	v_and_b32_e32 v9, 0xffff0000, v175
	ds_write2st64_b32 v162, v174, v172 offset1:64
	v_mul_f32_e32 v9, v188, v9
	v_cvt_pk_bf16_f32 v17, v8, v9
	s_waitcnt vmcnt(5)
	v_lshlrev_b32_e32 v8, 16, v178
	v_mul_f32_e32 v8, v189, v8
	v_and_b32_e32 v9, 0xffff0000, v178
	ds_write2st64_b32 v163, v177, v175 offset1:64
	v_mul_f32_e32 v9, v189, v9
	v_cvt_pk_bf16_f32 v18, v8, v9
	s_waitcnt vmcnt(2)
	v_lshlrev_b32_e32 v8, 16, v181
	v_mul_f32_e32 v8, v190, v8
	v_and_b32_e32 v9, 0xffff0000, v181
	ds_write2st64_b32 v164, v180, v178 offset1:64
	v_mul_f32_e32 v9, v190, v9
	v_cvt_pk_bf16_f32 v19, v8, v9
	v_and_b32_e32 v8, 0xffff, v12
	v_lshl_or_b32 v8, v13, 16, v8
	v_perm_b32 v12, v13, v12, s101
	v_perm_b32 v9, v15, v14, s100
	v_perm_b32 v13, v15, v14, s101
	v_perm_b32 v10, v17, v16, s100
	v_perm_b32 v11, v19, v18, s100
	v_perm_b32 v14, v17, v16, s101
	v_perm_b32 v15, v19, v18, s101
	v_add_u32_e32 v16, v158, v157
	s_add_i32 s56, s83, -1
	s_waitcnt vmcnt(0)
	ds_write2st64_b32 v165, v191, v181 offset1:64
	ds_write_b128 v16, v[8:11] offset:32768
	ds_write_b128 v16, v[12:15] offset:32832
	v_perm_b32 v8, v144, v141, s100
	v_perm_b32 v9, v170, v167, s100
	v_perm_b32 v10, v176, v173, s100
	v_perm_b32 v11, v182, v179, s100
	v_perm_b32 v12, v144, v141, s101
	v_perm_b32 v13, v170, v167, s101
	v_perm_b32 v14, v176, v173, s101
	v_perm_b32 v15, v182, v179, s101
	s_cmp_gt_u32 s56, 6
	ds_write_b128 v16, v[8:11] offset:49152
	ds_write_b128 v16, v[12:15] offset:49216
	s_cbranch_scc1 .LBB0_706
	s_and_b64 vcc, s[20:21], exec
	s_cselect_b32 s51, s83, s42
	s_lshl_b32 s51, s51, 6
	s_add_i32 s57, s51, s74
	s_add_i32 s51, s57, s77
	v_mad_i64_i32 v[8:9], vcc, s51, v205, v[66:67]
	v_lshl_add_u64 v[10:11], v[8:9], 0, s[78:79]
	s_mov_b32 s51, s79
	s_mov_b32 s53, s79
	global_load_dword v140, v[10:11], off
	v_lshl_add_u64 v[10:11], v[8:9], 0, s[50:51]
	v_lshl_add_u64 v[8:9], v[8:9], 0, s[52:53]
	s_add_i32 vcc_lo, s57, s88
	global_load_dword v141, v[10:11], off
	global_load_dword v142, v[8:9], off
	v_mad_i64_i32 v[8:9], vcc, vcc_lo, v205, v[66:67]
	v_lshl_add_u64 v[10:11], v[8:9], 0, s[78:79]
	global_load_dword v143, v[10:11], off
	v_lshl_add_u64 v[10:11], v[8:9], 0, s[50:51]
	v_lshl_add_u64 v[8:9], v[8:9], 0, s[52:53]
	s_add_i32 vcc_lo, s57, s85
	global_load_dword v144, v[10:11], off
	global_load_dword v145, v[8:9], off
	v_mad_i64_i32 v[8:9], vcc, vcc_lo, v205, v[66:67]
	v_lshl_add_u64 v[10:11], v[8:9], 0, s[78:79]
	global_load_dword v166, v[10:11], off
	v_lshl_add_u64 v[10:11], v[8:9], 0, s[50:51]
	v_lshl_add_u64 v[8:9], v[8:9], 0, s[52:53]
	s_add_i32 vcc_lo, s57, s92
	global_load_dword v167, v[10:11], off
	global_load_dword v168, v[8:9], off
	v_mad_i64_i32 v[8:9], vcc, vcc_lo, v205, v[66:67]
	v_lshl_add_u64 v[10:11], v[8:9], 0, s[78:79]
	global_load_dword v169, v[10:11], off
	v_lshl_add_u64 v[10:11], v[8:9], 0, s[50:51]
	v_lshl_add_u64 v[8:9], v[8:9], 0, s[52:53]
	s_add_i32 vcc_lo, s57, s89
	global_load_dword v170, v[10:11], off
	global_load_dword v171, v[8:9], off
	v_mad_i64_i32 v[8:9], vcc, vcc_lo, v205, v[66:67]
	v_lshl_add_u64 v[10:11], v[8:9], 0, s[78:79]
	global_load_dword v172, v[10:11], off
	v_lshl_add_u64 v[10:11], v[8:9], 0, s[50:51]
	v_lshl_add_u64 v[8:9], v[8:9], 0, s[52:53]
	s_add_i32 vcc_lo, s57, s96
	global_load_dword v173, v[10:11], off
	global_load_dword v174, v[8:9], off
	v_mad_i64_i32 v[8:9], vcc, vcc_lo, v205, v[66:67]
	v_lshl_add_u64 v[10:11], v[8:9], 0, s[78:79]
	global_load_dword v175, v[10:11], off
	v_lshl_add_u64 v[10:11], v[8:9], 0, s[50:51]
	v_lshl_add_u64 v[8:9], v[8:9], 0, s[52:53]
	s_add_i32 vcc_lo, s57, s93
	global_load_dword v176, v[10:11], off
	global_load_dword v177, v[8:9], off
	v_mad_i64_i32 v[8:9], vcc, vcc_lo, v205, v[66:67]
	v_lshl_add_u64 v[10:11], v[8:9], 0, s[78:79]
	global_load_dword v178, v[10:11], off
	v_lshl_add_u64 v[10:11], v[8:9], 0, s[50:51]
	v_lshl_add_u64 v[8:9], v[8:9], 0, s[52:53]
	s_add_i32 s57, s57, s58
	global_load_dword v179, v[10:11], off
	global_load_dword v180, v[8:9], off
	v_mad_i64_i32 v[8:9], vcc, s57, v205, v[66:67]
	v_lshl_add_u64 v[10:11], v[8:9], 0, s[78:79]
	global_load_dword v181, v[10:11], off
	v_lshl_add_u64 v[10:11], v[8:9], 0, s[50:51]
	v_lshl_add_u64 v[8:9], v[8:9], 0, s[52:53]
	global_load_dword v182, v[10:11], off
	global_load_dword v191, v[8:9], off

.LBB0_730:
	s_waitcnt vmcnt(23)
	v_lshlrev_b32_e32 v32, 16, v166
	v_and_b32_e32 v33, 0xffff0000, v166
	v_pk_add_f32 v[34:35], v[32:33], 0 op_sel_hi:[1,0]
	s_waitcnt vmcnt(20)
	v_lshlrev_b32_e32 v36, 16, v169
	v_and_b32_e32 v37, 0xffff0000, v169
	v_pk_add_f32 v[38:39], v[34:35], v[36:37]
	s_waitcnt vmcnt(17)
	v_lshlrev_b32_e32 v40, 16, v172
	v_and_b32_e32 v41, 0xffff0000, v172
	v_pk_add_f32 v[42:43], v[38:39], v[40:41]
	s_waitcnt vmcnt(14)
	v_lshlrev_b32_e32 v44, 16, v175
	v_and_b32_e32 v45, 0xffff0000, v175
	v_pk_add_f32 v[46:47], v[42:43], v[44:45]
	s_waitcnt vmcnt(11)
	v_lshlrev_b32_e32 v48, 16, v178
	v_and_b32_e32 v49, 0xffff0000, v178
	v_pk_add_f32 v[50:51], v[46:47], v[48:49]
	s_waitcnt vmcnt(8)
	v_lshlrev_b32_e32 v26, 16, v181
	v_and_b32_e32 v27, 0xffff0000, v181
	v_pk_add_f32 v[28:29], v[50:51], v[26:27]
	s_waitcnt vmcnt(5)
	v_lshlrev_b32_e32 v22, 16, v184
	v_and_b32_e32 v23, 0xffff0000, v184
	v_pk_add_f32 v[24:25], v[28:29], v[22:23]
	s_waitcnt vmcnt(2)
	v_lshlrev_b32_e32 v18, 16, v187
	v_and_b32_e32 v19, 0xffff0000, v187
	v_mov_b32_e32 v190, v146
	v_pk_add_f32 v[20:21], v[24:25], v[18:19]
	v_add_u32_e32 v8, s80, v156
	ds_write_b64 v8, v[20:21]
	s_waitcnt lgkmcnt(0)
	s_barrier
	v_add_u32_e32 v52, s26, v156
	ds_read2st64_b64 v[8:11], v52 offset1:1
	ds_read2st64_b64 v[12:15], v52 offset0:2 offset1:3
	v_pk_mul_f32 v[32:33], v[32:33], s[94:95] op_sel_hi:[1,0]
	v_pk_mul_f32 v[26:27], v[26:27], s[94:95] op_sel_hi:[1,0]
	v_exp_f32_e32 v32, v32
	s_waitcnt lgkmcnt(1)
	v_pk_add_f32 v[8:9], v[8:9], 0 op_sel_hi:[1,0]
	v_exp_f32_e32 v33, v33
	v_cndmask_b32_e64 v17, 0, v9, s[6:7]
	v_cndmask_b32_e64 v16, 0, v8, s[6:7]
	v_pk_add_f32 v[30:31], v[10:11], v[16:17]
	v_pk_add_f32 v[8:9], v[8:9], v[10:11]
	v_cndmask_b32_e64 v17, v17, v31, s[8:9]
	v_cndmask_b32_e64 v16, v16, v30, s[8:9]
	s_waitcnt lgkmcnt(0)
	v_pk_add_f32 v[10:11], v[12:13], v[16:17]
	v_pk_add_f32 v[12:13], v[8:9], v[12:13]
	v_cndmask_b32_e64 v17, v17, v11, s[10:11]
	v_cndmask_b32_e64 v16, v16, v10, s[10:11]
	ds_read2st64_b64 v[8:11], v52 offset0:4 offset1:5
	v_pk_add_f32 v[30:31], v[14:15], v[16:17]
	v_pk_add_f32 v[32:33], v[32:33], 1.0 op_sel_hi:[1,0] neg_lo:[1,0] neg_hi:[1,0]
	v_cndmask_b32_e64 v31, v17, v31, s[4:5]
	v_cndmask_b32_e64 v30, v16, v30, s[4:5]
	v_pk_add_f32 v[16:17], v[12:13], v[14:15]
	ds_read2st64_b64 v[12:15], v52 offset0:6 offset1:7
	s_waitcnt lgkmcnt(1)
	v_pk_add_f32 v[52:53], v[8:9], v[30:31]
	v_exp_f32_e32 v26, v26
	v_cndmask_b32_e64 v31, v31, v53, s[12:13]
	v_cndmask_b32_e64 v30, v30, v52, s[12:13]
	v_pk_add_f32 v[52:53], v[10:11], v[30:31]
	v_exp_f32_e32 v27, v27
	v_cndmask_b32_e64 v31, v31, v53, s[14:15]
	v_cndmask_b32_e64 v30, v30, v52, s[14:15]
	s_waitcnt lgkmcnt(0)
	v_pk_add_f32 v[52:53], v[12:13], v[30:31]
	v_pk_add_f32 v[26:27], v[26:27], 1.0 op_sel_hi:[1,0] neg_lo:[1,0] neg_hi:[1,0]
	v_cndmask_b32_e64 v31, v31, v53, s[16:17]
	v_cndmask_b32_e64 v30, v30, v52, s[16:17]
	v_pk_add_f32 v[52:53], v[14:15], v[30:31]
	v_pk_mul_f32 v[22:23], v[22:23], s[94:95] op_sel_hi:[1,0]
	v_cndmask_b32_e64 v31, v31, v53, s[18:19]
	v_cndmask_b32_e64 v30, v30, v52, s[18:19]
	v_pk_add_f32 v[30:31], v[30:31], v[16:17] neg_lo:[0,1] neg_hi:[0,1]
	v_exp_f32_e32 v22, v22
	v_pk_mul_f32 v[30:31], v[30:31], s[94:95] op_sel_hi:[1,0]
	v_exp_f32_e32 v23, v23
	v_pk_fma_f32 v[34:35], v[34:35], s[94:95], v[30:31] op_sel_hi:[1,0,1]
	v_pk_fma_f32 v[28:29], v[28:29], s[94:95], v[30:31] op_sel_hi:[1,0,1]
	v_med3_f32 v52, v35, s81, v206
	v_med3_f32 v53, v34, s81, v206
	v_exp_f32_e64 v34, -v53
	v_exp_f32_e64 v35, -v52
	v_pk_fma_f32 v[24:25], v[24:25], s[94:95], v[30:31] op_sel_hi:[1,0,1]
	v_pk_add_f32 v[22:23], v[22:23], 1.0 op_sel_hi:[1,0] neg_lo:[1,0] neg_hi:[1,0]
	v_pk_fma_f32 v[20:21], v[20:21], s[94:95], v[30:31] op_sel_hi:[1,0,1]
	v_pk_mul_f32 v[32:33], v[32:33], v[34:35]
	v_exp_f32_e32 v34, v53
	v_exp_f32_e32 v35, v52
	v_cvt_pk_bf16_f32 v52, v32, v33
	v_lshlrev_b32_e32 v32, 16, v168
	v_and_b32_e32 v33, 0xffff0000, v168
	v_pk_mul_f32 v[32:33], v[34:35], v[32:33]
	v_pk_mul_f32 v[18:19], v[18:19], s[94:95] op_sel_hi:[1,0]
	v_cvt_pk_bf16_f32 v53, v32, v33
	v_pk_fma_f32 v[32:33], v[38:39], s[94:95], v[30:31] op_sel_hi:[1,0,1]
	v_exp_f32_e32 v18, v18
	v_med3_f32 v38, v33, s81, v206
	v_med3_f32 v39, v32, s81, v206
	v_pk_mul_f32 v[32:33], v[36:37], s[94:95] op_sel_hi:[1,0]
	v_exp_f32_e64 v34, -v39
	v_exp_f32_e32 v32, v32
	v_exp_f32_e32 v33, v33
	v_exp_f32_e64 v35, -v38
	v_add_u32_e32 v36, s60, v148
	ds_write2st64_b32 v36, v53, v52 offset1:64
	v_pk_add_f32 v[32:33], v[32:33], 1.0 op_sel_hi:[1,0] neg_lo:[1,0] neg_hi:[1,0]
	v_exp_f32_e32 v19, v19
	v_pk_mul_f32 v[32:33], v[32:33], v[34:35]
	v_exp_f32_e32 v34, v39
	v_exp_f32_e32 v35, v38
	v_cvt_pk_bf16_f32 v37, v32, v33
	v_lshlrev_b32_e32 v32, 16, v171
	v_and_b32_e32 v33, 0xffff0000, v171
	v_pk_mul_f32 v[32:33], v[34:35], v[32:33]
	v_pk_add_f32 v[18:19], v[18:19], 1.0 op_sel_hi:[1,0] neg_lo:[1,0] neg_hi:[1,0]
	v_cvt_pk_bf16_f32 v38, v32, v33
	v_pk_fma_f32 v[32:33], v[42:43], s[94:95], v[30:31] op_sel_hi:[1,0,1]
	v_add_u32_e32 v43, 0x80, v36
	v_med3_f32 v39, v33, s81, v206
	v_med3_f32 v42, v32, s81, v206
	v_pk_mul_f32 v[32:33], v[40:41], s[94:95] op_sel_hi:[1,0]
	v_exp_f32_e64 v34, -v42
	v_exp_f32_e32 v32, v32
	v_exp_f32_e32 v33, v33
	v_exp_f32_e64 v35, -v39
	v_add_u32_e32 v40, 64, v36
	ds_write2st64_b32 v40, v38, v37 offset1:64
	v_pk_add_f32 v[32:33], v[32:33], 1.0 op_sel_hi:[1,0] neg_lo:[1,0] neg_hi:[1,0]
	s_andn2_b64 vcc, exec, s[36:37]
	v_pk_mul_f32 v[32:33], v[32:33], v[34:35]
	v_exp_f32_e32 v34, v42
	v_exp_f32_e32 v35, v39
	v_cvt_pk_bf16_f32 v38, v32, v33
	v_lshlrev_b32_e32 v32, 16, v174
	v_and_b32_e32 v33, 0xffff0000, v174
	v_pk_mul_f32 v[32:33], v[34:35], v[32:33]
	s_nop 0
	v_cvt_pk_bf16_f32 v39, v32, v33
	v_pk_fma_f32 v[32:33], v[46:47], s[94:95], v[30:31] op_sel_hi:[1,0,1]
	ds_write2st64_b32 v43, v39, v38 offset1:64
	v_med3_f32 v41, v33, s81, v206
	v_med3_f32 v42, v32, s81, v206
	v_pk_mul_f32 v[32:33], v[44:45], s[94:95] op_sel_hi:[1,0]
	v_exp_f32_e64 v34, -v42
	v_exp_f32_e32 v32, v32
	v_exp_f32_e32 v33, v33
	v_exp_f32_e64 v35, -v41
	v_add_u32_e32 v45, 0xc0, v36
	v_pk_add_f32 v[32:33], v[32:33], 1.0 op_sel_hi:[1,0] neg_lo:[1,0] neg_hi:[1,0]
	s_nop 0
	v_pk_mul_f32 v[32:33], v[32:33], v[34:35]
	v_exp_f32_e32 v34, v42
	v_exp_f32_e32 v35, v41
	v_cvt_pk_bf16_f32 v39, v32, v33
	v_lshlrev_b32_e32 v32, 16, v177
	v_and_b32_e32 v33, 0xffff0000, v177
	v_pk_mul_f32 v[32:33], v[34:35], v[32:33]
	s_nop 0
	v_cvt_pk_bf16_f32 v41, v32, v33
	v_pk_fma_f32 v[32:33], v[50:51], s[94:95], v[30:31] op_sel_hi:[1,0,1]
	ds_write2st64_b32 v45, v41, v39 offset1:64
	v_med3_f32 v42, v33, s81, v206
	v_med3_f32 v44, v32, s81, v206
	v_pk_mul_f32 v[32:33], v[48:49], s[94:95] op_sel_hi:[1,0]
	v_exp_f32_e64 v34, -v44
	v_exp_f32_e32 v32, v32
	v_exp_f32_e32 v33, v33
	v_exp_f32_e64 v35, -v42
	v_pk_add_f32 v[32:33], v[32:33], 1.0 op_sel_hi:[1,0] neg_lo:[1,0] neg_hi:[1,0]
	s_nop 0
	v_pk_mul_f32 v[32:33], v[32:33], v[34:35]
	v_exp_f32_e32 v34, v44
	v_exp_f32_e32 v35, v42
	v_cvt_pk_bf16_f32 v41, v32, v33
	v_lshlrev_b32_e32 v32, 16, v180
	v_and_b32_e32 v33, 0xffff0000, v180
	v_pk_mul_f32 v[32:33], v[34:35], v[32:33]
	v_med3_f32 v34, v29, s81, v206
	v_med3_f32 v35, v28, s81, v206
	v_exp_f32_e64 v28, -v35
	v_exp_f32_e64 v29, -v34
	v_cvt_pk_bf16_f32 v32, v32, v33
	ds_write2st64_b32 v36, v32, v41 offset0:1 offset1:65
	v_pk_mul_f32 v[26:27], v[26:27], v[28:29]
	v_exp_f32_e32 v28, v35
	v_exp_f32_e32 v29, v34
	v_cvt_pk_bf16_f32 v32, v26, v27
	v_lshlrev_b32_e32 v26, 16, v183
	v_and_b32_e32 v27, 0xffff0000, v183
	v_pk_mul_f32 v[26:27], v[28:29], v[26:27]
	v_med3_f32 v28, v25, s81, v206
	v_med3_f32 v29, v24, s81, v206
	v_exp_f32_e64 v24, -v29
	v_exp_f32_e64 v25, -v28
	v_cvt_pk_bf16_f32 v26, v26, v27
	ds_write2st64_b32 v40, v26, v32 offset0:1 offset1:65
	v_pk_mul_f32 v[22:23], v[22:23], v[24:25]
	v_exp_f32_e32 v24, v29
	v_exp_f32_e32 v25, v28
	v_cvt_pk_bf16_f32 v26, v22, v23
	v_lshlrev_b32_e32 v22, 16, v186
	v_and_b32_e32 v23, 0xffff0000, v186
	v_pk_mul_f32 v[22:23], v[24:25], v[22:23]
	v_med3_f32 v24, v21, s81, v206
	v_med3_f32 v25, v20, s81, v206
	v_exp_f32_e64 v20, -v25
	v_exp_f32_e64 v21, -v24
	v_cvt_pk_bf16_f32 v22, v22, v23
	ds_write2st64_b32 v43, v22, v26 offset0:1 offset1:65
	v_pk_mul_f32 v[18:19], v[18:19], v[20:21]
	v_exp_f32_e32 v20, v25
	v_exp_f32_e32 v21, v24
	v_cvt_pk_bf16_f32 v25, v18, v19
	s_waitcnt vmcnt(0)
	v_lshlrev_b32_e32 v18, 16, v189
	v_and_b32_e32 v19, 0xffff0000, v189
	v_pk_mul_f32 v[18:19], v[20:21], v[18:19]
	v_cvt_pk_bf16_f32 v18, v18, v19
	ds_write2st64_b32 v45, v18, v25 offset0:1 offset1:65
	v_and_b32_e32 v21, 0xffff, v26
	v_lshrrev_b32_e32 v26, 16, v26
	v_perm_b32 v18, v37, v52, s100
	v_perm_b32 v19, v39, v38, s100
	v_perm_b32 v20, v32, v41, s100
	v_lshl_or_b32 v21, v25, 16, v21
	v_perm_b32 v22, v37, v52, s101
	v_perm_b32 v23, v39, v38, s101
	v_perm_b32 v24, v32, v41, s101
	v_and_or_b32 v25, v25, s95, v26
	v_add_u32_e32 v26, v158, v157
	ds_write_b128 v26, v[18:21] offset:32768
	ds_write_b128 v26, v[22:25] offset:32832
	v_perm_b32 v18, v170, v167, s100
	v_perm_b32 v19, v176, v173, s100
	v_perm_b32 v20, v182, v179, s100
	v_perm_b32 v21, v188, v185, s100
	v_perm_b32 v22, v170, v167, s101
	v_perm_b32 v23, v176, v173, s101
	v_perm_b32 v24, v182, v179, s101
	v_perm_b32 v25, v188, v185, s101
	ds_write_b128 v26, v[18:21] offset:49152
	ds_write_b128 v26, v[22:25] offset:49216
	s_cbranch_vccnz .LBB0_732
	v_pk_add_f32 v[8:9], v[16:17], v[8:9]
	s_nop 0
	v_pk_add_f32 v[8:9], v[8:9], v[10:11]
	s_nop 0
	v_pk_add_f32 v[8:9], v[8:9], v[12:13]
	v_add_u32_e32 v12, s27, v156
	v_pk_add_f32 v[8:9], v[8:9], v[14:15]
	s_nop 0
	v_mul_f32_e32 v10, 0x3fb8aa3b, v8
	v_mul_f32_e32 v11, 0x3fb8aa3b, v9
	v_exp_f32_e32 v10, v10
	v_exp_f32_e32 v11, v11
	v_pk_add_f32 v[8:9], v[8:9], v[16:17] neg_lo:[0,1] neg_hi:[0,1]
	ds_write_b64 v12, v[10:11]
	v_mul_f32_e32 v8, 0x3fb8aa3b, v8
	v_mul_f32_e32 v9, 0x3fb8aa3b, v9
	v_exp_f32_e32 v8, v8
	v_exp_f32_e32 v9, v9
	v_mul_f32_e32 v10, 0x3fb8aa3b, v16
	v_mul_f32_e32 v11, 0x3fb8aa3b, v17
	v_exp_f32_e32 v10, v10
	v_exp_f32_e32 v11, v11
	v_add_u32_e32 v12, s33, v156
	ds_write_b64 v12, v[8:9]
	v_add_u32_e32 v8, s67, v156
	ds_write_b64 v8, v[10:11]
